# PEER down maths on the matrix cores: per row 8 exact fp8->bf16 pair conversions + four block-diagonal 4x4x4 bf16 MFMAs (f32 accumulate) instead of f32 conversions + packed FMAs; hand-written reduce-sc
# speedup vs baseline: 1.0345x; 1.0068x over previous
; DI int tidx() { int t = threadIdx.x & 255; asm volatile("" : "+v"(t)); return t; }
; DI int ftid() { int t = threadIdx.x; asm volatile("" : "+v"(t)); return t; }
; #define PD_E(t, E) do { const char* eb_ = eiu + (size_t)(t) * 512; _Pragma("unroll") for (int q = 0; q < 4; ++q) E[q] = *(const i32x4_t*)(eb_ + (eio + 16u * q)); } while (0)
; #define PD_H(t, H) do { const char* hb_ = h2u + (size_t)(t) * 2048; H[0] = *(const u32x4*)(hb_ + h2o); H[1] = *(const u32x4*)(hb_ + (h2o + 16u)); } while (0)
; #define PD_TAB(E, W) do { _Pragma("unroll") for (int q = 0; q < 16; ++q) W[q] = *(const u32x4*)(tabu + ((unsigned)E[q >> 2][q & 3] * 128u + tabo)); } while (0)
; DI void phase_peerdown(const Params& p, int bid, int nb) {
;   const int lane = tidx() & 63, wid = __builtin_amdgcn_readfirstlane(ftid() >> 6), e8 = lane >> 3, c = lane & 7;
;   const int x = bid & 7, gw = (bid >> 3) * 8 + wid, nw = (nb >> 3) * 8;
;   const char* h2u = p.ws + WS_H + 256 * x; const unsigned h2o = 32u * c;
;   const char* tabu = p.ws + WS_PU + (size_t)x * 16384 * 128; const unsigned tabo = 16u * c;
;   const char* eiu = p.ws + WS_EIDX; const unsigned eio = 64u * e8;
;   char* pdu = p.ws + WS_PD + (size_t)x * T_ * 256; const unsigned pdo = 32u * e8 + 4u * c;
;   const bool c0 = (lane & 1) != 0, c1 = (lane & 2) != 0, c2 = (lane & 4) != 0;
;     ...
;   i32x4_t eA[4], eB[4]; u32x4 hA[2], hB[2], wA[16], wB[16];
;   int t = gw; if (t >= T_) return;
;   int t1 = t + nw;
;   PD_E(t, eA); PD_H(t, hA); PD_TAB(eA, wA);
;   if (t1 < T_) { PD_E(t1, eB); PD_H(t1, hB); }
.LBB0_1735:
	s_or_b64 exec, exec, s[0:1]
	v_mov_b32_e32 v116, v206
	s_waitcnt lgkmcnt(0)
	v_mov_b32_e32 v0, v207
	s_barrier
	v_readlane_b32 s2, v250, 0
	v_readfirstlane_b32 s0, v0
	s_ashr_i32 s0, s0, 6
	s_and_b32 s19, s2, 7
	s_and_b32 s49, s2, -8
	s_add_i32 s12, s0, s49
	s_and_b32 s18, s86, -8
	s_lshl_b32 s48, s19, 21
	s_add_u32 s16, s84, 0x12000000
	s_addc_u32 s17, s85, 0
	s_cmpk_gt_i32 s12, 0x7fff
	v_readlane_b32 s3, v250, 1
	s_cbranch_scc1 .LBB0_1753
	s_lshl_b32 s0, s19, 8
	s_add_u32 s8, s56, s0
	s_addc_u32 s9, s57, 0
	s_add_u32 s0, s84, s48
	s_addc_u32 s1, s85, 0
	s_add_u32 s6, s0, 0xe000000
	s_addc_u32 s7, s1, 0
	v_bfe_u32 v117, v116, 3, 3
	v_and_b32_e32 v118, 7, v116
	v_lshlrev_b32_e32 v209, 4, v118
	v_lshlrev_b32_e32 v112, 6, v117
	v_lshlrev_b32_e32 v114, 5, v118
	v_mov_b32_e32 v113, 0
	v_mov_b32_e32 v115, 0
	v_lshl_add_u64 v[180:181], s[16:17], 0, v[112:113]
	v_lshl_add_u64 v[182:183], s[8:9], 0, v[114:115]
	s_lshl_b32 s0, s19, 23
	s_add_u32 s10, s84, s0
	s_addc_u32 s11, s85, 0
	s_add_u32 s10, s10, 0x14000000
	s_addc_u32 s11, s11, 0
	v_lshlrev_b32_e32 v118, 2, v118
	v_lshl_or_b32 v118, v117, 5, v118
	v_mov_b32_e32 v119, 0
	v_lshl_add_u64 v[178:179], s[10:11], 0, v[118:119]
	v_and_b32_e32 v117, 1, v116
	v_cmp_eq_u32_e64 s[0:1], 0, v117
	v_and_b32_e32 v117, 2, v116
	v_cmp_eq_u32_e64 s[2:3], 0, v117
	v_and_b32_e32 v117, 4, v116
	v_cmp_eq_u32_e64 s[4:5], 0, v117
	v_and_b32_e32 v117, 3, v116
	v_cmp_eq_u32_e64 s[22:23], 1, v117
	v_cmp_eq_u32_e64 s[24:25], 2, v117
	v_cmp_eq_u32_e64 s[26:27], 3, v117
	s_mov_b32 s21, 0
	s_add_u32 s20, s12, 0x0
	s_lshl_b32 s20, s20, 9
	v_lshl_add_u64 v[0:1], v[180:181], 0, s[20:21]
	global_load_dwordx4 v[12:15], v[0:1], off offset:48
	global_load_dwordx4 v[8:11], v[0:1], off offset:32
	global_load_dwordx4 v[4:7], v[0:1], off offset:16
	s_nop 0
	global_load_dwordx4 v[0:3], v[0:1], off
	s_add_u32 s20, s12, 0x100
	s_lshl_b32 s20, s20, 9
	v_lshl_add_u64 v[80:81], v[180:181], 0, s[20:21]
	global_load_dwordx4 v[64:67], v[80:81], off offset:48
	global_load_dwordx4 v[68:71], v[80:81], off offset:32
	global_load_dwordx4 v[72:75], v[80:81], off offset:16
	s_nop 0
	global_load_dwordx4 v[80:83], v[80:81], off
	s_add_u32 s20, s12, 0x0
	s_lshl_b32 s20, s20, 11
	v_lshl_add_u64 v[20:21], v[182:183], 0, s[20:21]
	global_load_dwordx4 v[16:19], v[20:21], off offset:16
	s_nop 0
	global_load_dwordx4 v[20:23], v[20:21], off
	s_add_u32 s20, s12, 0x100
	s_lshl_b32 s20, s20, 11
	v_lshl_add_u64 v[108:109], v[182:183], 0, s[20:21]
	global_load_dwordx4 v[100:103], v[108:109], off offset:16
	s_nop 0
	global_load_dwordx4 v[108:111], v[108:109], off
	s_waitcnt vmcnt(8)
	v_lshl_or_b32 v0, v0, 7, v209
	global_load_dwordx4 v[24:27], v0, s[6:7]
	v_lshl_or_b32 v1, v1, 7, v209
	global_load_dwordx4 v[28:31], v1, s[6:7]
	v_lshl_or_b32 v2, v2, 7, v209
	global_load_dwordx4 v[32:35], v2, s[6:7]
	v_lshl_or_b32 v3, v3, 7, v209
	global_load_dwordx4 v[36:39], v3, s[6:7]
	v_lshl_or_b32 v4, v4, 7, v209
	global_load_dwordx4 v[40:43], v4, s[6:7]
	v_lshl_or_b32 v5, v5, 7, v209
	global_load_dwordx4 v[44:47], v5, s[6:7]
	v_lshl_or_b32 v6, v6, 7, v209
	global_load_dwordx4 v[48:51], v6, s[6:7]
	v_lshl_or_b32 v7, v7, 7, v209
	global_load_dwordx4 v[52:55], v7, s[6:7]
	v_lshl_or_b32 v8, v8, 7, v209
	global_load_dwordx4 v[56:59], v8, s[6:7]
	v_lshl_or_b32 v9, v9, 7, v209
	global_load_dwordx4 v[60:63], v9, s[6:7]
	v_lshl_or_b32 v10, v10, 7, v209
	global_load_dwordx4 v[76:79], v10, s[6:7]
	v_lshl_or_b32 v11, v11, 7, v209
	global_load_dwordx4 v[84:87], v11, s[6:7]
	v_lshl_or_b32 v12, v12, 7, v209
	global_load_dwordx4 v[88:91], v12, s[6:7]
	v_lshl_or_b32 v13, v13, 7, v209
	global_load_dwordx4 v[92:95], v13, s[6:7]
	v_lshl_or_b32 v14, v14, 7, v209
	global_load_dwordx4 v[96:99], v14, s[6:7]
	v_lshl_or_b32 v15, v15, 7, v209
	global_load_dwordx4 v[104:107], v15, s[6:7]
	s_add_u32 s20, s12, 0x200
	s_lshl_b32 s20, s20, 9
	v_lshl_add_u64 v[0:1], v[180:181], 0, s[20:21]
	global_load_dwordx4 v[12:15], v[0:1], off offset:48
	global_load_dwordx4 v[8:11], v[0:1], off offset:32
	global_load_dwordx4 v[4:7], v[0:1], off offset:16
	s_nop 0
	global_load_dwordx4 v[0:3], v[0:1], off
	s_waitcnt vmcnt(24)
	v_lshl_or_b32 v80, v80, 7, v209
	global_load_dwordx4 v[112:115], v80, s[6:7]
	v_lshl_or_b32 v81, v81, 7, v209
	global_load_dwordx4 v[116:119], v81, s[6:7]
	v_lshl_or_b32 v82, v82, 7, v209
	global_load_dwordx4 v[120:123], v82, s[6:7]
	v_lshl_or_b32 v83, v83, 7, v209
	global_load_dwordx4 v[124:127], v83, s[6:7]
	v_lshl_or_b32 v72, v72, 7, v209
	global_load_dwordx4 v[128:131], v72, s[6:7]
	v_lshl_or_b32 v73, v73, 7, v209
	global_load_dwordx4 v[132:135], v73, s[6:7]
	v_lshl_or_b32 v74, v74, 7, v209
	global_load_dwordx4 v[136:139], v74, s[6:7]
	v_lshl_or_b32 v75, v75, 7, v209
	global_load_dwordx4 v[140:143], v75, s[6:7]
	v_lshl_or_b32 v68, v68, 7, v209
	global_load_dwordx4 v[144:147], v68, s[6:7]
	v_lshl_or_b32 v69, v69, 7, v209
	global_load_dwordx4 v[148:151], v69, s[6:7]
	v_lshl_or_b32 v70, v70, 7, v209
	global_load_dwordx4 v[152:155], v70, s[6:7]
	v_lshl_or_b32 v71, v71, 7, v209
	global_load_dwordx4 v[156:159], v71, s[6:7]
	v_lshl_or_b32 v64, v64, 7, v209
	global_load_dwordx4 v[160:163], v64, s[6:7]
	v_lshl_or_b32 v65, v65, 7, v209
	global_load_dwordx4 v[164:167], v65, s[6:7]
	v_lshl_or_b32 v66, v66, 7, v209
	global_load_dwordx4 v[168:171], v66, s[6:7]
	v_lshl_or_b32 v67, v67, 7, v209
	global_load_dwordx4 v[172:175], v67, s[6:7]
	s_add_u32 s20, s12, 0x300
	s_lshl_b32 s20, s20, 9
	v_lshl_add_u64 v[80:81], v[180:181], 0, s[20:21]
	global_load_dwordx4 v[64:67], v[80:81], off offset:48
	global_load_dwordx4 v[68:71], v[80:81], off offset:32
	global_load_dwordx4 v[72:75], v[80:81], off offset:16
	s_nop 0
	global_load_dwordx4 v[80:83], v[80:81], off
	s_mov_b32 s14, s12
	s_waitcnt vmcnt(20)
	v_cvt_scalef32_pk_bf16_fp8 v210, v24, 1.0
	v_cvt_scalef32_pk_bf16_fp8 v211, v24, 1.0 op_sel:[1,0,0]
	v_cvt_scalef32_pk_bf16_fp8 v212, v25, 1.0
	v_cvt_scalef32_pk_bf16_fp8 v213, v25, 1.0 op_sel:[1,0,0]
	v_mfma_f32_4x4x4_16b_bf16 v[228:231], v[210:211], v[20:21], 0
	v_cvt_scalef32_pk_bf16_fp8 v214, v26, 1.0
	v_cvt_scalef32_pk_bf16_fp8 v215, v26, 1.0 op_sel:[1,0,0]
	v_mfma_f32_4x4x4_16b_bf16 v[228:231], v[212:213], v[22:23], v[228:231]
	v_cvt_scalef32_pk_bf16_fp8 v216, v27, 1.0
	v_cvt_scalef32_pk_bf16_fp8 v217, v27, 1.0 op_sel:[1,0,0]
	v_lshl_or_b32 v0, v0, 7, v209
	global_load_dwordx4 v[24:27], v0, s[6:7]
	v_mfma_f32_4x4x4_16b_bf16 v[228:231], v[214:215], v[16:17], v[228:231]
	v_cvt_scalef32_pk_bf16_fp8 v218, v28, 1.0
	v_cvt_scalef32_pk_bf16_fp8 v219, v28, 1.0 op_sel:[1,0,0]
	v_mfma_f32_4x4x4_16b_bf16 v[228:231], v[216:217], v[18:19], v[228:231]
	v_cvt_scalef32_pk_bf16_fp8 v220, v29, 1.0
	v_cvt_scalef32_pk_bf16_fp8 v221, v29, 1.0 op_sel:[1,0,0]
	v_mfma_f32_4x4x4_16b_bf16 v[232:235], v[218:219], v[20:21], 0
	v_cvt_scalef32_pk_bf16_fp8 v222, v30, 1.0
	v_cvt_scalef32_pk_bf16_fp8 v223, v30, 1.0 op_sel:[1,0,0]
	v_mfma_f32_4x4x4_16b_bf16 v[232:235], v[220:221], v[22:23], v[232:235]
	v_cvt_scalef32_pk_bf16_fp8 v224, v31, 1.0
	v_cvt_scalef32_pk_bf16_fp8 v225, v31, 1.0 op_sel:[1,0,0]
	v_lshl_or_b32 v1, v1, 7, v209
	global_load_dwordx4 v[28:31], v1, s[6:7]
	v_mfma_f32_4x4x4_16b_bf16 v[232:235], v[222:223], v[16:17], v[232:235]
	v_cvt_scalef32_pk_bf16_fp8 v210, v32, 1.0
	v_cvt_scalef32_pk_bf16_fp8 v211, v32, 1.0 op_sel:[1,0,0]
	v_mfma_f32_4x4x4_16b_bf16 v[232:235], v[224:225], v[18:19], v[232:235]
	v_cvt_scalef32_pk_bf16_fp8 v212, v33, 1.0
	v_cvt_scalef32_pk_bf16_fp8 v213, v33, 1.0 op_sel:[1,0,0]
	v_cndmask_b32_e64 v184, v228, v229, s[22:23]
	v_cndmask_b32_e64 v184, v184, v230, s[24:25]
	v_cndmask_b32_e64 v184, v184, v231, s[26:27]
	v_mfma_f32_4x4x4_16b_bf16 v[228:231], v[210:211], v[20:21], 0
	v_cvt_scalef32_pk_bf16_fp8 v214, v34, 1.0
	v_cvt_scalef32_pk_bf16_fp8 v215, v34, 1.0 op_sel:[1,0,0]
	v_mfma_f32_4x4x4_16b_bf16 v[228:231], v[212:213], v[22:23], v[228:231]
	v_cvt_scalef32_pk_bf16_fp8 v216, v35, 1.0
	v_cvt_scalef32_pk_bf16_fp8 v217, v35, 1.0 op_sel:[1,0,0]
	v_lshl_or_b32 v2, v2, 7, v209
	global_load_dwordx4 v[32:35], v2, s[6:7]
	v_mfma_f32_4x4x4_16b_bf16 v[228:231], v[214:215], v[16:17], v[228:231]
	v_cvt_scalef32_pk_bf16_fp8 v218, v36, 1.0
	v_cvt_scalef32_pk_bf16_fp8 v219, v36, 1.0 op_sel:[1,0,0]
	v_mfma_f32_4x4x4_16b_bf16 v[228:231], v[216:217], v[18:19], v[228:231]
	v_cvt_scalef32_pk_bf16_fp8 v220, v37, 1.0
	v_cvt_scalef32_pk_bf16_fp8 v221, v37, 1.0 op_sel:[1,0,0]
	v_cndmask_b32_e64 v185, v232, v233, s[22:23]
	v_cndmask_b32_e64 v185, v185, v234, s[24:25]
	v_cndmask_b32_e64 v185, v185, v235, s[26:27]
	v_mfma_f32_4x4x4_16b_bf16 v[232:235], v[218:219], v[20:21], 0
	v_cvt_scalef32_pk_bf16_fp8 v222, v38, 1.0
	v_cvt_scalef32_pk_bf16_fp8 v223, v38, 1.0 op_sel:[1,0,0]
	v_mfma_f32_4x4x4_16b_bf16 v[232:235], v[220:221], v[22:23], v[232:235]
	v_cvt_scalef32_pk_bf16_fp8 v224, v39, 1.0
	v_cvt_scalef32_pk_bf16_fp8 v225, v39, 1.0 op_sel:[1,0,0]
	v_lshl_or_b32 v3, v3, 7, v209
	global_load_dwordx4 v[36:39], v3, s[6:7]
	v_mfma_f32_4x4x4_16b_bf16 v[232:235], v[222:223], v[16:17], v[232:235]
	v_cvt_scalef32_pk_bf16_fp8 v210, v40, 1.0
	v_cvt_scalef32_pk_bf16_fp8 v211, v40, 1.0 op_sel:[1,0,0]
	v_mfma_f32_4x4x4_16b_bf16 v[232:235], v[224:225], v[18:19], v[232:235]
	v_cvt_scalef32_pk_bf16_fp8 v212, v41, 1.0
	v_cvt_scalef32_pk_bf16_fp8 v213, v41, 1.0 op_sel:[1,0,0]
	v_cndmask_b32_e64 v186, v228, v229, s[22:23]
	v_cndmask_b32_e64 v186, v186, v230, s[24:25]
	v_cndmask_b32_e64 v186, v186, v231, s[26:27]
	v_mfma_f32_4x4x4_16b_bf16 v[228:231], v[210:211], v[20:21], 0
	v_cvt_scalef32_pk_bf16_fp8 v214, v42, 1.0
	v_cvt_scalef32_pk_bf16_fp8 v215, v42, 1.0 op_sel:[1,0,0]
	v_mfma_f32_4x4x4_16b_bf16 v[228:231], v[212:213], v[22:23], v[228:231]
	v_cvt_scalef32_pk_bf16_fp8 v216, v43, 1.0
	v_cvt_scalef32_pk_bf16_fp8 v217, v43, 1.0 op_sel:[1,0,0]
	v_lshl_or_b32 v4, v4, 7, v209
	global_load_dwordx4 v[40:43], v4, s[6:7]
	v_mfma_f32_4x4x4_16b_bf16 v[228:231], v[214:215], v[16:17], v[228:231]
	v_cvt_scalef32_pk_bf16_fp8 v218, v44, 1.0
	v_cvt_scalef32_pk_bf16_fp8 v219, v44, 1.0 op_sel:[1,0,0]
	v_mfma_f32_4x4x4_16b_bf16 v[228:231], v[216:217], v[18:19], v[228:231]
	v_cvt_scalef32_pk_bf16_fp8 v220, v45, 1.0
	v_cvt_scalef32_pk_bf16_fp8 v221, v45, 1.0 op_sel:[1,0,0]
	v_cndmask_b32_e64 v187, v232, v233, s[22:23]
	v_cndmask_b32_e64 v187, v187, v234, s[24:25]
	v_cndmask_b32_e64 v187, v187, v235, s[26:27]
	v_mfma_f32_4x4x4_16b_bf16 v[232:235], v[218:219], v[20:21], 0
	v_cvt_scalef32_pk_bf16_fp8 v222, v46, 1.0
	v_cvt_scalef32_pk_bf16_fp8 v223, v46, 1.0 op_sel:[1,0,0]
	v_mfma_f32_4x4x4_16b_bf16 v[232:235], v[220:221], v[22:23], v[232:235]
	v_cvt_scalef32_pk_bf16_fp8 v224, v47, 1.0
	v_cvt_scalef32_pk_bf16_fp8 v225, v47, 1.0 op_sel:[1,0,0]
	v_lshl_or_b32 v5, v5, 7, v209
	global_load_dwordx4 v[44:47], v5, s[6:7]
	v_mfma_f32_4x4x4_16b_bf16 v[232:235], v[222:223], v[16:17], v[232:235]
	v_cvt_scalef32_pk_bf16_fp8 v210, v48, 1.0
	v_cvt_scalef32_pk_bf16_fp8 v211, v48, 1.0 op_sel:[1,0,0]
	v_mfma_f32_4x4x4_16b_bf16 v[232:235], v[224:225], v[18:19], v[232:235]
	v_cvt_scalef32_pk_bf16_fp8 v212, v49, 1.0
	v_cvt_scalef32_pk_bf16_fp8 v213, v49, 1.0 op_sel:[1,0,0]
	v_cndmask_b32_e64 v188, v228, v229, s[22:23]
	v_cndmask_b32_e64 v188, v188, v230, s[24:25]
	v_cndmask_b32_e64 v188, v188, v231, s[26:27]
	v_mfma_f32_4x4x4_16b_bf16 v[228:231], v[210:211], v[20:21], 0
	v_cvt_scalef32_pk_bf16_fp8 v214, v50, 1.0
	v_cvt_scalef32_pk_bf16_fp8 v215, v50, 1.0 op_sel:[1,0,0]
	v_mfma_f32_4x4x4_16b_bf16 v[228:231], v[212:213], v[22:23], v[228:231]
	v_cvt_scalef32_pk_bf16_fp8 v216, v51, 1.0
	v_cvt_scalef32_pk_bf16_fp8 v217, v51, 1.0 op_sel:[1,0,0]
	v_lshl_or_b32 v6, v6, 7, v209
	global_load_dwordx4 v[48:51], v6, s[6:7]
	v_mfma_f32_4x4x4_16b_bf16 v[228:231], v[214:215], v[16:17], v[228:231]
	v_cvt_scalef32_pk_bf16_fp8 v218, v52, 1.0
	v_cvt_scalef32_pk_bf16_fp8 v219, v52, 1.0 op_sel:[1,0,0]
	v_mfma_f32_4x4x4_16b_bf16 v[228:231], v[216:217], v[18:19], v[228:231]
	v_cvt_scalef32_pk_bf16_fp8 v220, v53, 1.0
	v_cvt_scalef32_pk_bf16_fp8 v221, v53, 1.0 op_sel:[1,0,0]
	v_cndmask_b32_e64 v189, v232, v233, s[22:23]
	v_cndmask_b32_e64 v189, v189, v234, s[24:25]
	v_cndmask_b32_e64 v189, v189, v235, s[26:27]
	v_mfma_f32_4x4x4_16b_bf16 v[232:235], v[218:219], v[20:21], 0
	v_cvt_scalef32_pk_bf16_fp8 v222, v54, 1.0
	v_cvt_scalef32_pk_bf16_fp8 v223, v54, 1.0 op_sel:[1,0,0]
	v_mfma_f32_4x4x4_16b_bf16 v[232:235], v[220:221], v[22:23], v[232:235]
	v_cvt_scalef32_pk_bf16_fp8 v224, v55, 1.0
	v_cvt_scalef32_pk_bf16_fp8 v225, v55, 1.0 op_sel:[1,0,0]
	v_lshl_or_b32 v7, v7, 7, v209
	global_load_dwordx4 v[52:55], v7, s[6:7]
	v_mfma_f32_4x4x4_16b_bf16 v[232:235], v[222:223], v[16:17], v[232:235]
	v_cvt_scalef32_pk_bf16_fp8 v210, v56, 1.0
	v_cvt_scalef32_pk_bf16_fp8 v211, v56, 1.0 op_sel:[1,0,0]
	v_mfma_f32_4x4x4_16b_bf16 v[232:235], v[224:225], v[18:19], v[232:235]
	v_cvt_scalef32_pk_bf16_fp8 v212, v57, 1.0
	v_cvt_scalef32_pk_bf16_fp8 v213, v57, 1.0 op_sel:[1,0,0]
	v_cndmask_b32_e64 v190, v228, v229, s[22:23]
	v_cndmask_b32_e64 v190, v190, v230, s[24:25]
	v_cndmask_b32_e64 v190, v190, v231, s[26:27]
	v_mfma_f32_4x4x4_16b_bf16 v[228:231], v[210:211], v[20:21], 0
	v_cvt_scalef32_pk_bf16_fp8 v214, v58, 1.0
	v_cvt_scalef32_pk_bf16_fp8 v215, v58, 1.0 op_sel:[1,0,0]
	v_mfma_f32_4x4x4_16b_bf16 v[228:231], v[212:213], v[22:23], v[228:231]
	v_cvt_scalef32_pk_bf16_fp8 v216, v59, 1.0
	v_cvt_scalef32_pk_bf16_fp8 v217, v59, 1.0 op_sel:[1,0,0]
	v_lshl_or_b32 v8, v8, 7, v209
	global_load_dwordx4 v[56:59], v8, s[6:7]
	v_mfma_f32_4x4x4_16b_bf16 v[228:231], v[214:215], v[16:17], v[228:231]
	v_cvt_scalef32_pk_bf16_fp8 v218, v60, 1.0
	v_cvt_scalef32_pk_bf16_fp8 v219, v60, 1.0 op_sel:[1,0,0]
	v_mfma_f32_4x4x4_16b_bf16 v[228:231], v[216:217], v[18:19], v[228:231]
	v_cvt_scalef32_pk_bf16_fp8 v220, v61, 1.0
	v_cvt_scalef32_pk_bf16_fp8 v221, v61, 1.0 op_sel:[1,0,0]
	v_cndmask_b32_e64 v191, v232, v233, s[22:23]
	v_cndmask_b32_e64 v191, v191, v234, s[24:25]
	v_cndmask_b32_e64 v191, v191, v235, s[26:27]
	v_mfma_f32_4x4x4_16b_bf16 v[232:235], v[218:219], v[20:21], 0
	v_cvt_scalef32_pk_bf16_fp8 v222, v62, 1.0
	v_cvt_scalef32_pk_bf16_fp8 v223, v62, 1.0 op_sel:[1,0,0]
	v_mfma_f32_4x4x4_16b_bf16 v[232:235], v[220:221], v[22:23], v[232:235]
	v_cvt_scalef32_pk_bf16_fp8 v224, v63, 1.0
	v_cvt_scalef32_pk_bf16_fp8 v225, v63, 1.0 op_sel:[1,0,0]
	v_lshl_or_b32 v9, v9, 7, v209
	global_load_dwordx4 v[60:63], v9, s[6:7]
	v_mfma_f32_4x4x4_16b_bf16 v[232:235], v[222:223], v[16:17], v[232:235]
	v_cvt_scalef32_pk_bf16_fp8 v210, v76, 1.0
	v_cvt_scalef32_pk_bf16_fp8 v211, v76, 1.0 op_sel:[1,0,0]
	v_mfma_f32_4x4x4_16b_bf16 v[232:235], v[224:225], v[18:19], v[232:235]
	v_cvt_scalef32_pk_bf16_fp8 v212, v77, 1.0
	v_cvt_scalef32_pk_bf16_fp8 v213, v77, 1.0 op_sel:[1,0,0]
	v_cndmask_b32_e64 v192, v228, v229, s[22:23]
	v_cndmask_b32_e64 v192, v192, v230, s[24:25]
	v_cndmask_b32_e64 v192, v192, v231, s[26:27]
	v_mfma_f32_4x4x4_16b_bf16 v[228:231], v[210:211], v[20:21], 0
	v_cvt_scalef32_pk_bf16_fp8 v214, v78, 1.0
	v_cvt_scalef32_pk_bf16_fp8 v215, v78, 1.0 op_sel:[1,0,0]
	v_mfma_f32_4x4x4_16b_bf16 v[228:231], v[212:213], v[22:23], v[228:231]
	v_cvt_scalef32_pk_bf16_fp8 v216, v79, 1.0
	v_cvt_scalef32_pk_bf16_fp8 v217, v79, 1.0 op_sel:[1,0,0]
	v_lshl_or_b32 v10, v10, 7, v209
	global_load_dwordx4 v[76:79], v10, s[6:7]
	v_mfma_f32_4x4x4_16b_bf16 v[228:231], v[214:215], v[16:17], v[228:231]
	v_cvt_scalef32_pk_bf16_fp8 v218, v84, 1.0
	v_cvt_scalef32_pk_bf16_fp8 v219, v84, 1.0 op_sel:[1,0,0]
	v_mfma_f32_4x4x4_16b_bf16 v[228:231], v[216:217], v[18:19], v[228:231]
	v_cvt_scalef32_pk_bf16_fp8 v220, v85, 1.0
	v_cvt_scalef32_pk_bf16_fp8 v221, v85, 1.0 op_sel:[1,0,0]
	v_cndmask_b32_e64 v193, v232, v233, s[22:23]
	v_cndmask_b32_e64 v193, v193, v234, s[24:25]
	v_cndmask_b32_e64 v193, v193, v235, s[26:27]
	v_mfma_f32_4x4x4_16b_bf16 v[232:235], v[218:219], v[20:21], 0
	v_cvt_scalef32_pk_bf16_fp8 v222, v86, 1.0
	v_cvt_scalef32_pk_bf16_fp8 v223, v86, 1.0 op_sel:[1,0,0]
	v_mfma_f32_4x4x4_16b_bf16 v[232:235], v[220:221], v[22:23], v[232:235]
	v_cvt_scalef32_pk_bf16_fp8 v224, v87, 1.0
	v_cvt_scalef32_pk_bf16_fp8 v225, v87, 1.0 op_sel:[1,0,0]
	v_lshl_or_b32 v11, v11, 7, v209
	global_load_dwordx4 v[84:87], v11, s[6:7]
	v_mfma_f32_4x4x4_16b_bf16 v[232:235], v[222:223], v[16:17], v[232:235]
	v_cvt_scalef32_pk_bf16_fp8 v210, v88, 1.0
	v_cvt_scalef32_pk_bf16_fp8 v211, v88, 1.0 op_sel:[1,0,0]
	v_mfma_f32_4x4x4_16b_bf16 v[232:235], v[224:225], v[18:19], v[232:235]
	v_cvt_scalef32_pk_bf16_fp8 v212, v89, 1.0
	v_cvt_scalef32_pk_bf16_fp8 v213, v89, 1.0 op_sel:[1,0,0]
	v_cndmask_b32_e64 v194, v228, v229, s[22:23]
	v_cndmask_b32_e64 v194, v194, v230, s[24:25]
	v_cndmask_b32_e64 v194, v194, v231, s[26:27]
	v_mfma_f32_4x4x4_16b_bf16 v[228:231], v[210:211], v[20:21], 0
	v_cvt_scalef32_pk_bf16_fp8 v214, v90, 1.0
	v_cvt_scalef32_pk_bf16_fp8 v215, v90, 1.0 op_sel:[1,0,0]
	v_mfma_f32_4x4x4_16b_bf16 v[228:231], v[212:213], v[22:23], v[228:231]
	v_cvt_scalef32_pk_bf16_fp8 v216, v91, 1.0
	v_cvt_scalef32_pk_bf16_fp8 v217, v91, 1.0 op_sel:[1,0,0]
	v_lshl_or_b32 v12, v12, 7, v209
	global_load_dwordx4 v[88:91], v12, s[6:7]
	v_mfma_f32_4x4x4_16b_bf16 v[228:231], v[214:215], v[16:17], v[228:231]
	v_cvt_scalef32_pk_bf16_fp8 v218, v92, 1.0
	v_cvt_scalef32_pk_bf16_fp8 v219, v92, 1.0 op_sel:[1,0,0]
	v_mfma_f32_4x4x4_16b_bf16 v[228:231], v[216:217], v[18:19], v[228:231]
	v_cvt_scalef32_pk_bf16_fp8 v220, v93, 1.0
	v_cvt_scalef32_pk_bf16_fp8 v221, v93, 1.0 op_sel:[1,0,0]
	v_cndmask_b32_e64 v195, v232, v233, s[22:23]
	v_cndmask_b32_e64 v195, v195, v234, s[24:25]
	v_cndmask_b32_e64 v195, v195, v235, s[26:27]
	v_mfma_f32_4x4x4_16b_bf16 v[232:235], v[218:219], v[20:21], 0
	v_cvt_scalef32_pk_bf16_fp8 v222, v94, 1.0
	v_cvt_scalef32_pk_bf16_fp8 v223, v94, 1.0 op_sel:[1,0,0]
	v_mfma_f32_4x4x4_16b_bf16 v[232:235], v[220:221], v[22:23], v[232:235]
	v_cvt_scalef32_pk_bf16_fp8 v224, v95, 1.0
	v_cvt_scalef32_pk_bf16_fp8 v225, v95, 1.0 op_sel:[1,0,0]
	v_lshl_or_b32 v13, v13, 7, v209
	global_load_dwordx4 v[92:95], v13, s[6:7]
	v_mfma_f32_4x4x4_16b_bf16 v[232:235], v[222:223], v[16:17], v[232:235]
	v_cvt_scalef32_pk_bf16_fp8 v210, v96, 1.0
	v_cvt_scalef32_pk_bf16_fp8 v211, v96, 1.0 op_sel:[1,0,0]
	v_mfma_f32_4x4x4_16b_bf16 v[232:235], v[224:225], v[18:19], v[232:235]
	v_cvt_scalef32_pk_bf16_fp8 v212, v97, 1.0
	v_cvt_scalef32_pk_bf16_fp8 v213, v97, 1.0 op_sel:[1,0,0]
	v_cndmask_b32_e64 v196, v228, v229, s[22:23]
	v_cndmask_b32_e64 v196, v196, v230, s[24:25]
	v_cndmask_b32_e64 v196, v196, v231, s[26:27]
	v_mfma_f32_4x4x4_16b_bf16 v[228:231], v[210:211], v[20:21], 0
	v_cvt_scalef32_pk_bf16_fp8 v214, v98, 1.0
	v_cvt_scalef32_pk_bf16_fp8 v215, v98, 1.0 op_sel:[1,0,0]
	v_mfma_f32_4x4x4_16b_bf16 v[228:231], v[212:213], v[22:23], v[228:231]
	v_cvt_scalef32_pk_bf16_fp8 v216, v99, 1.0
	v_cvt_scalef32_pk_bf16_fp8 v217, v99, 1.0 op_sel:[1,0,0]
	v_lshl_or_b32 v14, v14, 7, v209
	global_load_dwordx4 v[96:99], v14, s[6:7]
	v_mfma_f32_4x4x4_16b_bf16 v[228:231], v[214:215], v[16:17], v[228:231]
	v_cvt_scalef32_pk_bf16_fp8 v218, v104, 1.0
	v_cvt_scalef32_pk_bf16_fp8 v219, v104, 1.0 op_sel:[1,0,0]
	v_mfma_f32_4x4x4_16b_bf16 v[228:231], v[216:217], v[18:19], v[228:231]
	v_cvt_scalef32_pk_bf16_fp8 v220, v105, 1.0
	v_cvt_scalef32_pk_bf16_fp8 v221, v105, 1.0 op_sel:[1,0,0]
	v_cndmask_b32_e64 v197, v232, v233, s[22:23]
	v_cndmask_b32_e64 v197, v197, v234, s[24:25]
	v_cndmask_b32_e64 v197, v197, v235, s[26:27]
	v_mfma_f32_4x4x4_16b_bf16 v[232:235], v[218:219], v[20:21], 0
	v_cvt_scalef32_pk_bf16_fp8 v222, v106, 1.0
	v_cvt_scalef32_pk_bf16_fp8 v223, v106, 1.0 op_sel:[1,0,0]
	v_mfma_f32_4x4x4_16b_bf16 v[232:235], v[220:221], v[22:23], v[232:235]
	v_cvt_scalef32_pk_bf16_fp8 v224, v107, 1.0
	v_cvt_scalef32_pk_bf16_fp8 v225, v107, 1.0 op_sel:[1,0,0]
	v_lshl_or_b32 v15, v15, 7, v209
	global_load_dwordx4 v[104:107], v15, s[6:7]
	v_mfma_f32_4x4x4_16b_bf16 v[232:235], v[222:223], v[16:17], v[232:235]
	s_nop 1
	v_mfma_f32_4x4x4_16b_bf16 v[232:235], v[224:225], v[18:19], v[232:235]
	v_cndmask_b32_e64 v198, v228, v229, s[22:23]
	v_cndmask_b32_e64 v198, v198, v230, s[24:25]
	v_cndmask_b32_e64 v198, v198, v231, s[26:27]
	s_nop 4
	v_cndmask_b32_e64 v199, v232, v233, s[22:23]
	v_cndmask_b32_e64 v199, v199, v234, s[24:25]
	v_cndmask_b32_e64 v199, v199, v235, s[26:27]
	v_cndmask_b32_e64 v200, v184, v192, s[4:5]
	v_cndmask_b32_e64 v201, v192, v184, s[4:5]
	v_cndmask_b32_e64 v202, v185, v193, s[4:5]
	v_cndmask_b32_e64 v203, v193, v185, s[4:5]
	v_cndmask_b32_e64 v204, v186, v194, s[4:5]
	v_cndmask_b32_e64 v205, v194, v186, s[4:5]
	v_cndmask_b32_e64 v236, v187, v195, s[4:5]
	v_cndmask_b32_e64 v237, v195, v187, s[4:5]
	v_cndmask_b32_e64 v238, v188, v196, s[4:5]
	v_cndmask_b32_e64 v239, v196, v188, s[4:5]
	v_cndmask_b32_e64 v240, v189, v197, s[4:5]
	v_cndmask_b32_e64 v241, v197, v189, s[4:5]
	v_cndmask_b32_e64 v242, v190, v198, s[4:5]
	v_cndmask_b32_e64 v243, v198, v190, s[4:5]
	v_cndmask_b32_e64 v244, v191, v199, s[4:5]
	v_cndmask_b32_e64 v245, v199, v191, s[4:5]
	v_add_f32_dpp v246, v200, v201 row_half_mirror row_mask:0xf bank_mask:0xf
	v_add_f32_dpp v247, v202, v203 row_half_mirror row_mask:0xf bank_mask:0xf
	v_add_f32_dpp v248, v204, v205 row_half_mirror row_mask:0xf bank_mask:0xf
	v_add_f32_dpp v249, v236, v237 row_half_mirror row_mask:0xf bank_mask:0xf
	v_add_f32_dpp v226, v238, v239 row_half_mirror row_mask:0xf bank_mask:0xf
	v_add_f32_dpp v227, v240, v241 row_half_mirror row_mask:0xf bank_mask:0xf
	v_add_f32_dpp v210, v242, v243 row_half_mirror row_mask:0xf bank_mask:0xf
	v_add_f32_dpp v211, v244, v245 row_half_mirror row_mask:0xf bank_mask:0xf
	v_cndmask_b32_e64 v200, v246, v226, s[2:3]
	v_cndmask_b32_e64 v201, v226, v246, s[2:3]
	v_cndmask_b32_e64 v202, v247, v227, s[2:3]
	v_cndmask_b32_e64 v203, v227, v247, s[2:3]
	v_cndmask_b32_e64 v204, v248, v210, s[2:3]
	v_cndmask_b32_e64 v205, v210, v248, s[2:3]
	v_cndmask_b32_e64 v236, v249, v211, s[2:3]
	v_cndmask_b32_e64 v237, v211, v249, s[2:3]
	v_add_f32_dpp v212, v200, v201 quad_perm:[2,3,0,1] row_mask:0xf bank_mask:0xf
	v_add_f32_dpp v213, v202, v203 quad_perm:[2,3,0,1] row_mask:0xf bank_mask:0xf
	v_add_f32_dpp v214, v204, v205 quad_perm:[2,3,0,1] row_mask:0xf bank_mask:0xf
	v_add_f32_dpp v215, v236, v237 quad_perm:[2,3,0,1] row_mask:0xf bank_mask:0xf
	v_cndmask_b32_e64 v200, v212, v214, s[0:1]
	v_cndmask_b32_e64 v201, v214, v212, s[0:1]
	v_cndmask_b32_e64 v202, v213, v215, s[0:1]
	v_cndmask_b32_e64 v203, v215, v213, s[0:1]
	s_nop 1
	v_add_f32_dpp v216, v200, v201 quad_perm:[1,0,3,2] row_mask:0xf bank_mask:0xf
	v_add_f32_dpp v217, v202, v203 quad_perm:[1,0,3,2] row_mask:0xf bank_mask:0xf
	s_ashr_i32 s15, s14, 31
	s_lshl_b64 s[14:15], s[14:15], 8
	v_cvt_pk_bf16_f32 v186, v216, v217
	v_lshl_add_u64 v[184:185], v[178:179], 0, s[14:15]
	global_store_dword v[184:185], v186, off
	s_add_u32 s20, s12, 0x200
	s_lshl_b32 s20, s20, 11
	v_lshl_add_u64 v[20:21], v[182:183], 0, s[20:21]
	global_load_dwordx4 v[16:19], v[20:21], off offset:16
	s_nop 0
	global_load_dwordx4 v[20:23], v[20:21], off
	s_add_u32 s20, s12, 0x400
	s_lshl_b32 s20, s20, 9
	v_lshl_add_u64 v[0:1], v[180:181], 0, s[20:21]
	global_load_dwordx4 v[12:15], v[0:1], off offset:48
	global_load_dwordx4 v[8:11], v[0:1], off offset:32
	global_load_dwordx4 v[4:7], v[0:1], off offset:16
	s_nop 0
	global_load_dwordx4 v[0:3], v[0:1], off
	s_add_u32 s10, s12, 0x100
	s_waitcnt vmcnt(23)
	v_cvt_scalef32_pk_bf16_fp8 v210, v112, 1.0
	v_cvt_scalef32_pk_bf16_fp8 v211, v112, 1.0 op_sel:[1,0,0]
	v_cvt_scalef32_pk_bf16_fp8 v212, v113, 1.0
	v_cvt_scalef32_pk_bf16_fp8 v213, v113, 1.0 op_sel:[1,0,0]
	v_mfma_f32_4x4x4_16b_bf16 v[228:231], v[210:211], v[108:109], 0
	v_cvt_scalef32_pk_bf16_fp8 v214, v114, 1.0
	v_cvt_scalef32_pk_bf16_fp8 v215, v114, 1.0 op_sel:[1,0,0]
	v_mfma_f32_4x4x4_16b_bf16 v[228:231], v[212:213], v[110:111], v[228:231]
	v_cvt_scalef32_pk_bf16_fp8 v216, v115, 1.0
	v_cvt_scalef32_pk_bf16_fp8 v217, v115, 1.0 op_sel:[1,0,0]
	v_lshl_or_b32 v80, v80, 7, v209
	global_load_dwordx4 v[112:115], v80, s[6:7]
	v_mfma_f32_4x4x4_16b_bf16 v[228:231], v[214:215], v[100:101], v[228:231]
	v_cvt_scalef32_pk_bf16_fp8 v218, v116, 1.0
	v_cvt_scalef32_pk_bf16_fp8 v219, v116, 1.0 op_sel:[1,0,0]
	v_mfma_f32_4x4x4_16b_bf16 v[228:231], v[216:217], v[102:103], v[228:231]
	v_cvt_scalef32_pk_bf16_fp8 v220, v117, 1.0
	v_cvt_scalef32_pk_bf16_fp8 v221, v117, 1.0 op_sel:[1,0,0]
	v_mfma_f32_4x4x4_16b_bf16 v[232:235], v[218:219], v[108:109], 0
	v_cvt_scalef32_pk_bf16_fp8 v222, v118, 1.0
	v_cvt_scalef32_pk_bf16_fp8 v223, v118, 1.0 op_sel:[1,0,0]
	v_mfma_f32_4x4x4_16b_bf16 v[232:235], v[220:221], v[110:111], v[232:235]
	v_cvt_scalef32_pk_bf16_fp8 v224, v119, 1.0
	v_cvt_scalef32_pk_bf16_fp8 v225, v119, 1.0 op_sel:[1,0,0]
	v_lshl_or_b32 v81, v81, 7, v209
	global_load_dwordx4 v[116:119], v81, s[6:7]
	v_mfma_f32_4x4x4_16b_bf16 v[232:235], v[222:223], v[100:101], v[232:235]
	v_cvt_scalef32_pk_bf16_fp8 v210, v120, 1.0
	v_cvt_scalef32_pk_bf16_fp8 v211, v120, 1.0 op_sel:[1,0,0]
	v_mfma_f32_4x4x4_16b_bf16 v[232:235], v[224:225], v[102:103], v[232:235]
	v_cvt_scalef32_pk_bf16_fp8 v212, v121, 1.0
	v_cvt_scalef32_pk_bf16_fp8 v213, v121, 1.0 op_sel:[1,0,0]
	v_cndmask_b32_e64 v184, v228, v229, s[22:23]
	v_cndmask_b32_e64 v184, v184, v230, s[24:25]
	v_cndmask_b32_e64 v184, v184, v231, s[26:27]
	v_mfma_f32_4x4x4_16b_bf16 v[228:231], v[210:211], v[108:109], 0
	v_cvt_scalef32_pk_bf16_fp8 v214, v122, 1.0
	v_cvt_scalef32_pk_bf16_fp8 v215, v122, 1.0 op_sel:[1,0,0]
	v_mfma_f32_4x4x4_16b_bf16 v[228:231], v[212:213], v[110:111], v[228:231]
	v_cvt_scalef32_pk_bf16_fp8 v216, v123, 1.0
	v_cvt_scalef32_pk_bf16_fp8 v217, v123, 1.0 op_sel:[1,0,0]
	v_lshl_or_b32 v82, v82, 7, v209
	global_load_dwordx4 v[120:123], v82, s[6:7]
	v_mfma_f32_4x4x4_16b_bf16 v[228:231], v[214:215], v[100:101], v[228:231]
	v_cvt_scalef32_pk_bf16_fp8 v218, v124, 1.0
	v_cvt_scalef32_pk_bf16_fp8 v219, v124, 1.0 op_sel:[1,0,0]
	v_mfma_f32_4x4x4_16b_bf16 v[228:231], v[216:217], v[102:103], v[228:231]
	v_cvt_scalef32_pk_bf16_fp8 v220, v125, 1.0
	v_cvt_scalef32_pk_bf16_fp8 v221, v125, 1.0 op_sel:[1,0,0]
	v_cndmask_b32_e64 v185, v232, v233, s[22:23]
	v_cndmask_b32_e64 v185, v185, v234, s[24:25]
	v_cndmask_b32_e64 v185, v185, v235, s[26:27]
	v_mfma_f32_4x4x4_16b_bf16 v[232:235], v[218:219], v[108:109], 0
	v_cvt_scalef32_pk_bf16_fp8 v222, v126, 1.0
	v_cvt_scalef32_pk_bf16_fp8 v223, v126, 1.0 op_sel:[1,0,0]
	v_mfma_f32_4x4x4_16b_bf16 v[232:235], v[220:221], v[110:111], v[232:235]
	v_cvt_scalef32_pk_bf16_fp8 v224, v127, 1.0
	v_cvt_scalef32_pk_bf16_fp8 v225, v127, 1.0 op_sel:[1,0,0]
	v_lshl_or_b32 v83, v83, 7, v209
	global_load_dwordx4 v[124:127], v83, s[6:7]
	v_mfma_f32_4x4x4_16b_bf16 v[232:235], v[222:223], v[100:101], v[232:235]
	v_cvt_scalef32_pk_bf16_fp8 v210, v128, 1.0
	v_cvt_scalef32_pk_bf16_fp8 v211, v128, 1.0 op_sel:[1,0,0]
	v_mfma_f32_4x4x4_16b_bf16 v[232:235], v[224:225], v[102:103], v[232:235]
	v_cvt_scalef32_pk_bf16_fp8 v212, v129, 1.0
	v_cvt_scalef32_pk_bf16_fp8 v213, v129, 1.0 op_sel:[1,0,0]
	v_cndmask_b32_e64 v186, v228, v229, s[22:23]
	v_cndmask_b32_e64 v186, v186, v230, s[24:25]
	v_cndmask_b32_e64 v186, v186, v231, s[26:27]
	v_mfma_f32_4x4x4_16b_bf16 v[228:231], v[210:211], v[108:109], 0
	v_cvt_scalef32_pk_bf16_fp8 v214, v130, 1.0
	v_cvt_scalef32_pk_bf16_fp8 v215, v130, 1.0 op_sel:[1,0,0]
	v_mfma_f32_4x4x4_16b_bf16 v[228:231], v[212:213], v[110:111], v[228:231]
	v_cvt_scalef32_pk_bf16_fp8 v216, v131, 1.0
	v_cvt_scalef32_pk_bf16_fp8 v217, v131, 1.0 op_sel:[1,0,0]
	v_lshl_or_b32 v72, v72, 7, v209
	global_load_dwordx4 v[128:131], v72, s[6:7]
	v_mfma_f32_4x4x4_16b_bf16 v[228:231], v[214:215], v[100:101], v[228:231]
	v_cvt_scalef32_pk_bf16_fp8 v218, v132, 1.0
	v_cvt_scalef32_pk_bf16_fp8 v219, v132, 1.0 op_sel:[1,0,0]
	v_mfma_f32_4x4x4_16b_bf16 v[228:231], v[216:217], v[102:103], v[228:231]
	v_cvt_scalef32_pk_bf16_fp8 v220, v133, 1.0
	v_cvt_scalef32_pk_bf16_fp8 v221, v133, 1.0 op_sel:[1,0,0]
	v_cndmask_b32_e64 v187, v232, v233, s[22:23]
	v_cndmask_b32_e64 v187, v187, v234, s[24:25]
	v_cndmask_b32_e64 v187, v187, v235, s[26:27]
	v_mfma_f32_4x4x4_16b_bf16 v[232:235], v[218:219], v[108:109], 0
	v_cvt_scalef32_pk_bf16_fp8 v222, v134, 1.0
	v_cvt_scalef32_pk_bf16_fp8 v223, v134, 1.0 op_sel:[1,0,0]
	v_mfma_f32_4x4x4_16b_bf16 v[232:235], v[220:221], v[110:111], v[232:235]
	v_cvt_scalef32_pk_bf16_fp8 v224, v135, 1.0
	v_cvt_scalef32_pk_bf16_fp8 v225, v135, 1.0 op_sel:[1,0,0]
	v_lshl_or_b32 v73, v73, 7, v209
	global_load_dwordx4 v[132:135], v73, s[6:7]
	v_mfma_f32_4x4x4_16b_bf16 v[232:235], v[222:223], v[100:101], v[232:235]
	v_cvt_scalef32_pk_bf16_fp8 v210, v136, 1.0
	v_cvt_scalef32_pk_bf16_fp8 v211, v136, 1.0 op_sel:[1,0,0]
	v_mfma_f32_4x4x4_16b_bf16 v[232:235], v[224:225], v[102:103], v[232:235]
	v_cvt_scalef32_pk_bf16_fp8 v212, v137, 1.0
	v_cvt_scalef32_pk_bf16_fp8 v213, v137, 1.0 op_sel:[1,0,0]
	v_cndmask_b32_e64 v188, v228, v229, s[22:23]
	v_cndmask_b32_e64 v188, v188, v230, s[24:25]
	v_cndmask_b32_e64 v188, v188, v231, s[26:27]
	v_mfma_f32_4x4x4_16b_bf16 v[228:231], v[210:211], v[108:109], 0
	v_cvt_scalef32_pk_bf16_fp8 v214, v138, 1.0
	v_cvt_scalef32_pk_bf16_fp8 v215, v138, 1.0 op_sel:[1,0,0]
	v_mfma_f32_4x4x4_16b_bf16 v[228:231], v[212:213], v[110:111], v[228:231]
	v_cvt_scalef32_pk_bf16_fp8 v216, v139, 1.0
	v_cvt_scalef32_pk_bf16_fp8 v217, v139, 1.0 op_sel:[1,0,0]
	v_lshl_or_b32 v74, v74, 7, v209
	global_load_dwordx4 v[136:139], v74, s[6:7]
	v_mfma_f32_4x4x4_16b_bf16 v[228:231], v[214:215], v[100:101], v[228:231]
	v_cvt_scalef32_pk_bf16_fp8 v218, v140, 1.0
	v_cvt_scalef32_pk_bf16_fp8 v219, v140, 1.0 op_sel:[1,0,0]
	v_mfma_f32_4x4x4_16b_bf16 v[228:231], v[216:217], v[102:103], v[228:231]
	v_cvt_scalef32_pk_bf16_fp8 v220, v141, 1.0
	v_cvt_scalef32_pk_bf16_fp8 v221, v141, 1.0 op_sel:[1,0,0]
	v_cndmask_b32_e64 v189, v232, v233, s[22:23]
	v_cndmask_b32_e64 v189, v189, v234, s[24:25]
	v_cndmask_b32_e64 v189, v189, v235, s[26:27]
	v_mfma_f32_4x4x4_16b_bf16 v[232:235], v[218:219], v[108:109], 0
	v_cvt_scalef32_pk_bf16_fp8 v222, v142, 1.0
	v_cvt_scalef32_pk_bf16_fp8 v223, v142, 1.0 op_sel:[1,0,0]
	v_mfma_f32_4x4x4_16b_bf16 v[232:235], v[220:221], v[110:111], v[232:235]
	v_cvt_scalef32_pk_bf16_fp8 v224, v143, 1.0
	v_cvt_scalef32_pk_bf16_fp8 v225, v143, 1.0 op_sel:[1,0,0]
	v_lshl_or_b32 v75, v75, 7, v209
	global_load_dwordx4 v[140:143], v75, s[6:7]
	v_mfma_f32_4x4x4_16b_bf16 v[232:235], v[222:223], v[100:101], v[232:235]
	v_cvt_scalef32_pk_bf16_fp8 v210, v144, 1.0
	v_cvt_scalef32_pk_bf16_fp8 v211, v144, 1.0 op_sel:[1,0,0]
	v_mfma_f32_4x4x4_16b_bf16 v[232:235], v[224:225], v[102:103], v[232:235]
	v_cvt_scalef32_pk_bf16_fp8 v212, v145, 1.0
	v_cvt_scalef32_pk_bf16_fp8 v213, v145, 1.0 op_sel:[1,0,0]
	v_cndmask_b32_e64 v190, v228, v229, s[22:23]
	v_cndmask_b32_e64 v190, v190, v230, s[24:25]
	v_cndmask_b32_e64 v190, v190, v231, s[26:27]
	v_mfma_f32_4x4x4_16b_bf16 v[228:231], v[210:211], v[108:109], 0
	v_cvt_scalef32_pk_bf16_fp8 v214, v146, 1.0
	v_cvt_scalef32_pk_bf16_fp8 v215, v146, 1.0 op_sel:[1,0,0]
	v_mfma_f32_4x4x4_16b_bf16 v[228:231], v[212:213], v[110:111], v[228:231]
	v_cvt_scalef32_pk_bf16_fp8 v216, v147, 1.0
	v_cvt_scalef32_pk_bf16_fp8 v217, v147, 1.0 op_sel:[1,0,0]
	v_lshl_or_b32 v68, v68, 7, v209
	global_load_dwordx4 v[144:147], v68, s[6:7]
	v_mfma_f32_4x4x4_16b_bf16 v[228:231], v[214:215], v[100:101], v[228:231]
	v_cvt_scalef32_pk_bf16_fp8 v218, v148, 1.0
	v_cvt_scalef32_pk_bf16_fp8 v219, v148, 1.0 op_sel:[1,0,0]
	v_mfma_f32_4x4x4_16b_bf16 v[228:231], v[216:217], v[102:103], v[228:231]
	v_cvt_scalef32_pk_bf16_fp8 v220, v149, 1.0
	v_cvt_scalef32_pk_bf16_fp8 v221, v149, 1.0 op_sel:[1,0,0]
	v_cndmask_b32_e64 v191, v232, v233, s[22:23]
	v_cndmask_b32_e64 v191, v191, v234, s[24:25]
	v_cndmask_b32_e64 v191, v191, v235, s[26:27]
	v_mfma_f32_4x4x4_16b_bf16 v[232:235], v[218:219], v[108:109], 0
	v_cvt_scalef32_pk_bf16_fp8 v222, v150, 1.0
	v_cvt_scalef32_pk_bf16_fp8 v223, v150, 1.0 op_sel:[1,0,0]
	v_mfma_f32_4x4x4_16b_bf16 v[232:235], v[220:221], v[110:111], v[232:235]
	v_cvt_scalef32_pk_bf16_fp8 v224, v151, 1.0
	v_cvt_scalef32_pk_bf16_fp8 v225, v151, 1.0 op_sel:[1,0,0]
	v_lshl_or_b32 v69, v69, 7, v209
	global_load_dwordx4 v[148:151], v69, s[6:7]
	v_mfma_f32_4x4x4_16b_bf16 v[232:235], v[222:223], v[100:101], v[232:235]
	v_cvt_scalef32_pk_bf16_fp8 v210, v152, 1.0
	v_cvt_scalef32_pk_bf16_fp8 v211, v152, 1.0 op_sel:[1,0,0]
	v_mfma_f32_4x4x4_16b_bf16 v[232:235], v[224:225], v[102:103], v[232:235]
	v_cvt_scalef32_pk_bf16_fp8 v212, v153, 1.0
	v_cvt_scalef32_pk_bf16_fp8 v213, v153, 1.0 op_sel:[1,0,0]
	v_cndmask_b32_e64 v192, v228, v229, s[22:23]
	v_cndmask_b32_e64 v192, v192, v230, s[24:25]
	v_cndmask_b32_e64 v192, v192, v231, s[26:27]
	v_mfma_f32_4x4x4_16b_bf16 v[228:231], v[210:211], v[108:109], 0
	v_cvt_scalef32_pk_bf16_fp8 v214, v154, 1.0
	v_cvt_scalef32_pk_bf16_fp8 v215, v154, 1.0 op_sel:[1,0,0]
	v_mfma_f32_4x4x4_16b_bf16 v[228:231], v[212:213], v[110:111], v[228:231]
	v_cvt_scalef32_pk_bf16_fp8 v216, v155, 1.0
	v_cvt_scalef32_pk_bf16_fp8 v217, v155, 1.0 op_sel:[1,0,0]
	v_lshl_or_b32 v70, v70, 7, v209
	global_load_dwordx4 v[152:155], v70, s[6:7]
	v_mfma_f32_4x4x4_16b_bf16 v[228:231], v[214:215], v[100:101], v[228:231]
	v_cvt_scalef32_pk_bf16_fp8 v218, v156, 1.0
	v_cvt_scalef32_pk_bf16_fp8 v219, v156, 1.0 op_sel:[1,0,0]
	v_mfma_f32_4x4x4_16b_bf16 v[228:231], v[216:217], v[102:103], v[228:231]
	v_cvt_scalef32_pk_bf16_fp8 v220, v157, 1.0
	v_cvt_scalef32_pk_bf16_fp8 v221, v157, 1.0 op_sel:[1,0,0]
	v_cndmask_b32_e64 v193, v232, v233, s[22:23]
	v_cndmask_b32_e64 v193, v193, v234, s[24:25]
	v_cndmask_b32_e64 v193, v193, v235, s[26:27]
	v_mfma_f32_4x4x4_16b_bf16 v[232:235], v[218:219], v[108:109], 0
	v_cvt_scalef32_pk_bf16_fp8 v222, v158, 1.0
	v_cvt_scalef32_pk_bf16_fp8 v223, v158, 1.0 op_sel:[1,0,0]
	v_mfma_f32_4x4x4_16b_bf16 v[232:235], v[220:221], v[110:111], v[232:235]
	v_cvt_scalef32_pk_bf16_fp8 v224, v159, 1.0
	v_cvt_scalef32_pk_bf16_fp8 v225, v159, 1.0 op_sel:[1,0,0]
	v_lshl_or_b32 v71, v71, 7, v209
	global_load_dwordx4 v[156:159], v71, s[6:7]
	v_mfma_f32_4x4x4_16b_bf16 v[232:235], v[222:223], v[100:101], v[232:235]
	v_cvt_scalef32_pk_bf16_fp8 v210, v160, 1.0
	v_cvt_scalef32_pk_bf16_fp8 v211, v160, 1.0 op_sel:[1,0,0]
	v_mfma_f32_4x4x4_16b_bf16 v[232:235], v[224:225], v[102:103], v[232:235]
	v_cvt_scalef32_pk_bf16_fp8 v212, v161, 1.0
	v_cvt_scalef32_pk_bf16_fp8 v213, v161, 1.0 op_sel:[1,0,0]
	v_cndmask_b32_e64 v194, v228, v229, s[22:23]
	v_cndmask_b32_e64 v194, v194, v230, s[24:25]
	v_cndmask_b32_e64 v194, v194, v231, s[26:27]
	v_mfma_f32_4x4x4_16b_bf16 v[228:231], v[210:211], v[108:109], 0
	v_cvt_scalef32_pk_bf16_fp8 v214, v162, 1.0
	v_cvt_scalef32_pk_bf16_fp8 v215, v162, 1.0 op_sel:[1,0,0]
	v_mfma_f32_4x4x4_16b_bf16 v[228:231], v[212:213], v[110:111], v[228:231]
	v_cvt_scalef32_pk_bf16_fp8 v216, v163, 1.0
	v_cvt_scalef32_pk_bf16_fp8 v217, v163, 1.0 op_sel:[1,0,0]
	v_lshl_or_b32 v64, v64, 7, v209
	global_load_dwordx4 v[160:163], v64, s[6:7]
	v_mfma_f32_4x4x4_16b_bf16 v[228:231], v[214:215], v[100:101], v[228:231]
	v_cvt_scalef32_pk_bf16_fp8 v218, v164, 1.0
	v_cvt_scalef32_pk_bf16_fp8 v219, v164, 1.0 op_sel:[1,0,0]
	v_mfma_f32_4x4x4_16b_bf16 v[228:231], v[216:217], v[102:103], v[228:231]
	v_cvt_scalef32_pk_bf16_fp8 v220, v165, 1.0
	v_cvt_scalef32_pk_bf16_fp8 v221, v165, 1.0 op_sel:[1,0,0]
	v_cndmask_b32_e64 v195, v232, v233, s[22:23]
	v_cndmask_b32_e64 v195, v195, v234, s[24:25]
	v_cndmask_b32_e64 v195, v195, v235, s[26:27]
	v_mfma_f32_4x4x4_16b_bf16 v[232:235], v[218:219], v[108:109], 0
	v_cvt_scalef32_pk_bf16_fp8 v222, v166, 1.0
	v_cvt_scalef32_pk_bf16_fp8 v223, v166, 1.0 op_sel:[1,0,0]
	v_mfma_f32_4x4x4_16b_bf16 v[232:235], v[220:221], v[110:111], v[232:235]
	v_cvt_scalef32_pk_bf16_fp8 v224, v167, 1.0
	v_cvt_scalef32_pk_bf16_fp8 v225, v167, 1.0 op_sel:[1,0,0]
	v_lshl_or_b32 v65, v65, 7, v209
	global_load_dwordx4 v[164:167], v65, s[6:7]
	v_mfma_f32_4x4x4_16b_bf16 v[232:235], v[222:223], v[100:101], v[232:235]
	v_cvt_scalef32_pk_bf16_fp8 v210, v168, 1.0
	v_cvt_scalef32_pk_bf16_fp8 v211, v168, 1.0 op_sel:[1,0,0]
	v_mfma_f32_4x4x4_16b_bf16 v[232:235], v[224:225], v[102:103], v[232:235]
	v_cvt_scalef32_pk_bf16_fp8 v212, v169, 1.0
	v_cvt_scalef32_pk_bf16_fp8 v213, v169, 1.0 op_sel:[1,0,0]
	v_cndmask_b32_e64 v196, v228, v229, s[22:23]
	v_cndmask_b32_e64 v196, v196, v230, s[24:25]
	v_cndmask_b32_e64 v196, v196, v231, s[26:27]
	v_mfma_f32_4x4x4_16b_bf16 v[228:231], v[210:211], v[108:109], 0
	v_cvt_scalef32_pk_bf16_fp8 v214, v170, 1.0
	v_cvt_scalef32_pk_bf16_fp8 v215, v170, 1.0 op_sel:[1,0,0]
	v_mfma_f32_4x4x4_16b_bf16 v[228:231], v[212:213], v[110:111], v[228:231]
	v_cvt_scalef32_pk_bf16_fp8 v216, v171, 1.0
	v_cvt_scalef32_pk_bf16_fp8 v217, v171, 1.0 op_sel:[1,0,0]
	v_lshl_or_b32 v66, v66, 7, v209
	global_load_dwordx4 v[168:171], v66, s[6:7]
	v_mfma_f32_4x4x4_16b_bf16 v[228:231], v[214:215], v[100:101], v[228:231]
	v_cvt_scalef32_pk_bf16_fp8 v218, v172, 1.0
	v_cvt_scalef32_pk_bf16_fp8 v219, v172, 1.0 op_sel:[1,0,0]
	v_mfma_f32_4x4x4_16b_bf16 v[228:231], v[216:217], v[102:103], v[228:231]
	v_cvt_scalef32_pk_bf16_fp8 v220, v173, 1.0
	v_cvt_scalef32_pk_bf16_fp8 v221, v173, 1.0 op_sel:[1,0,0]
	v_cndmask_b32_e64 v197, v232, v233, s[22:23]
	v_cndmask_b32_e64 v197, v197, v234, s[24:25]
	v_cndmask_b32_e64 v197, v197, v235, s[26:27]
	v_mfma_f32_4x4x4_16b_bf16 v[232:235], v[218:219], v[108:109], 0
	v_cvt_scalef32_pk_bf16_fp8 v222, v174, 1.0
	v_cvt_scalef32_pk_bf16_fp8 v223, v174, 1.0 op_sel:[1,0,0]
	v_mfma_f32_4x4x4_16b_bf16 v[232:235], v[220:221], v[110:111], v[232:235]
	v_cvt_scalef32_pk_bf16_fp8 v224, v175, 1.0
	v_cvt_scalef32_pk_bf16_fp8 v225, v175, 1.0 op_sel:[1,0,0]
	v_lshl_or_b32 v67, v67, 7, v209
	global_load_dwordx4 v[172:175], v67, s[6:7]
	v_mfma_f32_4x4x4_16b_bf16 v[232:235], v[222:223], v[100:101], v[232:235]
	s_nop 1
	v_mfma_f32_4x4x4_16b_bf16 v[232:235], v[224:225], v[102:103], v[232:235]
	v_cndmask_b32_e64 v198, v228, v229, s[22:23]
	v_cndmask_b32_e64 v198, v198, v230, s[24:25]
	v_cndmask_b32_e64 v198, v198, v231, s[26:27]
	s_nop 4
	v_cndmask_b32_e64 v199, v232, v233, s[22:23]
	v_cndmask_b32_e64 v199, v199, v234, s[24:25]
	v_cndmask_b32_e64 v199, v199, v235, s[26:27]
	v_cndmask_b32_e64 v200, v184, v192, s[4:5]
	v_cndmask_b32_e64 v201, v192, v184, s[4:5]
	v_cndmask_b32_e64 v202, v185, v193, s[4:5]
	v_cndmask_b32_e64 v203, v193, v185, s[4:5]
	v_cndmask_b32_e64 v204, v186, v194, s[4:5]
	v_cndmask_b32_e64 v205, v194, v186, s[4:5]
	v_cndmask_b32_e64 v236, v187, v195, s[4:5]
	v_cndmask_b32_e64 v237, v195, v187, s[4:5]
	v_cndmask_b32_e64 v238, v188, v196, s[4:5]
	v_cndmask_b32_e64 v239, v196, v188, s[4:5]
	v_cndmask_b32_e64 v240, v189, v197, s[4:5]
	v_cndmask_b32_e64 v241, v197, v189, s[4:5]
	v_cndmask_b32_e64 v242, v190, v198, s[4:5]
	v_cndmask_b32_e64 v243, v198, v190, s[4:5]
	v_cndmask_b32_e64 v244, v191, v199, s[4:5]
	v_cndmask_b32_e64 v245, v199, v191, s[4:5]
	v_add_f32_dpp v246, v200, v201 row_half_mirror row_mask:0xf bank_mask:0xf
	v_add_f32_dpp v247, v202, v203 row_half_mirror row_mask:0xf bank_mask:0xf
	v_add_f32_dpp v248, v204, v205 row_half_mirror row_mask:0xf bank_mask:0xf
	v_add_f32_dpp v249, v236, v237 row_half_mirror row_mask:0xf bank_mask:0xf
	v_add_f32_dpp v226, v238, v239 row_half_mirror row_mask:0xf bank_mask:0xf
	v_add_f32_dpp v227, v240, v241 row_half_mirror row_mask:0xf bank_mask:0xf
	v_add_f32_dpp v210, v242, v243 row_half_mirror row_mask:0xf bank_mask:0xf
	v_add_f32_dpp v211, v244, v245 row_half_mirror row_mask:0xf bank_mask:0xf
	v_cndmask_b32_e64 v200, v246, v226, s[2:3]
	v_cndmask_b32_e64 v201, v226, v246, s[2:3]
	v_cndmask_b32_e64 v202, v247, v227, s[2:3]
	v_cndmask_b32_e64 v203, v227, v247, s[2:3]
	v_cndmask_b32_e64 v204, v248, v210, s[2:3]
	v_cndmask_b32_e64 v205, v210, v248, s[2:3]
	v_cndmask_b32_e64 v236, v249, v211, s[2:3]
	v_cndmask_b32_e64 v237, v211, v249, s[2:3]
	v_add_f32_dpp v212, v200, v201 quad_perm:[2,3,0,1] row_mask:0xf bank_mask:0xf
	v_add_f32_dpp v213, v202, v203 quad_perm:[2,3,0,1] row_mask:0xf bank_mask:0xf
	v_add_f32_dpp v214, v204, v205 quad_perm:[2,3,0,1] row_mask:0xf bank_mask:0xf
	v_add_f32_dpp v215, v236, v237 quad_perm:[2,3,0,1] row_mask:0xf bank_mask:0xf
	v_cndmask_b32_e64 v200, v212, v214, s[0:1]
	v_cndmask_b32_e64 v201, v214, v212, s[0:1]
	v_cndmask_b32_e64 v202, v213, v215, s[0:1]
	v_cndmask_b32_e64 v203, v215, v213, s[0:1]
	s_nop 1
	v_add_f32_dpp v216, v200, v201 quad_perm:[1,0,3,2] row_mask:0xf bank_mask:0xf
	v_add_f32_dpp v217, v202, v203 quad_perm:[1,0,3,2] row_mask:0xf bank_mask:0xf
	s_ashr_i32 s11, s10, 31
	s_lshl_b64 s[10:11], s[10:11], 8
	v_cvt_pk_bf16_f32 v186, v216, v217
	v_lshl_add_u64 v[184:185], v[178:179], 0, s[10:11]
	global_store_dword v[184:185], v186, off
	s_add_u32 s20, s12, 0x300
	s_lshl_b32 s20, s20, 11
	v_lshl_add_u64 v[108:109], v[182:183], 0, s[20:21]
	global_load_dwordx4 v[100:103], v[108:109], off offset:16
	s_nop 0
	global_load_dwordx4 v[108:111], v[108:109], off
	s_add_u32 s20, s12, 0x500
	s_lshl_b32 s20, s20, 9
	v_lshl_add_u64 v[80:81], v[180:181], 0, s[20:21]
	global_load_dwordx4 v[64:67], v[80:81], off offset:48
	global_load_dwordx4 v[68:71], v[80:81], off offset:32
	global_load_dwordx4 v[72:75], v[80:81], off offset:16
	s_nop 0
	global_load_dwordx4 v[80:83], v[80:81], off
	s_add_u32 s12, s12, 0x200
	s_mov_b32 s13, 61
; #define PD_E(t, E) do { const char* eb_ = eiu + (size_t)(t) * 512; _Pragma("unroll") for (int q = 0; q < 4; ++q) E[q] = *(const i32x4_t*)(eb_ + (eio + 16u * q)); } while (0)
; #define PD_H(t, H) do { const char* hb_ = h2u + (size_t)(t) * 2048; H[0] = *(const u32x4*)(hb_ + h2o); H[1] = *(const u32x4*)(hb_ + (h2o + 16u)); } while (0)
; #define PD_TAB(E, W) do { _Pragma("unroll") for (int q = 0; q < 16; ++q) W[q] = *(const u32x4*)(tabu + ((unsigned)E[q >> 2][q & 3] * 128u + tabo)); } while (0)
; DI void phase_peerdown(const Params& p, int bid, int nb) {
;     ...
;   for (;;) {
;     if (t1 < T_) PD_TAB(eB, wB);
;     const int t2 = t1 + nw; if (t2 < T_) PD_E(t2, eA);
;     PD_MATH(t, wA, hA);
;     if (t1 >= T_) break;
;     if (t2 < T_) { PD_H(t2, hA); PD_TAB(eA, wA); }
;     const int t3 = t2 + nw; if (t3 < T_) PD_E(t3, eB);
;     PD_MATH(t1, wB, hB);
.Lpd2_loop:
	s_mov_b32 s14, s12
	s_waitcnt vmcnt(23)
	v_cvt_scalef32_pk_bf16_fp8 v210, v24, 1.0
	v_cvt_scalef32_pk_bf16_fp8 v211, v24, 1.0 op_sel:[1,0,0]
	v_cvt_scalef32_pk_bf16_fp8 v212, v25, 1.0
	v_cvt_scalef32_pk_bf16_fp8 v213, v25, 1.0 op_sel:[1,0,0]
	v_mfma_f32_4x4x4_16b_bf16 v[228:231], v[210:211], v[20:21], 0
	v_cvt_scalef32_pk_bf16_fp8 v214, v26, 1.0
	v_cvt_scalef32_pk_bf16_fp8 v215, v26, 1.0 op_sel:[1,0,0]
	v_mfma_f32_4x4x4_16b_bf16 v[228:231], v[212:213], v[22:23], v[228:231]
	v_cvt_scalef32_pk_bf16_fp8 v216, v27, 1.0
	v_cvt_scalef32_pk_bf16_fp8 v217, v27, 1.0 op_sel:[1,0,0]
	v_lshl_or_b32 v0, v0, 7, v209
	global_load_dwordx4 v[24:27], v0, s[6:7]
	v_mfma_f32_4x4x4_16b_bf16 v[228:231], v[214:215], v[16:17], v[228:231]
	v_cvt_scalef32_pk_bf16_fp8 v218, v28, 1.0
	v_cvt_scalef32_pk_bf16_fp8 v219, v28, 1.0 op_sel:[1,0,0]
	v_mfma_f32_4x4x4_16b_bf16 v[228:231], v[216:217], v[18:19], v[228:231]
	v_cvt_scalef32_pk_bf16_fp8 v220, v29, 1.0
	v_cvt_scalef32_pk_bf16_fp8 v221, v29, 1.0 op_sel:[1,0,0]
	v_mfma_f32_4x4x4_16b_bf16 v[232:235], v[218:219], v[20:21], 0
	v_cvt_scalef32_pk_bf16_fp8 v222, v30, 1.0
	v_cvt_scalef32_pk_bf16_fp8 v223, v30, 1.0 op_sel:[1,0,0]
	v_mfma_f32_4x4x4_16b_bf16 v[232:235], v[220:221], v[22:23], v[232:235]
	v_cvt_scalef32_pk_bf16_fp8 v224, v31, 1.0
	v_cvt_scalef32_pk_bf16_fp8 v225, v31, 1.0 op_sel:[1,0,0]
	v_lshl_or_b32 v1, v1, 7, v209
	global_load_dwordx4 v[28:31], v1, s[6:7]
	v_mfma_f32_4x4x4_16b_bf16 v[232:235], v[222:223], v[16:17], v[232:235]
	v_cvt_scalef32_pk_bf16_fp8 v210, v32, 1.0
	v_cvt_scalef32_pk_bf16_fp8 v211, v32, 1.0 op_sel:[1,0,0]
	v_mfma_f32_4x4x4_16b_bf16 v[232:235], v[224:225], v[18:19], v[232:235]
	v_cvt_scalef32_pk_bf16_fp8 v212, v33, 1.0
	v_cvt_scalef32_pk_bf16_fp8 v213, v33, 1.0 op_sel:[1,0,0]
	v_cndmask_b32_e64 v184, v228, v229, s[22:23]
	v_cndmask_b32_e64 v184, v184, v230, s[24:25]
	v_cndmask_b32_e64 v184, v184, v231, s[26:27]
	v_mfma_f32_4x4x4_16b_bf16 v[228:231], v[210:211], v[20:21], 0
	v_cvt_scalef32_pk_bf16_fp8 v214, v34, 1.0
	v_cvt_scalef32_pk_bf16_fp8 v215, v34, 1.0 op_sel:[1,0,0]
	v_mfma_f32_4x4x4_16b_bf16 v[228:231], v[212:213], v[22:23], v[228:231]
	v_cvt_scalef32_pk_bf16_fp8 v216, v35, 1.0
	v_cvt_scalef32_pk_bf16_fp8 v217, v35, 1.0 op_sel:[1,0,0]
	v_lshl_or_b32 v2, v2, 7, v209
	global_load_dwordx4 v[32:35], v2, s[6:7]
	v_mfma_f32_4x4x4_16b_bf16 v[228:231], v[214:215], v[16:17], v[228:231]
	v_cvt_scalef32_pk_bf16_fp8 v218, v36, 1.0
	v_cvt_scalef32_pk_bf16_fp8 v219, v36, 1.0 op_sel:[1,0,0]
	v_mfma_f32_4x4x4_16b_bf16 v[228:231], v[216:217], v[18:19], v[228:231]
	v_cvt_scalef32_pk_bf16_fp8 v220, v37, 1.0
	v_cvt_scalef32_pk_bf16_fp8 v221, v37, 1.0 op_sel:[1,0,0]
	v_cndmask_b32_e64 v185, v232, v233, s[22:23]
	v_cndmask_b32_e64 v185, v185, v234, s[24:25]
	v_cndmask_b32_e64 v185, v185, v235, s[26:27]
	v_mfma_f32_4x4x4_16b_bf16 v[232:235], v[218:219], v[20:21], 0
	v_cvt_scalef32_pk_bf16_fp8 v222, v38, 1.0
	v_cvt_scalef32_pk_bf16_fp8 v223, v38, 1.0 op_sel:[1,0,0]
	v_mfma_f32_4x4x4_16b_bf16 v[232:235], v[220:221], v[22:23], v[232:235]
	v_cvt_scalef32_pk_bf16_fp8 v224, v39, 1.0
	v_cvt_scalef32_pk_bf16_fp8 v225, v39, 1.0 op_sel:[1,0,0]
	v_lshl_or_b32 v3, v3, 7, v209
	global_load_dwordx4 v[36:39], v3, s[6:7]
	v_mfma_f32_4x4x4_16b_bf16 v[232:235], v[222:223], v[16:17], v[232:235]
	v_cvt_scalef32_pk_bf16_fp8 v210, v40, 1.0
	v_cvt_scalef32_pk_bf16_fp8 v211, v40, 1.0 op_sel:[1,0,0]
	v_mfma_f32_4x4x4_16b_bf16 v[232:235], v[224:225], v[18:19], v[232:235]
	v_cvt_scalef32_pk_bf16_fp8 v212, v41, 1.0
	v_cvt_scalef32_pk_bf16_fp8 v213, v41, 1.0 op_sel:[1,0,0]
	v_cndmask_b32_e64 v186, v228, v229, s[22:23]
	v_cndmask_b32_e64 v186, v186, v230, s[24:25]
	v_cndmask_b32_e64 v186, v186, v231, s[26:27]
	v_mfma_f32_4x4x4_16b_bf16 v[228:231], v[210:211], v[20:21], 0
	v_cvt_scalef32_pk_bf16_fp8 v214, v42, 1.0
	v_cvt_scalef32_pk_bf16_fp8 v215, v42, 1.0 op_sel:[1,0,0]
	v_mfma_f32_4x4x4_16b_bf16 v[228:231], v[212:213], v[22:23], v[228:231]
	v_cvt_scalef32_pk_bf16_fp8 v216, v43, 1.0
	v_cvt_scalef32_pk_bf16_fp8 v217, v43, 1.0 op_sel:[1,0,0]
	v_lshl_or_b32 v4, v4, 7, v209
	global_load_dwordx4 v[40:43], v4, s[6:7]
	v_mfma_f32_4x4x4_16b_bf16 v[228:231], v[214:215], v[16:17], v[228:231]
	v_cvt_scalef32_pk_bf16_fp8 v218, v44, 1.0
	v_cvt_scalef32_pk_bf16_fp8 v219, v44, 1.0 op_sel:[1,0,0]
	v_mfma_f32_4x4x4_16b_bf16 v[228:231], v[216:217], v[18:19], v[228:231]
	v_cvt_scalef32_pk_bf16_fp8 v220, v45, 1.0
	v_cvt_scalef32_pk_bf16_fp8 v221, v45, 1.0 op_sel:[1,0,0]
	v_cndmask_b32_e64 v187, v232, v233, s[22:23]
	v_cndmask_b32_e64 v187, v187, v234, s[24:25]
	v_cndmask_b32_e64 v187, v187, v235, s[26:27]
	v_mfma_f32_4x4x4_16b_bf16 v[232:235], v[218:219], v[20:21], 0
	v_cvt_scalef32_pk_bf16_fp8 v222, v46, 1.0
	v_cvt_scalef32_pk_bf16_fp8 v223, v46, 1.0 op_sel:[1,0,0]
	v_mfma_f32_4x4x4_16b_bf16 v[232:235], v[220:221], v[22:23], v[232:235]
	v_cvt_scalef32_pk_bf16_fp8 v224, v47, 1.0
	v_cvt_scalef32_pk_bf16_fp8 v225, v47, 1.0 op_sel:[1,0,0]
	v_lshl_or_b32 v5, v5, 7, v209
	global_load_dwordx4 v[44:47], v5, s[6:7]
	v_mfma_f32_4x4x4_16b_bf16 v[232:235], v[222:223], v[16:17], v[232:235]
	v_cvt_scalef32_pk_bf16_fp8 v210, v48, 1.0
	v_cvt_scalef32_pk_bf16_fp8 v211, v48, 1.0 op_sel:[1,0,0]
	v_mfma_f32_4x4x4_16b_bf16 v[232:235], v[224:225], v[18:19], v[232:235]
	v_cvt_scalef32_pk_bf16_fp8 v212, v49, 1.0
	v_cvt_scalef32_pk_bf16_fp8 v213, v49, 1.0 op_sel:[1,0,0]
	v_cndmask_b32_e64 v188, v228, v229, s[22:23]
	v_cndmask_b32_e64 v188, v188, v230, s[24:25]
	v_cndmask_b32_e64 v188, v188, v231, s[26:27]
	v_mfma_f32_4x4x4_16b_bf16 v[228:231], v[210:211], v[20:21], 0
	v_cvt_scalef32_pk_bf16_fp8 v214, v50, 1.0
	v_cvt_scalef32_pk_bf16_fp8 v215, v50, 1.0 op_sel:[1,0,0]
; #define PD_TAB(E, W) do { _Pragma("unroll") for (int q = 0; q < 16; ++q) W[q] = *(const u32x4*)(tabu + ((unsigned)E[q >> 2][q & 3] * 128u + tabo)); } while (0)
; DI void phase_peerdown(const Params& p, int bid, int nb) {
;     ...
;     if (t1 < T_) PD_TAB(eB, wB);
	v_mfma_f32_4x4x4_16b_bf16 v[228:231], v[212:213], v[22:23], v[228:231]
	v_cvt_scalef32_pk_bf16_fp8 v216, v51, 1.0
	v_cvt_scalef32_pk_bf16_fp8 v217, v51, 1.0 op_sel:[1,0,0]
	v_lshl_or_b32 v6, v6, 7, v209
	global_load_dwordx4 v[48:51], v6, s[6:7]
	v_mfma_f32_4x4x4_16b_bf16 v[228:231], v[214:215], v[16:17], v[228:231]
	v_cvt_scalef32_pk_bf16_fp8 v218, v52, 1.0
	v_cvt_scalef32_pk_bf16_fp8 v219, v52, 1.0 op_sel:[1,0,0]
	v_mfma_f32_4x4x4_16b_bf16 v[228:231], v[216:217], v[18:19], v[228:231]
	v_cvt_scalef32_pk_bf16_fp8 v220, v53, 1.0
	v_cvt_scalef32_pk_bf16_fp8 v221, v53, 1.0 op_sel:[1,0,0]
	v_cndmask_b32_e64 v189, v232, v233, s[22:23]
	v_cndmask_b32_e64 v189, v189, v234, s[24:25]
	v_cndmask_b32_e64 v189, v189, v235, s[26:27]
	v_mfma_f32_4x4x4_16b_bf16 v[232:235], v[218:219], v[20:21], 0
	v_cvt_scalef32_pk_bf16_fp8 v222, v54, 1.0
	v_cvt_scalef32_pk_bf16_fp8 v223, v54, 1.0 op_sel:[1,0,0]
	v_mfma_f32_4x4x4_16b_bf16 v[232:235], v[220:221], v[22:23], v[232:235]
	v_cvt_scalef32_pk_bf16_fp8 v224, v55, 1.0
	v_cvt_scalef32_pk_bf16_fp8 v225, v55, 1.0 op_sel:[1,0,0]
	v_lshl_or_b32 v7, v7, 7, v209
	global_load_dwordx4 v[52:55], v7, s[6:7]
	v_mfma_f32_4x4x4_16b_bf16 v[232:235], v[222:223], v[16:17], v[232:235]
	v_cvt_scalef32_pk_bf16_fp8 v210, v56, 1.0
	v_cvt_scalef32_pk_bf16_fp8 v211, v56, 1.0 op_sel:[1,0,0]
	v_mfma_f32_4x4x4_16b_bf16 v[232:235], v[224:225], v[18:19], v[232:235]
	v_cvt_scalef32_pk_bf16_fp8 v212, v57, 1.0
	v_cvt_scalef32_pk_bf16_fp8 v213, v57, 1.0 op_sel:[1,0,0]
	v_cndmask_b32_e64 v190, v228, v229, s[22:23]
	v_cndmask_b32_e64 v190, v190, v230, s[24:25]
	v_cndmask_b32_e64 v190, v190, v231, s[26:27]
	v_mfma_f32_4x4x4_16b_bf16 v[228:231], v[210:211], v[20:21], 0
	v_cvt_scalef32_pk_bf16_fp8 v214, v58, 1.0
	v_cvt_scalef32_pk_bf16_fp8 v215, v58, 1.0 op_sel:[1,0,0]
	v_mfma_f32_4x4x4_16b_bf16 v[228:231], v[212:213], v[22:23], v[228:231]
	v_cvt_scalef32_pk_bf16_fp8 v216, v59, 1.0
	v_cvt_scalef32_pk_bf16_fp8 v217, v59, 1.0 op_sel:[1,0,0]
	v_lshl_or_b32 v8, v8, 7, v209
	global_load_dwordx4 v[56:59], v8, s[6:7]
	v_mfma_f32_4x4x4_16b_bf16 v[228:231], v[214:215], v[16:17], v[228:231]
	v_cvt_scalef32_pk_bf16_fp8 v218, v60, 1.0
	v_cvt_scalef32_pk_bf16_fp8 v219, v60, 1.0 op_sel:[1,0,0]
	v_mfma_f32_4x4x4_16b_bf16 v[228:231], v[216:217], v[18:19], v[228:231]
	v_cvt_scalef32_pk_bf16_fp8 v220, v61, 1.0
	v_cvt_scalef32_pk_bf16_fp8 v221, v61, 1.0 op_sel:[1,0,0]
	v_cndmask_b32_e64 v191, v232, v233, s[22:23]
	v_cndmask_b32_e64 v191, v191, v234, s[24:25]
	v_cndmask_b32_e64 v191, v191, v235, s[26:27]
	v_mfma_f32_4x4x4_16b_bf16 v[232:235], v[218:219], v[20:21], 0
	v_cvt_scalef32_pk_bf16_fp8 v222, v62, 1.0
	v_cvt_scalef32_pk_bf16_fp8 v223, v62, 1.0 op_sel:[1,0,0]
	v_mfma_f32_4x4x4_16b_bf16 v[232:235], v[220:221], v[22:23], v[232:235]
	v_cvt_scalef32_pk_bf16_fp8 v224, v63, 1.0
	v_cvt_scalef32_pk_bf16_fp8 v225, v63, 1.0 op_sel:[1,0,0]
	v_lshl_or_b32 v9, v9, 7, v209
	global_load_dwordx4 v[60:63], v9, s[6:7]
	v_mfma_f32_4x4x4_16b_bf16 v[232:235], v[222:223], v[16:17], v[232:235]
	v_cvt_scalef32_pk_bf16_fp8 v210, v76, 1.0
	v_cvt_scalef32_pk_bf16_fp8 v211, v76, 1.0 op_sel:[1,0,0]
	v_mfma_f32_4x4x4_16b_bf16 v[232:235], v[224:225], v[18:19], v[232:235]
	v_cvt_scalef32_pk_bf16_fp8 v212, v77, 1.0
	v_cvt_scalef32_pk_bf16_fp8 v213, v77, 1.0 op_sel:[1,0,0]
	v_cndmask_b32_e64 v192, v228, v229, s[22:23]
	v_cndmask_b32_e64 v192, v192, v230, s[24:25]
	v_cndmask_b32_e64 v192, v192, v231, s[26:27]
	v_mfma_f32_4x4x4_16b_bf16 v[228:231], v[210:211], v[20:21], 0
	v_cvt_scalef32_pk_bf16_fp8 v214, v78, 1.0
	v_cvt_scalef32_pk_bf16_fp8 v215, v78, 1.0 op_sel:[1,0,0]
	v_mfma_f32_4x4x4_16b_bf16 v[228:231], v[212:213], v[22:23], v[228:231]
	v_cvt_scalef32_pk_bf16_fp8 v216, v79, 1.0
	v_cvt_scalef32_pk_bf16_fp8 v217, v79, 1.0 op_sel:[1,0,0]
	v_lshl_or_b32 v10, v10, 7, v209
	global_load_dwordx4 v[76:79], v10, s[6:7]
	v_mfma_f32_4x4x4_16b_bf16 v[228:231], v[214:215], v[16:17], v[228:231]
	v_cvt_scalef32_pk_bf16_fp8 v218, v84, 1.0
	v_cvt_scalef32_pk_bf16_fp8 v219, v84, 1.0 op_sel:[1,0,0]
	v_mfma_f32_4x4x4_16b_bf16 v[228:231], v[216:217], v[18:19], v[228:231]
	v_cvt_scalef32_pk_bf16_fp8 v220, v85, 1.0
	v_cvt_scalef32_pk_bf16_fp8 v221, v85, 1.0 op_sel:[1,0,0]
	v_cndmask_b32_e64 v193, v232, v233, s[22:23]
	v_cndmask_b32_e64 v193, v193, v234, s[24:25]
	v_cndmask_b32_e64 v193, v193, v235, s[26:27]
	v_mfma_f32_4x4x4_16b_bf16 v[232:235], v[218:219], v[20:21], 0
	v_cvt_scalef32_pk_bf16_fp8 v222, v86, 1.0
	v_cvt_scalef32_pk_bf16_fp8 v223, v86, 1.0 op_sel:[1,0,0]
	v_mfma_f32_4x4x4_16b_bf16 v[232:235], v[220:221], v[22:23], v[232:235]
	v_cvt_scalef32_pk_bf16_fp8 v224, v87, 1.0
	v_cvt_scalef32_pk_bf16_fp8 v225, v87, 1.0 op_sel:[1,0,0]
	v_lshl_or_b32 v11, v11, 7, v209
	global_load_dwordx4 v[84:87], v11, s[6:7]
	v_mfma_f32_4x4x4_16b_bf16 v[232:235], v[222:223], v[16:17], v[232:235]
	v_cvt_scalef32_pk_bf16_fp8 v210, v88, 1.0
	v_cvt_scalef32_pk_bf16_fp8 v211, v88, 1.0 op_sel:[1,0,0]
	v_mfma_f32_4x4x4_16b_bf16 v[232:235], v[224:225], v[18:19], v[232:235]
	v_cvt_scalef32_pk_bf16_fp8 v212, v89, 1.0
	v_cvt_scalef32_pk_bf16_fp8 v213, v89, 1.0 op_sel:[1,0,0]
	v_cndmask_b32_e64 v194, v228, v229, s[22:23]
	v_cndmask_b32_e64 v194, v194, v230, s[24:25]
	v_cndmask_b32_e64 v194, v194, v231, s[26:27]
	v_mfma_f32_4x4x4_16b_bf16 v[228:231], v[210:211], v[20:21], 0
	v_cvt_scalef32_pk_bf16_fp8 v214, v90, 1.0
	v_cvt_scalef32_pk_bf16_fp8 v215, v90, 1.0 op_sel:[1,0,0]
	v_mfma_f32_4x4x4_16b_bf16 v[228:231], v[212:213], v[22:23], v[228:231]
	v_cvt_scalef32_pk_bf16_fp8 v216, v91, 1.0
	v_cvt_scalef32_pk_bf16_fp8 v217, v91, 1.0 op_sel:[1,0,0]
	v_lshl_or_b32 v12, v12, 7, v209
	global_load_dwordx4 v[88:91], v12, s[6:7]
; #define PD_H(t, H) do { const char* hb_ = h2u + (size_t)(t) * 2048; H[0] = *(const u32x4*)(hb_ + h2o); H[1] = *(const u32x4*)(hb_ + (h2o + 16u)); } while (0)
; #define PD_TAB(E, W) do { _Pragma("unroll") for (int q = 0; q < 16; ++q) W[q] = *(const u32x4*)(tabu + ((unsigned)E[q >> 2][q & 3] * 128u + tabo)); } while (0)
; DI void phase_peerdown(const Params& p, int bid, int nb) {
;     ...
;     if (t2 < T_) { PD_H(t2, hA); PD_TAB(eA, wA); }
	v_mfma_f32_4x4x4_16b_bf16 v[228:231], v[214:215], v[16:17], v[228:231]
	v_cvt_scalef32_pk_bf16_fp8 v218, v92, 1.0
	v_cvt_scalef32_pk_bf16_fp8 v219, v92, 1.0 op_sel:[1,0,0]
	v_mfma_f32_4x4x4_16b_bf16 v[228:231], v[216:217], v[18:19], v[228:231]
	v_cvt_scalef32_pk_bf16_fp8 v220, v93, 1.0
	v_cvt_scalef32_pk_bf16_fp8 v221, v93, 1.0 op_sel:[1,0,0]
	v_cndmask_b32_e64 v195, v232, v233, s[22:23]
	v_cndmask_b32_e64 v195, v195, v234, s[24:25]
	v_cndmask_b32_e64 v195, v195, v235, s[26:27]
	v_mfma_f32_4x4x4_16b_bf16 v[232:235], v[218:219], v[20:21], 0
	v_cvt_scalef32_pk_bf16_fp8 v222, v94, 1.0
	v_cvt_scalef32_pk_bf16_fp8 v223, v94, 1.0 op_sel:[1,0,0]
	v_mfma_f32_4x4x4_16b_bf16 v[232:235], v[220:221], v[22:23], v[232:235]
	v_cvt_scalef32_pk_bf16_fp8 v224, v95, 1.0
	v_cvt_scalef32_pk_bf16_fp8 v225, v95, 1.0 op_sel:[1,0,0]
	v_lshl_or_b32 v13, v13, 7, v209
	global_load_dwordx4 v[92:95], v13, s[6:7]
	v_mfma_f32_4x4x4_16b_bf16 v[232:235], v[222:223], v[16:17], v[232:235]
	v_cvt_scalef32_pk_bf16_fp8 v210, v96, 1.0
	v_cvt_scalef32_pk_bf16_fp8 v211, v96, 1.0 op_sel:[1,0,0]
	v_mfma_f32_4x4x4_16b_bf16 v[232:235], v[224:225], v[18:19], v[232:235]
	v_cvt_scalef32_pk_bf16_fp8 v212, v97, 1.0
	v_cvt_scalef32_pk_bf16_fp8 v213, v97, 1.0 op_sel:[1,0,0]
	v_cndmask_b32_e64 v196, v228, v229, s[22:23]
	v_cndmask_b32_e64 v196, v196, v230, s[24:25]
	v_cndmask_b32_e64 v196, v196, v231, s[26:27]
	v_mfma_f32_4x4x4_16b_bf16 v[228:231], v[210:211], v[20:21], 0
	v_cvt_scalef32_pk_bf16_fp8 v214, v98, 1.0
	v_cvt_scalef32_pk_bf16_fp8 v215, v98, 1.0 op_sel:[1,0,0]
	v_mfma_f32_4x4x4_16b_bf16 v[228:231], v[212:213], v[22:23], v[228:231]
	v_cvt_scalef32_pk_bf16_fp8 v216, v99, 1.0
	v_cvt_scalef32_pk_bf16_fp8 v217, v99, 1.0 op_sel:[1,0,0]
	v_lshl_or_b32 v14, v14, 7, v209
	global_load_dwordx4 v[96:99], v14, s[6:7]
	v_mfma_f32_4x4x4_16b_bf16 v[228:231], v[214:215], v[16:17], v[228:231]
	v_cvt_scalef32_pk_bf16_fp8 v218, v104, 1.0
	v_cvt_scalef32_pk_bf16_fp8 v219, v104, 1.0 op_sel:[1,0,0]
	v_mfma_f32_4x4x4_16b_bf16 v[228:231], v[216:217], v[18:19], v[228:231]
	v_cvt_scalef32_pk_bf16_fp8 v220, v105, 1.0
	v_cvt_scalef32_pk_bf16_fp8 v221, v105, 1.0 op_sel:[1,0,0]
	v_cndmask_b32_e64 v197, v232, v233, s[22:23]
	v_cndmask_b32_e64 v197, v197, v234, s[24:25]
	v_cndmask_b32_e64 v197, v197, v235, s[26:27]
	v_mfma_f32_4x4x4_16b_bf16 v[232:235], v[218:219], v[20:21], 0
	v_cvt_scalef32_pk_bf16_fp8 v222, v106, 1.0
	v_cvt_scalef32_pk_bf16_fp8 v223, v106, 1.0 op_sel:[1,0,0]
	v_mfma_f32_4x4x4_16b_bf16 v[232:235], v[220:221], v[22:23], v[232:235]
	v_cvt_scalef32_pk_bf16_fp8 v224, v107, 1.0
	v_cvt_scalef32_pk_bf16_fp8 v225, v107, 1.0 op_sel:[1,0,0]
	v_lshl_or_b32 v15, v15, 7, v209
	global_load_dwordx4 v[104:107], v15, s[6:7]
	v_mfma_f32_4x4x4_16b_bf16 v[232:235], v[222:223], v[16:17], v[232:235]
	s_nop 1
	v_mfma_f32_4x4x4_16b_bf16 v[232:235], v[224:225], v[18:19], v[232:235]
	v_cndmask_b32_e64 v198, v228, v229, s[22:23]
	v_cndmask_b32_e64 v198, v198, v230, s[24:25]
	v_cndmask_b32_e64 v198, v198, v231, s[26:27]
	s_nop 4
	v_cndmask_b32_e64 v199, v232, v233, s[22:23]
	v_cndmask_b32_e64 v199, v199, v234, s[24:25]
	v_cndmask_b32_e64 v199, v199, v235, s[26:27]
	v_cndmask_b32_e64 v200, v184, v192, s[4:5]
	v_cndmask_b32_e64 v201, v192, v184, s[4:5]
	v_cndmask_b32_e64 v202, v185, v193, s[4:5]
	v_cndmask_b32_e64 v203, v193, v185, s[4:5]
	v_cndmask_b32_e64 v204, v186, v194, s[4:5]
	v_cndmask_b32_e64 v205, v194, v186, s[4:5]
	v_cndmask_b32_e64 v236, v187, v195, s[4:5]
	v_cndmask_b32_e64 v237, v195, v187, s[4:5]
	v_cndmask_b32_e64 v238, v188, v196, s[4:5]
	v_cndmask_b32_e64 v239, v196, v188, s[4:5]
	v_cndmask_b32_e64 v240, v189, v197, s[4:5]
	v_cndmask_b32_e64 v241, v197, v189, s[4:5]
	v_cndmask_b32_e64 v242, v190, v198, s[4:5]
	v_cndmask_b32_e64 v243, v198, v190, s[4:5]
	v_cndmask_b32_e64 v244, v191, v199, s[4:5]
	v_cndmask_b32_e64 v245, v199, v191, s[4:5]
	v_add_f32_dpp v246, v200, v201 row_half_mirror row_mask:0xf bank_mask:0xf
	v_add_f32_dpp v247, v202, v203 row_half_mirror row_mask:0xf bank_mask:0xf
	v_add_f32_dpp v248, v204, v205 row_half_mirror row_mask:0xf bank_mask:0xf
	v_add_f32_dpp v249, v236, v237 row_half_mirror row_mask:0xf bank_mask:0xf
	v_add_f32_dpp v226, v238, v239 row_half_mirror row_mask:0xf bank_mask:0xf
	v_add_f32_dpp v227, v240, v241 row_half_mirror row_mask:0xf bank_mask:0xf
	v_add_f32_dpp v210, v242, v243 row_half_mirror row_mask:0xf bank_mask:0xf
	v_add_f32_dpp v211, v244, v245 row_half_mirror row_mask:0xf bank_mask:0xf
	v_cndmask_b32_e64 v200, v246, v226, s[2:3]
	v_cndmask_b32_e64 v201, v226, v246, s[2:3]
	v_cndmask_b32_e64 v202, v247, v227, s[2:3]
	v_cndmask_b32_e64 v203, v227, v247, s[2:3]
	v_cndmask_b32_e64 v204, v248, v210, s[2:3]
	v_cndmask_b32_e64 v205, v210, v248, s[2:3]
	v_cndmask_b32_e64 v236, v249, v211, s[2:3]
	v_cndmask_b32_e64 v237, v211, v249, s[2:3]
	v_add_f32_dpp v212, v200, v201 quad_perm:[2,3,0,1] row_mask:0xf bank_mask:0xf
	v_add_f32_dpp v213, v202, v203 quad_perm:[2,3,0,1] row_mask:0xf bank_mask:0xf
	v_add_f32_dpp v214, v204, v205 quad_perm:[2,3,0,1] row_mask:0xf bank_mask:0xf
	v_add_f32_dpp v215, v236, v237 quad_perm:[2,3,0,1] row_mask:0xf bank_mask:0xf
	v_cndmask_b32_e64 v200, v212, v214, s[0:1]
	v_cndmask_b32_e64 v201, v214, v212, s[0:1]
	v_cndmask_b32_e64 v202, v213, v215, s[0:1]
	v_cndmask_b32_e64 v203, v215, v213, s[0:1]
	s_nop 1
	v_add_f32_dpp v216, v200, v201 quad_perm:[1,0,3,2] row_mask:0xf bank_mask:0xf
	v_add_f32_dpp v217, v202, v203 quad_perm:[1,0,3,2] row_mask:0xf bank_mask:0xf
	s_ashr_i32 s15, s14, 31
	s_lshl_b64 s[14:15], s[14:15], 8
	v_cvt_pk_bf16_f32 v186, v216, v217
	v_lshl_add_u64 v[184:185], v[178:179], 0, s[14:15]
	global_store_dword v[184:185], v186, off
	s_add_u32 s20, s12, 0x200
	s_lshl_b32 s20, s20, 11
	v_lshl_add_u64 v[20:21], v[182:183], 0, s[20:21]
	global_load_dwordx4 v[16:19], v[20:21], off offset:16
	s_nop 0
	global_load_dwordx4 v[20:23], v[20:21], off
	s_add_u32 s20, s12, 0x400
	s_lshl_b32 s20, s20, 9
	v_lshl_add_u64 v[0:1], v[180:181], 0, s[20:21]
	global_load_dwordx4 v[12:15], v[0:1], off offset:48
	global_load_dwordx4 v[8:11], v[0:1], off offset:32
	global_load_dwordx4 v[4:7], v[0:1], off offset:16
	s_nop 0
	global_load_dwordx4 v[0:3], v[0:1], off
	s_add_u32 s10, s12, 0x100
	s_waitcnt vmcnt(23)
; #define PD_E(t, E) do { const char* eb_ = eiu + (size_t)(t) * 512; _Pragma("unroll") for (int q = 0; q < 4; ++q) E[q] = *(const i32x4_t*)(eb_ + (eio + 16u * q)); } while (0)
; DI void phase_peerdown(const Params& p, int bid, int nb) {
;     ...
;     const int t3 = t2 + nw; if (t3 < T_) PD_E(t3, eB);
;     PD_MATH(t1, wB, hB);
	v_cvt_scalef32_pk_bf16_fp8 v210, v112, 1.0
	v_cvt_scalef32_pk_bf16_fp8 v211, v112, 1.0 op_sel:[1,0,0]
	v_cvt_scalef32_pk_bf16_fp8 v212, v113, 1.0
	v_cvt_scalef32_pk_bf16_fp8 v213, v113, 1.0 op_sel:[1,0,0]
	v_mfma_f32_4x4x4_16b_bf16 v[228:231], v[210:211], v[108:109], 0
	v_cvt_scalef32_pk_bf16_fp8 v214, v114, 1.0
	v_cvt_scalef32_pk_bf16_fp8 v215, v114, 1.0 op_sel:[1,0,0]
	v_mfma_f32_4x4x4_16b_bf16 v[228:231], v[212:213], v[110:111], v[228:231]
	v_cvt_scalef32_pk_bf16_fp8 v216, v115, 1.0
	v_cvt_scalef32_pk_bf16_fp8 v217, v115, 1.0 op_sel:[1,0,0]
	v_lshl_or_b32 v80, v80, 7, v209
	global_load_dwordx4 v[112:115], v80, s[6:7]
	v_mfma_f32_4x4x4_16b_bf16 v[228:231], v[214:215], v[100:101], v[228:231]
	v_cvt_scalef32_pk_bf16_fp8 v218, v116, 1.0
	v_cvt_scalef32_pk_bf16_fp8 v219, v116, 1.0 op_sel:[1,0,0]
	v_mfma_f32_4x4x4_16b_bf16 v[228:231], v[216:217], v[102:103], v[228:231]
	v_cvt_scalef32_pk_bf16_fp8 v220, v117, 1.0
	v_cvt_scalef32_pk_bf16_fp8 v221, v117, 1.0 op_sel:[1,0,0]
	v_mfma_f32_4x4x4_16b_bf16 v[232:235], v[218:219], v[108:109], 0
	v_cvt_scalef32_pk_bf16_fp8 v222, v118, 1.0
	v_cvt_scalef32_pk_bf16_fp8 v223, v118, 1.0 op_sel:[1,0,0]
	v_mfma_f32_4x4x4_16b_bf16 v[232:235], v[220:221], v[110:111], v[232:235]
	v_cvt_scalef32_pk_bf16_fp8 v224, v119, 1.0
	v_cvt_scalef32_pk_bf16_fp8 v225, v119, 1.0 op_sel:[1,0,0]
	v_lshl_or_b32 v81, v81, 7, v209
	global_load_dwordx4 v[116:119], v81, s[6:7]
	v_mfma_f32_4x4x4_16b_bf16 v[232:235], v[222:223], v[100:101], v[232:235]
	v_cvt_scalef32_pk_bf16_fp8 v210, v120, 1.0
	v_cvt_scalef32_pk_bf16_fp8 v211, v120, 1.0 op_sel:[1,0,0]
	v_mfma_f32_4x4x4_16b_bf16 v[232:235], v[224:225], v[102:103], v[232:235]
	v_cvt_scalef32_pk_bf16_fp8 v212, v121, 1.0
	v_cvt_scalef32_pk_bf16_fp8 v213, v121, 1.0 op_sel:[1,0,0]
	v_cndmask_b32_e64 v184, v228, v229, s[22:23]
	v_cndmask_b32_e64 v184, v184, v230, s[24:25]
	v_cndmask_b32_e64 v184, v184, v231, s[26:27]
	v_mfma_f32_4x4x4_16b_bf16 v[228:231], v[210:211], v[108:109], 0
	v_cvt_scalef32_pk_bf16_fp8 v214, v122, 1.0
	v_cvt_scalef32_pk_bf16_fp8 v215, v122, 1.0 op_sel:[1,0,0]
	v_mfma_f32_4x4x4_16b_bf16 v[228:231], v[212:213], v[110:111], v[228:231]
	v_cvt_scalef32_pk_bf16_fp8 v216, v123, 1.0
	v_cvt_scalef32_pk_bf16_fp8 v217, v123, 1.0 op_sel:[1,0,0]
	v_lshl_or_b32 v82, v82, 7, v209
	global_load_dwordx4 v[120:123], v82, s[6:7]
	v_mfma_f32_4x4x4_16b_bf16 v[228:231], v[214:215], v[100:101], v[228:231]
	v_cvt_scalef32_pk_bf16_fp8 v218, v124, 1.0
	v_cvt_scalef32_pk_bf16_fp8 v219, v124, 1.0 op_sel:[1,0,0]
	v_mfma_f32_4x4x4_16b_bf16 v[228:231], v[216:217], v[102:103], v[228:231]
	v_cvt_scalef32_pk_bf16_fp8 v220, v125, 1.0
	v_cvt_scalef32_pk_bf16_fp8 v221, v125, 1.0 op_sel:[1,0,0]
	v_cndmask_b32_e64 v185, v232, v233, s[22:23]
	v_cndmask_b32_e64 v185, v185, v234, s[24:25]
	v_cndmask_b32_e64 v185, v185, v235, s[26:27]
	v_mfma_f32_4x4x4_16b_bf16 v[232:235], v[218:219], v[108:109], 0
	v_cvt_scalef32_pk_bf16_fp8 v222, v126, 1.0
	v_cvt_scalef32_pk_bf16_fp8 v223, v126, 1.0 op_sel:[1,0,0]
	v_mfma_f32_4x4x4_16b_bf16 v[232:235], v[220:221], v[110:111], v[232:235]
	v_cvt_scalef32_pk_bf16_fp8 v224, v127, 1.0
	v_cvt_scalef32_pk_bf16_fp8 v225, v127, 1.0 op_sel:[1,0,0]
	v_lshl_or_b32 v83, v83, 7, v209
	global_load_dwordx4 v[124:127], v83, s[6:7]
	v_mfma_f32_4x4x4_16b_bf16 v[232:235], v[222:223], v[100:101], v[232:235]
	v_cvt_scalef32_pk_bf16_fp8 v210, v128, 1.0
	v_cvt_scalef32_pk_bf16_fp8 v211, v128, 1.0 op_sel:[1,0,0]
	v_mfma_f32_4x4x4_16b_bf16 v[232:235], v[224:225], v[102:103], v[232:235]
	v_cvt_scalef32_pk_bf16_fp8 v212, v129, 1.0
	v_cvt_scalef32_pk_bf16_fp8 v213, v129, 1.0 op_sel:[1,0,0]
	v_cndmask_b32_e64 v186, v228, v229, s[22:23]
	v_cndmask_b32_e64 v186, v186, v230, s[24:25]
	v_cndmask_b32_e64 v186, v186, v231, s[26:27]
	v_mfma_f32_4x4x4_16b_bf16 v[228:231], v[210:211], v[108:109], 0
	v_cvt_scalef32_pk_bf16_fp8 v214, v130, 1.0
	v_cvt_scalef32_pk_bf16_fp8 v215, v130, 1.0 op_sel:[1,0,0]
	v_mfma_f32_4x4x4_16b_bf16 v[228:231], v[212:213], v[110:111], v[228:231]
	v_cvt_scalef32_pk_bf16_fp8 v216, v131, 1.0
	v_cvt_scalef32_pk_bf16_fp8 v217, v131, 1.0 op_sel:[1,0,0]
	v_lshl_or_b32 v72, v72, 7, v209
	global_load_dwordx4 v[128:131], v72, s[6:7]
	v_mfma_f32_4x4x4_16b_bf16 v[228:231], v[214:215], v[100:101], v[228:231]
	v_cvt_scalef32_pk_bf16_fp8 v218, v132, 1.0
	v_cvt_scalef32_pk_bf16_fp8 v219, v132, 1.0 op_sel:[1,0,0]
	v_mfma_f32_4x4x4_16b_bf16 v[228:231], v[216:217], v[102:103], v[228:231]
	v_cvt_scalef32_pk_bf16_fp8 v220, v133, 1.0
	v_cvt_scalef32_pk_bf16_fp8 v221, v133, 1.0 op_sel:[1,0,0]
	v_cndmask_b32_e64 v187, v232, v233, s[22:23]
	v_cndmask_b32_e64 v187, v187, v234, s[24:25]
	v_cndmask_b32_e64 v187, v187, v235, s[26:27]
	v_mfma_f32_4x4x4_16b_bf16 v[232:235], v[218:219], v[108:109], 0
	v_cvt_scalef32_pk_bf16_fp8 v222, v134, 1.0
	v_cvt_scalef32_pk_bf16_fp8 v223, v134, 1.0 op_sel:[1,0,0]
	v_mfma_f32_4x4x4_16b_bf16 v[232:235], v[220:221], v[110:111], v[232:235]
	v_cvt_scalef32_pk_bf16_fp8 v224, v135, 1.0
	v_cvt_scalef32_pk_bf16_fp8 v225, v135, 1.0 op_sel:[1,0,0]
	v_lshl_or_b32 v73, v73, 7, v209
	global_load_dwordx4 v[132:135], v73, s[6:7]
	v_mfma_f32_4x4x4_16b_bf16 v[232:235], v[222:223], v[100:101], v[232:235]
	v_cvt_scalef32_pk_bf16_fp8 v210, v136, 1.0
	v_cvt_scalef32_pk_bf16_fp8 v211, v136, 1.0 op_sel:[1,0,0]
	v_mfma_f32_4x4x4_16b_bf16 v[232:235], v[224:225], v[102:103], v[232:235]
	v_cvt_scalef32_pk_bf16_fp8 v212, v137, 1.0
	v_cvt_scalef32_pk_bf16_fp8 v213, v137, 1.0 op_sel:[1,0,0]
	v_cndmask_b32_e64 v188, v228, v229, s[22:23]
	v_cndmask_b32_e64 v188, v188, v230, s[24:25]
	v_cndmask_b32_e64 v188, v188, v231, s[26:27]
	v_mfma_f32_4x4x4_16b_bf16 v[228:231], v[210:211], v[108:109], 0
; #define PD_TAB(E, W) do { _Pragma("unroll") for (int q = 0; q < 16; ++q) W[q] = *(const u32x4*)(tabu + ((unsigned)E[q >> 2][q & 3] * 128u + tabo)); } while (0)
; DI void phase_peerdown(const Params& p, int bid, int nb) {
;     ...
;     if (t1 < T_) PD_TAB(eB, wB);
	v_cvt_scalef32_pk_bf16_fp8 v214, v138, 1.0
	v_cvt_scalef32_pk_bf16_fp8 v215, v138, 1.0 op_sel:[1,0,0]
	v_mfma_f32_4x4x4_16b_bf16 v[228:231], v[212:213], v[110:111], v[228:231]
	v_cvt_scalef32_pk_bf16_fp8 v216, v139, 1.0
	v_cvt_scalef32_pk_bf16_fp8 v217, v139, 1.0 op_sel:[1,0,0]
	v_lshl_or_b32 v74, v74, 7, v209
	global_load_dwordx4 v[136:139], v74, s[6:7]
	v_mfma_f32_4x4x4_16b_bf16 v[228:231], v[214:215], v[100:101], v[228:231]
	v_cvt_scalef32_pk_bf16_fp8 v218, v140, 1.0
	v_cvt_scalef32_pk_bf16_fp8 v219, v140, 1.0 op_sel:[1,0,0]
	v_mfma_f32_4x4x4_16b_bf16 v[228:231], v[216:217], v[102:103], v[228:231]
	v_cvt_scalef32_pk_bf16_fp8 v220, v141, 1.0
	v_cvt_scalef32_pk_bf16_fp8 v221, v141, 1.0 op_sel:[1,0,0]
	v_cndmask_b32_e64 v189, v232, v233, s[22:23]
	v_cndmask_b32_e64 v189, v189, v234, s[24:25]
	v_cndmask_b32_e64 v189, v189, v235, s[26:27]
	v_mfma_f32_4x4x4_16b_bf16 v[232:235], v[218:219], v[108:109], 0
	v_cvt_scalef32_pk_bf16_fp8 v222, v142, 1.0
	v_cvt_scalef32_pk_bf16_fp8 v223, v142, 1.0 op_sel:[1,0,0]
	v_mfma_f32_4x4x4_16b_bf16 v[232:235], v[220:221], v[110:111], v[232:235]
	v_cvt_scalef32_pk_bf16_fp8 v224, v143, 1.0
	v_cvt_scalef32_pk_bf16_fp8 v225, v143, 1.0 op_sel:[1,0,0]
	v_lshl_or_b32 v75, v75, 7, v209
	global_load_dwordx4 v[140:143], v75, s[6:7]
	v_mfma_f32_4x4x4_16b_bf16 v[232:235], v[222:223], v[100:101], v[232:235]
	v_cvt_scalef32_pk_bf16_fp8 v210, v144, 1.0
	v_cvt_scalef32_pk_bf16_fp8 v211, v144, 1.0 op_sel:[1,0,0]
	v_mfma_f32_4x4x4_16b_bf16 v[232:235], v[224:225], v[102:103], v[232:235]
	v_cvt_scalef32_pk_bf16_fp8 v212, v145, 1.0
	v_cvt_scalef32_pk_bf16_fp8 v213, v145, 1.0 op_sel:[1,0,0]
	v_cndmask_b32_e64 v190, v228, v229, s[22:23]
	v_cndmask_b32_e64 v190, v190, v230, s[24:25]
	v_cndmask_b32_e64 v190, v190, v231, s[26:27]
	v_mfma_f32_4x4x4_16b_bf16 v[228:231], v[210:211], v[108:109], 0
	v_cvt_scalef32_pk_bf16_fp8 v214, v146, 1.0
	v_cvt_scalef32_pk_bf16_fp8 v215, v146, 1.0 op_sel:[1,0,0]
	v_mfma_f32_4x4x4_16b_bf16 v[228:231], v[212:213], v[110:111], v[228:231]
	v_cvt_scalef32_pk_bf16_fp8 v216, v147, 1.0
	v_cvt_scalef32_pk_bf16_fp8 v217, v147, 1.0 op_sel:[1,0,0]
	v_lshl_or_b32 v68, v68, 7, v209
	global_load_dwordx4 v[144:147], v68, s[6:7]
	v_mfma_f32_4x4x4_16b_bf16 v[228:231], v[214:215], v[100:101], v[228:231]
	v_cvt_scalef32_pk_bf16_fp8 v218, v148, 1.0
	v_cvt_scalef32_pk_bf16_fp8 v219, v148, 1.0 op_sel:[1,0,0]
	v_mfma_f32_4x4x4_16b_bf16 v[228:231], v[216:217], v[102:103], v[228:231]
	v_cvt_scalef32_pk_bf16_fp8 v220, v149, 1.0
	v_cvt_scalef32_pk_bf16_fp8 v221, v149, 1.0 op_sel:[1,0,0]
	v_cndmask_b32_e64 v191, v232, v233, s[22:23]
	v_cndmask_b32_e64 v191, v191, v234, s[24:25]
	v_cndmask_b32_e64 v191, v191, v235, s[26:27]
	v_mfma_f32_4x4x4_16b_bf16 v[232:235], v[218:219], v[108:109], 0
	v_cvt_scalef32_pk_bf16_fp8 v222, v150, 1.0
	v_cvt_scalef32_pk_bf16_fp8 v223, v150, 1.0 op_sel:[1,0,0]
	v_mfma_f32_4x4x4_16b_bf16 v[232:235], v[220:221], v[110:111], v[232:235]
	v_cvt_scalef32_pk_bf16_fp8 v224, v151, 1.0
	v_cvt_scalef32_pk_bf16_fp8 v225, v151, 1.0 op_sel:[1,0,0]
	v_lshl_or_b32 v69, v69, 7, v209
	global_load_dwordx4 v[148:151], v69, s[6:7]
	v_mfma_f32_4x4x4_16b_bf16 v[232:235], v[222:223], v[100:101], v[232:235]
	v_cvt_scalef32_pk_bf16_fp8 v210, v152, 1.0
	v_cvt_scalef32_pk_bf16_fp8 v211, v152, 1.0 op_sel:[1,0,0]
	v_mfma_f32_4x4x4_16b_bf16 v[232:235], v[224:225], v[102:103], v[232:235]
	v_cvt_scalef32_pk_bf16_fp8 v212, v153, 1.0
	v_cvt_scalef32_pk_bf16_fp8 v213, v153, 1.0 op_sel:[1,0,0]
	v_cndmask_b32_e64 v192, v228, v229, s[22:23]
	v_cndmask_b32_e64 v192, v192, v230, s[24:25]
	v_cndmask_b32_e64 v192, v192, v231, s[26:27]
	v_mfma_f32_4x4x4_16b_bf16 v[228:231], v[210:211], v[108:109], 0
	v_cvt_scalef32_pk_bf16_fp8 v214, v154, 1.0
	v_cvt_scalef32_pk_bf16_fp8 v215, v154, 1.0 op_sel:[1,0,0]
	v_mfma_f32_4x4x4_16b_bf16 v[228:231], v[212:213], v[110:111], v[228:231]
	v_cvt_scalef32_pk_bf16_fp8 v216, v155, 1.0
	v_cvt_scalef32_pk_bf16_fp8 v217, v155, 1.0 op_sel:[1,0,0]
	v_lshl_or_b32 v70, v70, 7, v209
	global_load_dwordx4 v[152:155], v70, s[6:7]
	v_mfma_f32_4x4x4_16b_bf16 v[228:231], v[214:215], v[100:101], v[228:231]
	v_cvt_scalef32_pk_bf16_fp8 v218, v156, 1.0
	v_cvt_scalef32_pk_bf16_fp8 v219, v156, 1.0 op_sel:[1,0,0]
	v_mfma_f32_4x4x4_16b_bf16 v[228:231], v[216:217], v[102:103], v[228:231]
	v_cvt_scalef32_pk_bf16_fp8 v220, v157, 1.0
	v_cvt_scalef32_pk_bf16_fp8 v221, v157, 1.0 op_sel:[1,0,0]
	v_cndmask_b32_e64 v193, v232, v233, s[22:23]
	v_cndmask_b32_e64 v193, v193, v234, s[24:25]
	v_cndmask_b32_e64 v193, v193, v235, s[26:27]
	v_mfma_f32_4x4x4_16b_bf16 v[232:235], v[218:219], v[108:109], 0
	v_cvt_scalef32_pk_bf16_fp8 v222, v158, 1.0
	v_cvt_scalef32_pk_bf16_fp8 v223, v158, 1.0 op_sel:[1,0,0]
	v_mfma_f32_4x4x4_16b_bf16 v[232:235], v[220:221], v[110:111], v[232:235]
	v_cvt_scalef32_pk_bf16_fp8 v224, v159, 1.0
	v_cvt_scalef32_pk_bf16_fp8 v225, v159, 1.0 op_sel:[1,0,0]
	v_lshl_or_b32 v71, v71, 7, v209
	global_load_dwordx4 v[156:159], v71, s[6:7]
	v_mfma_f32_4x4x4_16b_bf16 v[232:235], v[222:223], v[100:101], v[232:235]
	v_cvt_scalef32_pk_bf16_fp8 v210, v160, 1.0
	v_cvt_scalef32_pk_bf16_fp8 v211, v160, 1.0 op_sel:[1,0,0]
	v_mfma_f32_4x4x4_16b_bf16 v[232:235], v[224:225], v[102:103], v[232:235]
	v_cvt_scalef32_pk_bf16_fp8 v212, v161, 1.0
	v_cvt_scalef32_pk_bf16_fp8 v213, v161, 1.0 op_sel:[1,0,0]
	v_cndmask_b32_e64 v194, v228, v229, s[22:23]
	v_cndmask_b32_e64 v194, v194, v230, s[24:25]
	v_cndmask_b32_e64 v194, v194, v231, s[26:27]
	v_mfma_f32_4x4x4_16b_bf16 v[228:231], v[210:211], v[108:109], 0
	v_cvt_scalef32_pk_bf16_fp8 v214, v162, 1.0
	v_cvt_scalef32_pk_bf16_fp8 v215, v162, 1.0 op_sel:[1,0,0]
	v_mfma_f32_4x4x4_16b_bf16 v[228:231], v[212:213], v[110:111], v[228:231]
; #define PD_E(t, E) do { const char* eb_ = eiu + (size_t)(t) * 512; _Pragma("unroll") for (int q = 0; q < 4; ++q) E[q] = *(const i32x4_t*)(eb_ + (eio + 16u * q)); } while (0)
; #define PD_H(t, H) do { const char* hb_ = h2u + (size_t)(t) * 2048; H[0] = *(const u32x4*)(hb_ + h2o); H[1] = *(const u32x4*)(hb_ + (h2o + 16u)); } while (0)
; #define PD_TAB(E, W) do { _Pragma("unroll") for (int q = 0; q < 16; ++q) W[q] = *(const u32x4*)(tabu + ((unsigned)E[q >> 2][q & 3] * 128u + tabo)); } while (0)
; DI void phase_peerdown(const Params& p, int bid, int nb) {
;     ...
;   i32x4_t eA[4], eB[4]; u32x4 hA[2], hB[2], wA[16], wB[16];
;   int t = gw; if (t >= T_) return;
;   int t1 = t + nw;
;   PD_E(t, eA); PD_H(t, hA); PD_TAB(eA, wA);
;   if (t1 < T_) { PD_E(t1, eB); PD_H(t1, hB); }
;   for (;;) {
;     if (t1 < T_) PD_TAB(eB, wB);
;     const int t2 = t1 + nw; if (t2 < T_) PD_E(t2, eA);
;     PD_MATH(t, wA, hA);
;     if (t1 >= T_) break;
;     if (t2 < T_) { PD_H(t2, hA); PD_TAB(eA, wA); }
;     const int t3 = t2 + nw; if (t3 < T_) PD_E(t3, eB);
;     PD_MATH(t1, wB, hB);
;     if (t2 >= T_) break;
;     if (t3 < T_) PD_H(t3, hB);
;     t = t2; t1 = t3;
;   }
	v_cvt_scalef32_pk_bf16_fp8 v216, v163, 1.0
	v_cvt_scalef32_pk_bf16_fp8 v217, v163, 1.0 op_sel:[1,0,0]
	v_lshl_or_b32 v64, v64, 7, v209
	global_load_dwordx4 v[160:163], v64, s[6:7]
	v_mfma_f32_4x4x4_16b_bf16 v[228:231], v[214:215], v[100:101], v[228:231]
	v_cvt_scalef32_pk_bf16_fp8 v218, v164, 1.0
	v_cvt_scalef32_pk_bf16_fp8 v219, v164, 1.0 op_sel:[1,0,0]
	v_mfma_f32_4x4x4_16b_bf16 v[228:231], v[216:217], v[102:103], v[228:231]
	v_cvt_scalef32_pk_bf16_fp8 v220, v165, 1.0
	v_cvt_scalef32_pk_bf16_fp8 v221, v165, 1.0 op_sel:[1,0,0]
	v_cndmask_b32_e64 v195, v232, v233, s[22:23]
	v_cndmask_b32_e64 v195, v195, v234, s[24:25]
	v_cndmask_b32_e64 v195, v195, v235, s[26:27]
	v_mfma_f32_4x4x4_16b_bf16 v[232:235], v[218:219], v[108:109], 0
	v_cvt_scalef32_pk_bf16_fp8 v222, v166, 1.0
	v_cvt_scalef32_pk_bf16_fp8 v223, v166, 1.0 op_sel:[1,0,0]
	v_mfma_f32_4x4x4_16b_bf16 v[232:235], v[220:221], v[110:111], v[232:235]
	v_cvt_scalef32_pk_bf16_fp8 v224, v167, 1.0
	v_cvt_scalef32_pk_bf16_fp8 v225, v167, 1.0 op_sel:[1,0,0]
	v_lshl_or_b32 v65, v65, 7, v209
	global_load_dwordx4 v[164:167], v65, s[6:7]
	v_mfma_f32_4x4x4_16b_bf16 v[232:235], v[222:223], v[100:101], v[232:235]
	v_cvt_scalef32_pk_bf16_fp8 v210, v168, 1.0
	v_cvt_scalef32_pk_bf16_fp8 v211, v168, 1.0 op_sel:[1,0,0]
	v_mfma_f32_4x4x4_16b_bf16 v[232:235], v[224:225], v[102:103], v[232:235]
	v_cvt_scalef32_pk_bf16_fp8 v212, v169, 1.0
	v_cvt_scalef32_pk_bf16_fp8 v213, v169, 1.0 op_sel:[1,0,0]
	v_cndmask_b32_e64 v196, v228, v229, s[22:23]
	v_cndmask_b32_e64 v196, v196, v230, s[24:25]
	v_cndmask_b32_e64 v196, v196, v231, s[26:27]
	v_mfma_f32_4x4x4_16b_bf16 v[228:231], v[210:211], v[108:109], 0
	v_cvt_scalef32_pk_bf16_fp8 v214, v170, 1.0
	v_cvt_scalef32_pk_bf16_fp8 v215, v170, 1.0 op_sel:[1,0,0]
	v_mfma_f32_4x4x4_16b_bf16 v[228:231], v[212:213], v[110:111], v[228:231]
	v_cvt_scalef32_pk_bf16_fp8 v216, v171, 1.0
	v_cvt_scalef32_pk_bf16_fp8 v217, v171, 1.0 op_sel:[1,0,0]
	v_lshl_or_b32 v66, v66, 7, v209
	global_load_dwordx4 v[168:171], v66, s[6:7]
	v_mfma_f32_4x4x4_16b_bf16 v[228:231], v[214:215], v[100:101], v[228:231]
	v_cvt_scalef32_pk_bf16_fp8 v218, v172, 1.0
	v_cvt_scalef32_pk_bf16_fp8 v219, v172, 1.0 op_sel:[1,0,0]
	v_mfma_f32_4x4x4_16b_bf16 v[228:231], v[216:217], v[102:103], v[228:231]
	v_cvt_scalef32_pk_bf16_fp8 v220, v173, 1.0
	v_cvt_scalef32_pk_bf16_fp8 v221, v173, 1.0 op_sel:[1,0,0]
	v_cndmask_b32_e64 v197, v232, v233, s[22:23]
	v_cndmask_b32_e64 v197, v197, v234, s[24:25]
	v_cndmask_b32_e64 v197, v197, v235, s[26:27]
	v_mfma_f32_4x4x4_16b_bf16 v[232:235], v[218:219], v[108:109], 0
	v_cvt_scalef32_pk_bf16_fp8 v222, v174, 1.0
	v_cvt_scalef32_pk_bf16_fp8 v223, v174, 1.0 op_sel:[1,0,0]
	v_mfma_f32_4x4x4_16b_bf16 v[232:235], v[220:221], v[110:111], v[232:235]
	v_cvt_scalef32_pk_bf16_fp8 v224, v175, 1.0
	v_cvt_scalef32_pk_bf16_fp8 v225, v175, 1.0 op_sel:[1,0,0]
	v_lshl_or_b32 v67, v67, 7, v209
	global_load_dwordx4 v[172:175], v67, s[6:7]
	v_mfma_f32_4x4x4_16b_bf16 v[232:235], v[222:223], v[100:101], v[232:235]
	s_nop 1
	v_mfma_f32_4x4x4_16b_bf16 v[232:235], v[224:225], v[102:103], v[232:235]
	v_cndmask_b32_e64 v198, v228, v229, s[22:23]
	v_cndmask_b32_e64 v198, v198, v230, s[24:25]
	v_cndmask_b32_e64 v198, v198, v231, s[26:27]
	s_nop 4
	v_cndmask_b32_e64 v199, v232, v233, s[22:23]
	v_cndmask_b32_e64 v199, v199, v234, s[24:25]
	v_cndmask_b32_e64 v199, v199, v235, s[26:27]
	v_cndmask_b32_e64 v200, v184, v192, s[4:5]
	v_cndmask_b32_e64 v201, v192, v184, s[4:5]
	v_cndmask_b32_e64 v202, v185, v193, s[4:5]
	v_cndmask_b32_e64 v203, v193, v185, s[4:5]
	v_cndmask_b32_e64 v204, v186, v194, s[4:5]
	v_cndmask_b32_e64 v205, v194, v186, s[4:5]
	v_cndmask_b32_e64 v236, v187, v195, s[4:5]
	v_cndmask_b32_e64 v237, v195, v187, s[4:5]
	v_cndmask_b32_e64 v238, v188, v196, s[4:5]
	v_cndmask_b32_e64 v239, v196, v188, s[4:5]
	v_cndmask_b32_e64 v240, v189, v197, s[4:5]
	v_cndmask_b32_e64 v241, v197, v189, s[4:5]
	v_cndmask_b32_e64 v242, v190, v198, s[4:5]
	v_cndmask_b32_e64 v243, v198, v190, s[4:5]
	v_cndmask_b32_e64 v244, v191, v199, s[4:5]
	v_cndmask_b32_e64 v245, v199, v191, s[4:5]
	v_add_f32_dpp v246, v200, v201 row_half_mirror row_mask:0xf bank_mask:0xf
	v_add_f32_dpp v247, v202, v203 row_half_mirror row_mask:0xf bank_mask:0xf
	v_add_f32_dpp v248, v204, v205 row_half_mirror row_mask:0xf bank_mask:0xf
	v_add_f32_dpp v249, v236, v237 row_half_mirror row_mask:0xf bank_mask:0xf
	v_add_f32_dpp v226, v238, v239 row_half_mirror row_mask:0xf bank_mask:0xf
	v_add_f32_dpp v227, v240, v241 row_half_mirror row_mask:0xf bank_mask:0xf
	v_add_f32_dpp v210, v242, v243 row_half_mirror row_mask:0xf bank_mask:0xf
	v_add_f32_dpp v211, v244, v245 row_half_mirror row_mask:0xf bank_mask:0xf
	v_cndmask_b32_e64 v200, v246, v226, s[2:3]
	v_cndmask_b32_e64 v201, v226, v246, s[2:3]
	v_cndmask_b32_e64 v202, v247, v227, s[2:3]
	v_cndmask_b32_e64 v203, v227, v247, s[2:3]
	v_cndmask_b32_e64 v204, v248, v210, s[2:3]
	v_cndmask_b32_e64 v205, v210, v248, s[2:3]
	v_cndmask_b32_e64 v236, v249, v211, s[2:3]
	v_cndmask_b32_e64 v237, v211, v249, s[2:3]
	v_add_f32_dpp v212, v200, v201 quad_perm:[2,3,0,1] row_mask:0xf bank_mask:0xf
	v_add_f32_dpp v213, v202, v203 quad_perm:[2,3,0,1] row_mask:0xf bank_mask:0xf
	v_add_f32_dpp v214, v204, v205 quad_perm:[2,3,0,1] row_mask:0xf bank_mask:0xf
	v_add_f32_dpp v215, v236, v237 quad_perm:[2,3,0,1] row_mask:0xf bank_mask:0xf
	v_cndmask_b32_e64 v200, v212, v214, s[0:1]
	v_cndmask_b32_e64 v201, v214, v212, s[0:1]
	v_cndmask_b32_e64 v202, v213, v215, s[0:1]
	v_cndmask_b32_e64 v203, v215, v213, s[0:1]
	s_nop 1
	v_add_f32_dpp v216, v200, v201 quad_perm:[1,0,3,2] row_mask:0xf bank_mask:0xf
	v_add_f32_dpp v217, v202, v203 quad_perm:[1,0,3,2] row_mask:0xf bank_mask:0xf
	s_ashr_i32 s11, s10, 31
	s_lshl_b64 s[10:11], s[10:11], 8
	v_cvt_pk_bf16_f32 v186, v216, v217
	v_lshl_add_u64 v[184:185], v[178:179], 0, s[10:11]
	global_store_dword v[184:185], v186, off
	s_add_u32 s20, s12, 0x300
	s_lshl_b32 s20, s20, 11
	v_lshl_add_u64 v[108:109], v[182:183], 0, s[20:21]
	global_load_dwordx4 v[100:103], v[108:109], off offset:16
	s_nop 0
	global_load_dwordx4 v[108:111], v[108:109], off
	s_add_u32 s20, s12, 0x500
	s_lshl_b32 s20, s20, 9
	v_lshl_add_u64 v[80:81], v[180:181], 0, s[20:21]
	global_load_dwordx4 v[64:67], v[80:81], off offset:48
	global_load_dwordx4 v[68:71], v[80:81], off offset:32
	global_load_dwordx4 v[72:75], v[80:81], off offset:16
	s_nop 0
	global_load_dwordx4 v[80:83], v[80:81], off
	s_add_u32 s12, s12, 0x200
	s_sub_u32 s13, s13, 1
	s_cmp_lg_u32 s13, 0
	s_cbranch_scc1 .Lpd2_loop
; #define PD_TAB(E, W) do { _Pragma("unroll") for (int q = 0; q < 16; ++q) W[q] = *(const u32x4*)(tabu + ((unsigned)E[q >> 2][q & 3] * 128u + tabo)); } while (0)
; DI void phase_peerdown(const Params& p, int bid, int nb) {
;     ...
;     if (t1 < T_) PD_TAB(eB, wB);
	s_mov_b32 s14, s12
	s_waitcnt vmcnt(23)
	v_cvt_scalef32_pk_bf16_fp8 v210, v24, 1.0
	v_cvt_scalef32_pk_bf16_fp8 v211, v24, 1.0 op_sel:[1,0,0]
	v_cvt_scalef32_pk_bf16_fp8 v212, v25, 1.0
	v_cvt_scalef32_pk_bf16_fp8 v213, v25, 1.0 op_sel:[1,0,0]
	v_mfma_f32_4x4x4_16b_bf16 v[228:231], v[210:211], v[20:21], 0
	v_cvt_scalef32_pk_bf16_fp8 v214, v26, 1.0
	v_cvt_scalef32_pk_bf16_fp8 v215, v26, 1.0 op_sel:[1,0,0]
	v_mfma_f32_4x4x4_16b_bf16 v[228:231], v[212:213], v[22:23], v[228:231]
	v_cvt_scalef32_pk_bf16_fp8 v216, v27, 1.0
	v_cvt_scalef32_pk_bf16_fp8 v217, v27, 1.0 op_sel:[1,0,0]
	v_lshl_or_b32 v0, v0, 7, v209
	global_load_dwordx4 v[24:27], v0, s[6:7]
	v_mfma_f32_4x4x4_16b_bf16 v[228:231], v[214:215], v[16:17], v[228:231]
	v_cvt_scalef32_pk_bf16_fp8 v218, v28, 1.0
	v_cvt_scalef32_pk_bf16_fp8 v219, v28, 1.0 op_sel:[1,0,0]
	v_mfma_f32_4x4x4_16b_bf16 v[228:231], v[216:217], v[18:19], v[228:231]
	v_cvt_scalef32_pk_bf16_fp8 v220, v29, 1.0
	v_cvt_scalef32_pk_bf16_fp8 v221, v29, 1.0 op_sel:[1,0,0]
	v_mfma_f32_4x4x4_16b_bf16 v[232:235], v[218:219], v[20:21], 0
	v_cvt_scalef32_pk_bf16_fp8 v222, v30, 1.0
	v_cvt_scalef32_pk_bf16_fp8 v223, v30, 1.0 op_sel:[1,0,0]
	v_mfma_f32_4x4x4_16b_bf16 v[232:235], v[220:221], v[22:23], v[232:235]
	v_cvt_scalef32_pk_bf16_fp8 v224, v31, 1.0
	v_cvt_scalef32_pk_bf16_fp8 v225, v31, 1.0 op_sel:[1,0,0]
	v_lshl_or_b32 v1, v1, 7, v209
	global_load_dwordx4 v[28:31], v1, s[6:7]
	v_mfma_f32_4x4x4_16b_bf16 v[232:235], v[222:223], v[16:17], v[232:235]
	v_cvt_scalef32_pk_bf16_fp8 v210, v32, 1.0
	v_cvt_scalef32_pk_bf16_fp8 v211, v32, 1.0 op_sel:[1,0,0]
	v_mfma_f32_4x4x4_16b_bf16 v[232:235], v[224:225], v[18:19], v[232:235]
	v_cvt_scalef32_pk_bf16_fp8 v212, v33, 1.0
	v_cvt_scalef32_pk_bf16_fp8 v213, v33, 1.0 op_sel:[1,0,0]
	v_cndmask_b32_e64 v184, v228, v229, s[22:23]
	v_cndmask_b32_e64 v184, v184, v230, s[24:25]
	v_cndmask_b32_e64 v184, v184, v231, s[26:27]
	v_mfma_f32_4x4x4_16b_bf16 v[228:231], v[210:211], v[20:21], 0
	v_cvt_scalef32_pk_bf16_fp8 v214, v34, 1.0
	v_cvt_scalef32_pk_bf16_fp8 v215, v34, 1.0 op_sel:[1,0,0]
	v_mfma_f32_4x4x4_16b_bf16 v[228:231], v[212:213], v[22:23], v[228:231]
	v_cvt_scalef32_pk_bf16_fp8 v216, v35, 1.0
	v_cvt_scalef32_pk_bf16_fp8 v217, v35, 1.0 op_sel:[1,0,0]
	v_lshl_or_b32 v2, v2, 7, v209
	global_load_dwordx4 v[32:35], v2, s[6:7]
	v_mfma_f32_4x4x4_16b_bf16 v[228:231], v[214:215], v[16:17], v[228:231]
	v_cvt_scalef32_pk_bf16_fp8 v218, v36, 1.0
	v_cvt_scalef32_pk_bf16_fp8 v219, v36, 1.0 op_sel:[1,0,0]
	v_mfma_f32_4x4x4_16b_bf16 v[228:231], v[216:217], v[18:19], v[228:231]
	v_cvt_scalef32_pk_bf16_fp8 v220, v37, 1.0
	v_cvt_scalef32_pk_bf16_fp8 v221, v37, 1.0 op_sel:[1,0,0]
	v_cndmask_b32_e64 v185, v232, v233, s[22:23]
	v_cndmask_b32_e64 v185, v185, v234, s[24:25]
	v_cndmask_b32_e64 v185, v185, v235, s[26:27]
	v_mfma_f32_4x4x4_16b_bf16 v[232:235], v[218:219], v[20:21], 0
	v_cvt_scalef32_pk_bf16_fp8 v222, v38, 1.0
	v_cvt_scalef32_pk_bf16_fp8 v223, v38, 1.0 op_sel:[1,0,0]
	v_mfma_f32_4x4x4_16b_bf16 v[232:235], v[220:221], v[22:23], v[232:235]
	v_cvt_scalef32_pk_bf16_fp8 v224, v39, 1.0
	v_cvt_scalef32_pk_bf16_fp8 v225, v39, 1.0 op_sel:[1,0,0]
	v_lshl_or_b32 v3, v3, 7, v209
	global_load_dwordx4 v[36:39], v3, s[6:7]
	v_mfma_f32_4x4x4_16b_bf16 v[232:235], v[222:223], v[16:17], v[232:235]
	v_cvt_scalef32_pk_bf16_fp8 v210, v40, 1.0
	v_cvt_scalef32_pk_bf16_fp8 v211, v40, 1.0 op_sel:[1,0,0]
	v_mfma_f32_4x4x4_16b_bf16 v[232:235], v[224:225], v[18:19], v[232:235]
	v_cvt_scalef32_pk_bf16_fp8 v212, v41, 1.0
	v_cvt_scalef32_pk_bf16_fp8 v213, v41, 1.0 op_sel:[1,0,0]
	v_cndmask_b32_e64 v186, v228, v229, s[22:23]
	v_cndmask_b32_e64 v186, v186, v230, s[24:25]
	v_cndmask_b32_e64 v186, v186, v231, s[26:27]
	v_mfma_f32_4x4x4_16b_bf16 v[228:231], v[210:211], v[20:21], 0
	v_cvt_scalef32_pk_bf16_fp8 v214, v42, 1.0
	v_cvt_scalef32_pk_bf16_fp8 v215, v42, 1.0 op_sel:[1,0,0]
	v_mfma_f32_4x4x4_16b_bf16 v[228:231], v[212:213], v[22:23], v[228:231]
	v_cvt_scalef32_pk_bf16_fp8 v216, v43, 1.0
	v_cvt_scalef32_pk_bf16_fp8 v217, v43, 1.0 op_sel:[1,0,0]
	v_lshl_or_b32 v4, v4, 7, v209
	global_load_dwordx4 v[40:43], v4, s[6:7]
	v_mfma_f32_4x4x4_16b_bf16 v[228:231], v[214:215], v[16:17], v[228:231]
	v_cvt_scalef32_pk_bf16_fp8 v218, v44, 1.0
	v_cvt_scalef32_pk_bf16_fp8 v219, v44, 1.0 op_sel:[1,0,0]
	v_mfma_f32_4x4x4_16b_bf16 v[228:231], v[216:217], v[18:19], v[228:231]
	v_cvt_scalef32_pk_bf16_fp8 v220, v45, 1.0
	v_cvt_scalef32_pk_bf16_fp8 v221, v45, 1.0 op_sel:[1,0,0]
	v_cndmask_b32_e64 v187, v232, v233, s[22:23]
	v_cndmask_b32_e64 v187, v187, v234, s[24:25]
	v_cndmask_b32_e64 v187, v187, v235, s[26:27]
	v_mfma_f32_4x4x4_16b_bf16 v[232:235], v[218:219], v[20:21], 0
	v_cvt_scalef32_pk_bf16_fp8 v222, v46, 1.0
	v_cvt_scalef32_pk_bf16_fp8 v223, v46, 1.0 op_sel:[1,0,0]
	v_mfma_f32_4x4x4_16b_bf16 v[232:235], v[220:221], v[22:23], v[232:235]
	v_cvt_scalef32_pk_bf16_fp8 v224, v47, 1.0
	v_cvt_scalef32_pk_bf16_fp8 v225, v47, 1.0 op_sel:[1,0,0]
	v_lshl_or_b32 v5, v5, 7, v209
	global_load_dwordx4 v[44:47], v5, s[6:7]
	v_mfma_f32_4x4x4_16b_bf16 v[232:235], v[222:223], v[16:17], v[232:235]
	v_cvt_scalef32_pk_bf16_fp8 v210, v48, 1.0
	v_cvt_scalef32_pk_bf16_fp8 v211, v48, 1.0 op_sel:[1,0,0]
	v_mfma_f32_4x4x4_16b_bf16 v[232:235], v[224:225], v[18:19], v[232:235]
	v_cvt_scalef32_pk_bf16_fp8 v212, v49, 1.0
	v_cvt_scalef32_pk_bf16_fp8 v213, v49, 1.0 op_sel:[1,0,0]
	v_cndmask_b32_e64 v188, v228, v229, s[22:23]
	v_cndmask_b32_e64 v188, v188, v230, s[24:25]
	v_cndmask_b32_e64 v188, v188, v231, s[26:27]
	v_mfma_f32_4x4x4_16b_bf16 v[228:231], v[210:211], v[20:21], 0
	v_cvt_scalef32_pk_bf16_fp8 v214, v50, 1.0
	v_cvt_scalef32_pk_bf16_fp8 v215, v50, 1.0 op_sel:[1,0,0]
	v_mfma_f32_4x4x4_16b_bf16 v[228:231], v[212:213], v[22:23], v[228:231]
	v_cvt_scalef32_pk_bf16_fp8 v216, v51, 1.0
	v_cvt_scalef32_pk_bf16_fp8 v217, v51, 1.0 op_sel:[1,0,0]
	v_lshl_or_b32 v6, v6, 7, v209
	global_load_dwordx4 v[48:51], v6, s[6:7]
	v_mfma_f32_4x4x4_16b_bf16 v[228:231], v[214:215], v[16:17], v[228:231]
	v_cvt_scalef32_pk_bf16_fp8 v218, v52, 1.0
	v_cvt_scalef32_pk_bf16_fp8 v219, v52, 1.0 op_sel:[1,0,0]
	v_mfma_f32_4x4x4_16b_bf16 v[228:231], v[216:217], v[18:19], v[228:231]
	v_cvt_scalef32_pk_bf16_fp8 v220, v53, 1.0
	v_cvt_scalef32_pk_bf16_fp8 v221, v53, 1.0 op_sel:[1,0,0]
	v_cndmask_b32_e64 v189, v232, v233, s[22:23]
	v_cndmask_b32_e64 v189, v189, v234, s[24:25]
	v_cndmask_b32_e64 v189, v189, v235, s[26:27]
	v_mfma_f32_4x4x4_16b_bf16 v[232:235], v[218:219], v[20:21], 0
	v_cvt_scalef32_pk_bf16_fp8 v222, v54, 1.0
	v_cvt_scalef32_pk_bf16_fp8 v223, v54, 1.0 op_sel:[1,0,0]
	v_mfma_f32_4x4x4_16b_bf16 v[232:235], v[220:221], v[22:23], v[232:235]
	v_cvt_scalef32_pk_bf16_fp8 v224, v55, 1.0
	v_cvt_scalef32_pk_bf16_fp8 v225, v55, 1.0 op_sel:[1,0,0]
	v_lshl_or_b32 v7, v7, 7, v209
	global_load_dwordx4 v[52:55], v7, s[6:7]
	v_mfma_f32_4x4x4_16b_bf16 v[232:235], v[222:223], v[16:17], v[232:235]
	v_cvt_scalef32_pk_bf16_fp8 v210, v56, 1.0
	v_cvt_scalef32_pk_bf16_fp8 v211, v56, 1.0 op_sel:[1,0,0]
	v_mfma_f32_4x4x4_16b_bf16 v[232:235], v[224:225], v[18:19], v[232:235]
	v_cvt_scalef32_pk_bf16_fp8 v212, v57, 1.0
	v_cvt_scalef32_pk_bf16_fp8 v213, v57, 1.0 op_sel:[1,0,0]
	v_cndmask_b32_e64 v190, v228, v229, s[22:23]
	v_cndmask_b32_e64 v190, v190, v230, s[24:25]
	v_cndmask_b32_e64 v190, v190, v231, s[26:27]
	v_mfma_f32_4x4x4_16b_bf16 v[228:231], v[210:211], v[20:21], 0
	v_cvt_scalef32_pk_bf16_fp8 v214, v58, 1.0
	v_cvt_scalef32_pk_bf16_fp8 v215, v58, 1.0 op_sel:[1,0,0]
	v_mfma_f32_4x4x4_16b_bf16 v[228:231], v[212:213], v[22:23], v[228:231]
	v_cvt_scalef32_pk_bf16_fp8 v216, v59, 1.0
	v_cvt_scalef32_pk_bf16_fp8 v217, v59, 1.0 op_sel:[1,0,0]
	v_lshl_or_b32 v8, v8, 7, v209
	global_load_dwordx4 v[56:59], v8, s[6:7]
	v_mfma_f32_4x4x4_16b_bf16 v[228:231], v[214:215], v[16:17], v[228:231]
	v_cvt_scalef32_pk_bf16_fp8 v218, v60, 1.0
	v_cvt_scalef32_pk_bf16_fp8 v219, v60, 1.0 op_sel:[1,0,0]
	v_mfma_f32_4x4x4_16b_bf16 v[228:231], v[216:217], v[18:19], v[228:231]
	v_cvt_scalef32_pk_bf16_fp8 v220, v61, 1.0
	v_cvt_scalef32_pk_bf16_fp8 v221, v61, 1.0 op_sel:[1,0,0]
	v_cndmask_b32_e64 v191, v232, v233, s[22:23]
	v_cndmask_b32_e64 v191, v191, v234, s[24:25]
	v_cndmask_b32_e64 v191, v191, v235, s[26:27]
	v_mfma_f32_4x4x4_16b_bf16 v[232:235], v[218:219], v[20:21], 0
	v_cvt_scalef32_pk_bf16_fp8 v222, v62, 1.0
	v_cvt_scalef32_pk_bf16_fp8 v223, v62, 1.0 op_sel:[1,0,0]
	v_mfma_f32_4x4x4_16b_bf16 v[232:235], v[220:221], v[22:23], v[232:235]
	v_cvt_scalef32_pk_bf16_fp8 v224, v63, 1.0
	v_cvt_scalef32_pk_bf16_fp8 v225, v63, 1.0 op_sel:[1,0,0]
	v_lshl_or_b32 v9, v9, 7, v209
	global_load_dwordx4 v[60:63], v9, s[6:7]
	v_mfma_f32_4x4x4_16b_bf16 v[232:235], v[222:223], v[16:17], v[232:235]
	v_cvt_scalef32_pk_bf16_fp8 v210, v76, 1.0
	v_cvt_scalef32_pk_bf16_fp8 v211, v76, 1.0 op_sel:[1,0,0]
	v_mfma_f32_4x4x4_16b_bf16 v[232:235], v[224:225], v[18:19], v[232:235]
	v_cvt_scalef32_pk_bf16_fp8 v212, v77, 1.0
	v_cvt_scalef32_pk_bf16_fp8 v213, v77, 1.0 op_sel:[1,0,0]
	v_cndmask_b32_e64 v192, v228, v229, s[22:23]
	v_cndmask_b32_e64 v192, v192, v230, s[24:25]
	v_cndmask_b32_e64 v192, v192, v231, s[26:27]
	v_mfma_f32_4x4x4_16b_bf16 v[228:231], v[210:211], v[20:21], 0
	v_cvt_scalef32_pk_bf16_fp8 v214, v78, 1.0
	v_cvt_scalef32_pk_bf16_fp8 v215, v78, 1.0 op_sel:[1,0,0]
	v_mfma_f32_4x4x4_16b_bf16 v[228:231], v[212:213], v[22:23], v[228:231]
	v_cvt_scalef32_pk_bf16_fp8 v216, v79, 1.0
	v_cvt_scalef32_pk_bf16_fp8 v217, v79, 1.0 op_sel:[1,0,0]
	v_lshl_or_b32 v10, v10, 7, v209
	global_load_dwordx4 v[76:79], v10, s[6:7]
	v_mfma_f32_4x4x4_16b_bf16 v[228:231], v[214:215], v[16:17], v[228:231]
	v_cvt_scalef32_pk_bf16_fp8 v218, v84, 1.0
	v_cvt_scalef32_pk_bf16_fp8 v219, v84, 1.0 op_sel:[1,0,0]
	v_mfma_f32_4x4x4_16b_bf16 v[228:231], v[216:217], v[18:19], v[228:231]
	v_cvt_scalef32_pk_bf16_fp8 v220, v85, 1.0
	v_cvt_scalef32_pk_bf16_fp8 v221, v85, 1.0 op_sel:[1,0,0]
	v_cndmask_b32_e64 v193, v232, v233, s[22:23]
	v_cndmask_b32_e64 v193, v193, v234, s[24:25]
	v_cndmask_b32_e64 v193, v193, v235, s[26:27]
	v_mfma_f32_4x4x4_16b_bf16 v[232:235], v[218:219], v[20:21], 0
	v_cvt_scalef32_pk_bf16_fp8 v222, v86, 1.0
	v_cvt_scalef32_pk_bf16_fp8 v223, v86, 1.0 op_sel:[1,0,0]
	v_mfma_f32_4x4x4_16b_bf16 v[232:235], v[220:221], v[22:23], v[232:235]
	v_cvt_scalef32_pk_bf16_fp8 v224, v87, 1.0
	v_cvt_scalef32_pk_bf16_fp8 v225, v87, 1.0 op_sel:[1,0,0]
	v_lshl_or_b32 v11, v11, 7, v209
	global_load_dwordx4 v[84:87], v11, s[6:7]
	v_mfma_f32_4x4x4_16b_bf16 v[232:235], v[222:223], v[16:17], v[232:235]
	v_cvt_scalef32_pk_bf16_fp8 v210, v88, 1.0
	v_cvt_scalef32_pk_bf16_fp8 v211, v88, 1.0 op_sel:[1,0,0]
	v_mfma_f32_4x4x4_16b_bf16 v[232:235], v[224:225], v[18:19], v[232:235]
	v_cvt_scalef32_pk_bf16_fp8 v212, v89, 1.0
	v_cvt_scalef32_pk_bf16_fp8 v213, v89, 1.0 op_sel:[1,0,0]
	v_cndmask_b32_e64 v194, v228, v229, s[22:23]
	v_cndmask_b32_e64 v194, v194, v230, s[24:25]
	v_cndmask_b32_e64 v194, v194, v231, s[26:27]
	v_mfma_f32_4x4x4_16b_bf16 v[228:231], v[210:211], v[20:21], 0
	v_cvt_scalef32_pk_bf16_fp8 v214, v90, 1.0
	v_cvt_scalef32_pk_bf16_fp8 v215, v90, 1.0 op_sel:[1,0,0]
	v_mfma_f32_4x4x4_16b_bf16 v[228:231], v[212:213], v[22:23], v[228:231]
	v_cvt_scalef32_pk_bf16_fp8 v216, v91, 1.0
	v_cvt_scalef32_pk_bf16_fp8 v217, v91, 1.0 op_sel:[1,0,0]
	v_lshl_or_b32 v12, v12, 7, v209
	global_load_dwordx4 v[88:91], v12, s[6:7]
	v_mfma_f32_4x4x4_16b_bf16 v[228:231], v[214:215], v[16:17], v[228:231]
	v_cvt_scalef32_pk_bf16_fp8 v218, v92, 1.0
	v_cvt_scalef32_pk_bf16_fp8 v219, v92, 1.0 op_sel:[1,0,0]
	v_mfma_f32_4x4x4_16b_bf16 v[228:231], v[216:217], v[18:19], v[228:231]
	v_cvt_scalef32_pk_bf16_fp8 v220, v93, 1.0
	v_cvt_scalef32_pk_bf16_fp8 v221, v93, 1.0 op_sel:[1,0,0]
	v_cndmask_b32_e64 v195, v232, v233, s[22:23]
	v_cndmask_b32_e64 v195, v195, v234, s[24:25]
	v_cndmask_b32_e64 v195, v195, v235, s[26:27]
	v_mfma_f32_4x4x4_16b_bf16 v[232:235], v[218:219], v[20:21], 0
	v_cvt_scalef32_pk_bf16_fp8 v222, v94, 1.0
	v_cvt_scalef32_pk_bf16_fp8 v223, v94, 1.0 op_sel:[1,0,0]
	v_mfma_f32_4x4x4_16b_bf16 v[232:235], v[220:221], v[22:23], v[232:235]
	v_cvt_scalef32_pk_bf16_fp8 v224, v95, 1.0
	v_cvt_scalef32_pk_bf16_fp8 v225, v95, 1.0 op_sel:[1,0,0]
	v_lshl_or_b32 v13, v13, 7, v209
	global_load_dwordx4 v[92:95], v13, s[6:7]
	v_mfma_f32_4x4x4_16b_bf16 v[232:235], v[222:223], v[16:17], v[232:235]
	v_cvt_scalef32_pk_bf16_fp8 v210, v96, 1.0
	v_cvt_scalef32_pk_bf16_fp8 v211, v96, 1.0 op_sel:[1,0,0]
	v_mfma_f32_4x4x4_16b_bf16 v[232:235], v[224:225], v[18:19], v[232:235]
	v_cvt_scalef32_pk_bf16_fp8 v212, v97, 1.0
	v_cvt_scalef32_pk_bf16_fp8 v213, v97, 1.0 op_sel:[1,0,0]
	v_cndmask_b32_e64 v196, v228, v229, s[22:23]
	v_cndmask_b32_e64 v196, v196, v230, s[24:25]
	v_cndmask_b32_e64 v196, v196, v231, s[26:27]
	v_mfma_f32_4x4x4_16b_bf16 v[228:231], v[210:211], v[20:21], 0
	v_cvt_scalef32_pk_bf16_fp8 v214, v98, 1.0
	v_cvt_scalef32_pk_bf16_fp8 v215, v98, 1.0 op_sel:[1,0,0]
	v_mfma_f32_4x4x4_16b_bf16 v[228:231], v[212:213], v[22:23], v[228:231]
	v_cvt_scalef32_pk_bf16_fp8 v216, v99, 1.0
	v_cvt_scalef32_pk_bf16_fp8 v217, v99, 1.0 op_sel:[1,0,0]
	v_lshl_or_b32 v14, v14, 7, v209
	global_load_dwordx4 v[96:99], v14, s[6:7]
	v_mfma_f32_4x4x4_16b_bf16 v[228:231], v[214:215], v[16:17], v[228:231]
	v_cvt_scalef32_pk_bf16_fp8 v218, v104, 1.0
	v_cvt_scalef32_pk_bf16_fp8 v219, v104, 1.0 op_sel:[1,0,0]
	v_mfma_f32_4x4x4_16b_bf16 v[228:231], v[216:217], v[18:19], v[228:231]
	v_cvt_scalef32_pk_bf16_fp8 v220, v105, 1.0
	v_cvt_scalef32_pk_bf16_fp8 v221, v105, 1.0 op_sel:[1,0,0]
	v_cndmask_b32_e64 v197, v232, v233, s[22:23]
	v_cndmask_b32_e64 v197, v197, v234, s[24:25]
	v_cndmask_b32_e64 v197, v197, v235, s[26:27]
	v_mfma_f32_4x4x4_16b_bf16 v[232:235], v[218:219], v[20:21], 0
	v_cvt_scalef32_pk_bf16_fp8 v222, v106, 1.0
	v_cvt_scalef32_pk_bf16_fp8 v223, v106, 1.0 op_sel:[1,0,0]
	v_mfma_f32_4x4x4_16b_bf16 v[232:235], v[220:221], v[22:23], v[232:235]
	v_cvt_scalef32_pk_bf16_fp8 v224, v107, 1.0
	v_cvt_scalef32_pk_bf16_fp8 v225, v107, 1.0 op_sel:[1,0,0]
	v_lshl_or_b32 v15, v15, 7, v209
	global_load_dwordx4 v[104:107], v15, s[6:7]
	v_mfma_f32_4x4x4_16b_bf16 v[232:235], v[222:223], v[16:17], v[232:235]
	s_nop 1
	v_mfma_f32_4x4x4_16b_bf16 v[232:235], v[224:225], v[18:19], v[232:235]
	v_cndmask_b32_e64 v198, v228, v229, s[22:23]
	v_cndmask_b32_e64 v198, v198, v230, s[24:25]
	v_cndmask_b32_e64 v198, v198, v231, s[26:27]
	s_nop 4
	v_cndmask_b32_e64 v199, v232, v233, s[22:23]
	v_cndmask_b32_e64 v199, v199, v234, s[24:25]
	v_cndmask_b32_e64 v199, v199, v235, s[26:27]
	v_cndmask_b32_e64 v200, v184, v192, s[4:5]
	v_cndmask_b32_e64 v201, v192, v184, s[4:5]
	v_cndmask_b32_e64 v202, v185, v193, s[4:5]
	v_cndmask_b32_e64 v203, v193, v185, s[4:5]
	v_cndmask_b32_e64 v204, v186, v194, s[4:5]
	v_cndmask_b32_e64 v205, v194, v186, s[4:5]
	v_cndmask_b32_e64 v236, v187, v195, s[4:5]
	v_cndmask_b32_e64 v237, v195, v187, s[4:5]
	v_cndmask_b32_e64 v238, v188, v196, s[4:5]
	v_cndmask_b32_e64 v239, v196, v188, s[4:5]
	v_cndmask_b32_e64 v240, v189, v197, s[4:5]
	v_cndmask_b32_e64 v241, v197, v189, s[4:5]
	v_cndmask_b32_e64 v242, v190, v198, s[4:5]
	v_cndmask_b32_e64 v243, v198, v190, s[4:5]
	v_cndmask_b32_e64 v244, v191, v199, s[4:5]
	v_cndmask_b32_e64 v245, v199, v191, s[4:5]
	v_add_f32_dpp v246, v200, v201 row_half_mirror row_mask:0xf bank_mask:0xf
	v_add_f32_dpp v247, v202, v203 row_half_mirror row_mask:0xf bank_mask:0xf
	v_add_f32_dpp v248, v204, v205 row_half_mirror row_mask:0xf bank_mask:0xf
	v_add_f32_dpp v249, v236, v237 row_half_mirror row_mask:0xf bank_mask:0xf
	v_add_f32_dpp v226, v238, v239 row_half_mirror row_mask:0xf bank_mask:0xf
	v_add_f32_dpp v227, v240, v241 row_half_mirror row_mask:0xf bank_mask:0xf
	v_add_f32_dpp v210, v242, v243 row_half_mirror row_mask:0xf bank_mask:0xf
	v_add_f32_dpp v211, v244, v245 row_half_mirror row_mask:0xf bank_mask:0xf
	v_cndmask_b32_e64 v200, v246, v226, s[2:3]
	v_cndmask_b32_e64 v201, v226, v246, s[2:3]
	v_cndmask_b32_e64 v202, v247, v227, s[2:3]
	v_cndmask_b32_e64 v203, v227, v247, s[2:3]
	v_cndmask_b32_e64 v204, v248, v210, s[2:3]
	v_cndmask_b32_e64 v205, v210, v248, s[2:3]
	v_cndmask_b32_e64 v236, v249, v211, s[2:3]
	v_cndmask_b32_e64 v237, v211, v249, s[2:3]
	v_add_f32_dpp v212, v200, v201 quad_perm:[2,3,0,1] row_mask:0xf bank_mask:0xf
	v_add_f32_dpp v213, v202, v203 quad_perm:[2,3,0,1] row_mask:0xf bank_mask:0xf
	v_add_f32_dpp v214, v204, v205 quad_perm:[2,3,0,1] row_mask:0xf bank_mask:0xf
	v_add_f32_dpp v215, v236, v237 quad_perm:[2,3,0,1] row_mask:0xf bank_mask:0xf
	v_cndmask_b32_e64 v200, v212, v214, s[0:1]
	v_cndmask_b32_e64 v201, v214, v212, s[0:1]
	v_cndmask_b32_e64 v202, v213, v215, s[0:1]
	v_cndmask_b32_e64 v203, v215, v213, s[0:1]
	s_nop 1
	v_add_f32_dpp v216, v200, v201 quad_perm:[1,0,3,2] row_mask:0xf bank_mask:0xf
	v_add_f32_dpp v217, v202, v203 quad_perm:[1,0,3,2] row_mask:0xf bank_mask:0xf
	s_ashr_i32 s15, s14, 31
	s_lshl_b64 s[14:15], s[14:15], 8
	v_cvt_pk_bf16_f32 v186, v216, v217
	v_lshl_add_u64 v[184:185], v[178:179], 0, s[14:15]
	global_store_dword v[184:185], v186, off
	s_add_u32 s20, s12, 0x200
	s_lshl_b32 s20, s20, 11
	v_lshl_add_u64 v[20:21], v[182:183], 0, s[20:21]
	global_load_dwordx4 v[16:19], v[20:21], off offset:16
	s_nop 0
	global_load_dwordx4 v[20:23], v[20:21], off
	s_add_u32 s10, s12, 0x100
	s_waitcnt vmcnt(19)
	v_cvt_scalef32_pk_bf16_fp8 v210, v112, 1.0
	v_cvt_scalef32_pk_bf16_fp8 v211, v112, 1.0 op_sel:[1,0,0]
	v_cvt_scalef32_pk_bf16_fp8 v212, v113, 1.0
	v_cvt_scalef32_pk_bf16_fp8 v213, v113, 1.0 op_sel:[1,0,0]
	v_mfma_f32_4x4x4_16b_bf16 v[228:231], v[210:211], v[108:109], 0
	v_cvt_scalef32_pk_bf16_fp8 v214, v114, 1.0
	v_cvt_scalef32_pk_bf16_fp8 v215, v114, 1.0 op_sel:[1,0,0]
	v_mfma_f32_4x4x4_16b_bf16 v[228:231], v[212:213], v[110:111], v[228:231]
	v_cvt_scalef32_pk_bf16_fp8 v216, v115, 1.0
	v_cvt_scalef32_pk_bf16_fp8 v217, v115, 1.0 op_sel:[1,0,0]
	v_lshl_or_b32 v80, v80, 7, v209
	global_load_dwordx4 v[112:115], v80, s[6:7]
	v_mfma_f32_4x4x4_16b_bf16 v[228:231], v[214:215], v[100:101], v[228:231]
	v_cvt_scalef32_pk_bf16_fp8 v218, v116, 1.0
	v_cvt_scalef32_pk_bf16_fp8 v219, v116, 1.0 op_sel:[1,0,0]
	v_mfma_f32_4x4x4_16b_bf16 v[228:231], v[216:217], v[102:103], v[228:231]
	v_cvt_scalef32_pk_bf16_fp8 v220, v117, 1.0
	v_cvt_scalef32_pk_bf16_fp8 v221, v117, 1.0 op_sel:[1,0,0]
	v_mfma_f32_4x4x4_16b_bf16 v[232:235], v[218:219], v[108:109], 0
	v_cvt_scalef32_pk_bf16_fp8 v222, v118, 1.0
	v_cvt_scalef32_pk_bf16_fp8 v223, v118, 1.0 op_sel:[1,0,0]
	v_mfma_f32_4x4x4_16b_bf16 v[232:235], v[220:221], v[110:111], v[232:235]
	v_cvt_scalef32_pk_bf16_fp8 v224, v119, 1.0
	v_cvt_scalef32_pk_bf16_fp8 v225, v119, 1.0 op_sel:[1,0,0]
	v_lshl_or_b32 v81, v81, 7, v209
	global_load_dwordx4 v[116:119], v81, s[6:7]
	v_mfma_f32_4x4x4_16b_bf16 v[232:235], v[222:223], v[100:101], v[232:235]
	v_cvt_scalef32_pk_bf16_fp8 v210, v120, 1.0
	v_cvt_scalef32_pk_bf16_fp8 v211, v120, 1.0 op_sel:[1,0,0]
	v_mfma_f32_4x4x4_16b_bf16 v[232:235], v[224:225], v[102:103], v[232:235]
	v_cvt_scalef32_pk_bf16_fp8 v212, v121, 1.0
	v_cvt_scalef32_pk_bf16_fp8 v213, v121, 1.0 op_sel:[1,0,0]
	v_cndmask_b32_e64 v184, v228, v229, s[22:23]
	v_cndmask_b32_e64 v184, v184, v230, s[24:25]
	v_cndmask_b32_e64 v184, v184, v231, s[26:27]
	v_mfma_f32_4x4x4_16b_bf16 v[228:231], v[210:211], v[108:109], 0
	v_cvt_scalef32_pk_bf16_fp8 v214, v122, 1.0
	v_cvt_scalef32_pk_bf16_fp8 v215, v122, 1.0 op_sel:[1,0,0]
	v_mfma_f32_4x4x4_16b_bf16 v[228:231], v[212:213], v[110:111], v[228:231]
	v_cvt_scalef32_pk_bf16_fp8 v216, v123, 1.0
	v_cvt_scalef32_pk_bf16_fp8 v217, v123, 1.0 op_sel:[1,0,0]
	v_lshl_or_b32 v82, v82, 7, v209
	global_load_dwordx4 v[120:123], v82, s[6:7]
	v_mfma_f32_4x4x4_16b_bf16 v[228:231], v[214:215], v[100:101], v[228:231]
	v_cvt_scalef32_pk_bf16_fp8 v218, v124, 1.0
	v_cvt_scalef32_pk_bf16_fp8 v219, v124, 1.0 op_sel:[1,0,0]
	v_mfma_f32_4x4x4_16b_bf16 v[228:231], v[216:217], v[102:103], v[228:231]
	v_cvt_scalef32_pk_bf16_fp8 v220, v125, 1.0
	v_cvt_scalef32_pk_bf16_fp8 v221, v125, 1.0 op_sel:[1,0,0]
	v_cndmask_b32_e64 v185, v232, v233, s[22:23]
	v_cndmask_b32_e64 v185, v185, v234, s[24:25]
	v_cndmask_b32_e64 v185, v185, v235, s[26:27]
	v_mfma_f32_4x4x4_16b_bf16 v[232:235], v[218:219], v[108:109], 0
	v_cvt_scalef32_pk_bf16_fp8 v222, v126, 1.0
	v_cvt_scalef32_pk_bf16_fp8 v223, v126, 1.0 op_sel:[1,0,0]
	v_mfma_f32_4x4x4_16b_bf16 v[232:235], v[220:221], v[110:111], v[232:235]
	v_cvt_scalef32_pk_bf16_fp8 v224, v127, 1.0
	v_cvt_scalef32_pk_bf16_fp8 v225, v127, 1.0 op_sel:[1,0,0]
	v_lshl_or_b32 v83, v83, 7, v209
	global_load_dwordx4 v[124:127], v83, s[6:7]
	v_mfma_f32_4x4x4_16b_bf16 v[232:235], v[222:223], v[100:101], v[232:235]
	v_cvt_scalef32_pk_bf16_fp8 v210, v128, 1.0
	v_cvt_scalef32_pk_bf16_fp8 v211, v128, 1.0 op_sel:[1,0,0]
	v_mfma_f32_4x4x4_16b_bf16 v[232:235], v[224:225], v[102:103], v[232:235]
	v_cvt_scalef32_pk_bf16_fp8 v212, v129, 1.0
	v_cvt_scalef32_pk_bf16_fp8 v213, v129, 1.0 op_sel:[1,0,0]
	v_cndmask_b32_e64 v186, v228, v229, s[22:23]
	v_cndmask_b32_e64 v186, v186, v230, s[24:25]
	v_cndmask_b32_e64 v186, v186, v231, s[26:27]
	v_mfma_f32_4x4x4_16b_bf16 v[228:231], v[210:211], v[108:109], 0
	v_cvt_scalef32_pk_bf16_fp8 v214, v130, 1.0
	v_cvt_scalef32_pk_bf16_fp8 v215, v130, 1.0 op_sel:[1,0,0]
	v_mfma_f32_4x4x4_16b_bf16 v[228:231], v[212:213], v[110:111], v[228:231]
	v_cvt_scalef32_pk_bf16_fp8 v216, v131, 1.0
	v_cvt_scalef32_pk_bf16_fp8 v217, v131, 1.0 op_sel:[1,0,0]
	v_lshl_or_b32 v72, v72, 7, v209
	global_load_dwordx4 v[128:131], v72, s[6:7]
	v_mfma_f32_4x4x4_16b_bf16 v[228:231], v[214:215], v[100:101], v[228:231]
	v_cvt_scalef32_pk_bf16_fp8 v218, v132, 1.0
	v_cvt_scalef32_pk_bf16_fp8 v219, v132, 1.0 op_sel:[1,0,0]
	v_mfma_f32_4x4x4_16b_bf16 v[228:231], v[216:217], v[102:103], v[228:231]
	v_cvt_scalef32_pk_bf16_fp8 v220, v133, 1.0
	v_cvt_scalef32_pk_bf16_fp8 v221, v133, 1.0 op_sel:[1,0,0]
	v_cndmask_b32_e64 v187, v232, v233, s[22:23]
	v_cndmask_b32_e64 v187, v187, v234, s[24:25]
	v_cndmask_b32_e64 v187, v187, v235, s[26:27]
	v_mfma_f32_4x4x4_16b_bf16 v[232:235], v[218:219], v[108:109], 0
	v_cvt_scalef32_pk_bf16_fp8 v222, v134, 1.0
	v_cvt_scalef32_pk_bf16_fp8 v223, v134, 1.0 op_sel:[1,0,0]
	v_mfma_f32_4x4x4_16b_bf16 v[232:235], v[220:221], v[110:111], v[232:235]
	v_cvt_scalef32_pk_bf16_fp8 v224, v135, 1.0
	v_cvt_scalef32_pk_bf16_fp8 v225, v135, 1.0 op_sel:[1,0,0]
	v_lshl_or_b32 v73, v73, 7, v209
	global_load_dwordx4 v[132:135], v73, s[6:7]
	v_mfma_f32_4x4x4_16b_bf16 v[232:235], v[222:223], v[100:101], v[232:235]
	v_cvt_scalef32_pk_bf16_fp8 v210, v136, 1.0
	v_cvt_scalef32_pk_bf16_fp8 v211, v136, 1.0 op_sel:[1,0,0]
	v_mfma_f32_4x4x4_16b_bf16 v[232:235], v[224:225], v[102:103], v[232:235]
	v_cvt_scalef32_pk_bf16_fp8 v212, v137, 1.0
	v_cvt_scalef32_pk_bf16_fp8 v213, v137, 1.0 op_sel:[1,0,0]
	v_cndmask_b32_e64 v188, v228, v229, s[22:23]
	v_cndmask_b32_e64 v188, v188, v230, s[24:25]
	v_cndmask_b32_e64 v188, v188, v231, s[26:27]
	v_mfma_f32_4x4x4_16b_bf16 v[228:231], v[210:211], v[108:109], 0
	v_cvt_scalef32_pk_bf16_fp8 v214, v138, 1.0
	v_cvt_scalef32_pk_bf16_fp8 v215, v138, 1.0 op_sel:[1,0,0]
	v_mfma_f32_4x4x4_16b_bf16 v[228:231], v[212:213], v[110:111], v[228:231]
	v_cvt_scalef32_pk_bf16_fp8 v216, v139, 1.0
	v_cvt_scalef32_pk_bf16_fp8 v217, v139, 1.0 op_sel:[1,0,0]
	v_lshl_or_b32 v74, v74, 7, v209
	global_load_dwordx4 v[136:139], v74, s[6:7]
	v_mfma_f32_4x4x4_16b_bf16 v[228:231], v[214:215], v[100:101], v[228:231]
	v_cvt_scalef32_pk_bf16_fp8 v218, v140, 1.0
	v_cvt_scalef32_pk_bf16_fp8 v219, v140, 1.0 op_sel:[1,0,0]
	v_mfma_f32_4x4x4_16b_bf16 v[228:231], v[216:217], v[102:103], v[228:231]
	v_cvt_scalef32_pk_bf16_fp8 v220, v141, 1.0
	v_cvt_scalef32_pk_bf16_fp8 v221, v141, 1.0 op_sel:[1,0,0]
	v_cndmask_b32_e64 v189, v232, v233, s[22:23]
	v_cndmask_b32_e64 v189, v189, v234, s[24:25]
	v_cndmask_b32_e64 v189, v189, v235, s[26:27]
	v_mfma_f32_4x4x4_16b_bf16 v[232:235], v[218:219], v[108:109], 0
	v_cvt_scalef32_pk_bf16_fp8 v222, v142, 1.0
	v_cvt_scalef32_pk_bf16_fp8 v223, v142, 1.0 op_sel:[1,0,0]
	v_mfma_f32_4x4x4_16b_bf16 v[232:235], v[220:221], v[110:111], v[232:235]
	v_cvt_scalef32_pk_bf16_fp8 v224, v143, 1.0
	v_cvt_scalef32_pk_bf16_fp8 v225, v143, 1.0 op_sel:[1,0,0]
	v_lshl_or_b32 v75, v75, 7, v209
	global_load_dwordx4 v[140:143], v75, s[6:7]
	v_mfma_f32_4x4x4_16b_bf16 v[232:235], v[222:223], v[100:101], v[232:235]
	v_cvt_scalef32_pk_bf16_fp8 v210, v144, 1.0
	v_cvt_scalef32_pk_bf16_fp8 v211, v144, 1.0 op_sel:[1,0,0]
	v_mfma_f32_4x4x4_16b_bf16 v[232:235], v[224:225], v[102:103], v[232:235]
	v_cvt_scalef32_pk_bf16_fp8 v212, v145, 1.0
	v_cvt_scalef32_pk_bf16_fp8 v213, v145, 1.0 op_sel:[1,0,0]
	v_cndmask_b32_e64 v190, v228, v229, s[22:23]
	v_cndmask_b32_e64 v190, v190, v230, s[24:25]
	v_cndmask_b32_e64 v190, v190, v231, s[26:27]
	v_mfma_f32_4x4x4_16b_bf16 v[228:231], v[210:211], v[108:109], 0
	v_cvt_scalef32_pk_bf16_fp8 v214, v146, 1.0
	v_cvt_scalef32_pk_bf16_fp8 v215, v146, 1.0 op_sel:[1,0,0]
	v_mfma_f32_4x4x4_16b_bf16 v[228:231], v[212:213], v[110:111], v[228:231]
	v_cvt_scalef32_pk_bf16_fp8 v216, v147, 1.0
	v_cvt_scalef32_pk_bf16_fp8 v217, v147, 1.0 op_sel:[1,0,0]
	v_lshl_or_b32 v68, v68, 7, v209
	global_load_dwordx4 v[144:147], v68, s[6:7]
	v_mfma_f32_4x4x4_16b_bf16 v[228:231], v[214:215], v[100:101], v[228:231]
	v_cvt_scalef32_pk_bf16_fp8 v218, v148, 1.0
	v_cvt_scalef32_pk_bf16_fp8 v219, v148, 1.0 op_sel:[1,0,0]
	v_mfma_f32_4x4x4_16b_bf16 v[228:231], v[216:217], v[102:103], v[228:231]
	v_cvt_scalef32_pk_bf16_fp8 v220, v149, 1.0
	v_cvt_scalef32_pk_bf16_fp8 v221, v149, 1.0 op_sel:[1,0,0]
	v_cndmask_b32_e64 v191, v232, v233, s[22:23]
	v_cndmask_b32_e64 v191, v191, v234, s[24:25]
	v_cndmask_b32_e64 v191, v191, v235, s[26:27]
	v_mfma_f32_4x4x4_16b_bf16 v[232:235], v[218:219], v[108:109], 0
	v_cvt_scalef32_pk_bf16_fp8 v222, v150, 1.0
	v_cvt_scalef32_pk_bf16_fp8 v223, v150, 1.0 op_sel:[1,0,0]
	v_mfma_f32_4x4x4_16b_bf16 v[232:235], v[220:221], v[110:111], v[232:235]
	v_cvt_scalef32_pk_bf16_fp8 v224, v151, 1.0
	v_cvt_scalef32_pk_bf16_fp8 v225, v151, 1.0 op_sel:[1,0,0]
	v_lshl_or_b32 v69, v69, 7, v209
	global_load_dwordx4 v[148:151], v69, s[6:7]
	v_mfma_f32_4x4x4_16b_bf16 v[232:235], v[222:223], v[100:101], v[232:235]
	v_cvt_scalef32_pk_bf16_fp8 v210, v152, 1.0
	v_cvt_scalef32_pk_bf16_fp8 v211, v152, 1.0 op_sel:[1,0,0]
	v_mfma_f32_4x4x4_16b_bf16 v[232:235], v[224:225], v[102:103], v[232:235]
	v_cvt_scalef32_pk_bf16_fp8 v212, v153, 1.0
	v_cvt_scalef32_pk_bf16_fp8 v213, v153, 1.0 op_sel:[1,0,0]
	v_cndmask_b32_e64 v192, v228, v229, s[22:23]
	v_cndmask_b32_e64 v192, v192, v230, s[24:25]
	v_cndmask_b32_e64 v192, v192, v231, s[26:27]
	v_mfma_f32_4x4x4_16b_bf16 v[228:231], v[210:211], v[108:109], 0
	v_cvt_scalef32_pk_bf16_fp8 v214, v154, 1.0
	v_cvt_scalef32_pk_bf16_fp8 v215, v154, 1.0 op_sel:[1,0,0]
	v_mfma_f32_4x4x4_16b_bf16 v[228:231], v[212:213], v[110:111], v[228:231]
	v_cvt_scalef32_pk_bf16_fp8 v216, v155, 1.0
	v_cvt_scalef32_pk_bf16_fp8 v217, v155, 1.0 op_sel:[1,0,0]
	v_lshl_or_b32 v70, v70, 7, v209
	global_load_dwordx4 v[152:155], v70, s[6:7]
	v_mfma_f32_4x4x4_16b_bf16 v[228:231], v[214:215], v[100:101], v[228:231]
	v_cvt_scalef32_pk_bf16_fp8 v218, v156, 1.0
	v_cvt_scalef32_pk_bf16_fp8 v219, v156, 1.0 op_sel:[1,0,0]
	v_mfma_f32_4x4x4_16b_bf16 v[228:231], v[216:217], v[102:103], v[228:231]
	v_cvt_scalef32_pk_bf16_fp8 v220, v157, 1.0
	v_cvt_scalef32_pk_bf16_fp8 v221, v157, 1.0 op_sel:[1,0,0]
	v_cndmask_b32_e64 v193, v232, v233, s[22:23]
	v_cndmask_b32_e64 v193, v193, v234, s[24:25]
	v_cndmask_b32_e64 v193, v193, v235, s[26:27]
	v_mfma_f32_4x4x4_16b_bf16 v[232:235], v[218:219], v[108:109], 0
	v_cvt_scalef32_pk_bf16_fp8 v222, v158, 1.0
	v_cvt_scalef32_pk_bf16_fp8 v223, v158, 1.0 op_sel:[1,0,0]
	v_mfma_f32_4x4x4_16b_bf16 v[232:235], v[220:221], v[110:111], v[232:235]
	v_cvt_scalef32_pk_bf16_fp8 v224, v159, 1.0
	v_cvt_scalef32_pk_bf16_fp8 v225, v159, 1.0 op_sel:[1,0,0]
	v_lshl_or_b32 v71, v71, 7, v209
	global_load_dwordx4 v[156:159], v71, s[6:7]
	v_mfma_f32_4x4x4_16b_bf16 v[232:235], v[222:223], v[100:101], v[232:235]
	v_cvt_scalef32_pk_bf16_fp8 v210, v160, 1.0
	v_cvt_scalef32_pk_bf16_fp8 v211, v160, 1.0 op_sel:[1,0,0]
	v_mfma_f32_4x4x4_16b_bf16 v[232:235], v[224:225], v[102:103], v[232:235]
	v_cvt_scalef32_pk_bf16_fp8 v212, v161, 1.0
	v_cvt_scalef32_pk_bf16_fp8 v213, v161, 1.0 op_sel:[1,0,0]
	v_cndmask_b32_e64 v194, v228, v229, s[22:23]
	v_cndmask_b32_e64 v194, v194, v230, s[24:25]
	v_cndmask_b32_e64 v194, v194, v231, s[26:27]
	v_mfma_f32_4x4x4_16b_bf16 v[228:231], v[210:211], v[108:109], 0
	v_cvt_scalef32_pk_bf16_fp8 v214, v162, 1.0
	v_cvt_scalef32_pk_bf16_fp8 v215, v162, 1.0 op_sel:[1,0,0]
	v_mfma_f32_4x4x4_16b_bf16 v[228:231], v[212:213], v[110:111], v[228:231]
	v_cvt_scalef32_pk_bf16_fp8 v216, v163, 1.0
	v_cvt_scalef32_pk_bf16_fp8 v217, v163, 1.0 op_sel:[1,0,0]
	v_lshl_or_b32 v64, v64, 7, v209
	global_load_dwordx4 v[160:163], v64, s[6:7]
	v_mfma_f32_4x4x4_16b_bf16 v[228:231], v[214:215], v[100:101], v[228:231]
	v_cvt_scalef32_pk_bf16_fp8 v218, v164, 1.0
	v_cvt_scalef32_pk_bf16_fp8 v219, v164, 1.0 op_sel:[1,0,0]
	v_mfma_f32_4x4x4_16b_bf16 v[228:231], v[216:217], v[102:103], v[228:231]
	v_cvt_scalef32_pk_bf16_fp8 v220, v165, 1.0
	v_cvt_scalef32_pk_bf16_fp8 v221, v165, 1.0 op_sel:[1,0,0]
	v_cndmask_b32_e64 v195, v232, v233, s[22:23]
	v_cndmask_b32_e64 v195, v195, v234, s[24:25]
	v_cndmask_b32_e64 v195, v195, v235, s[26:27]
	v_mfma_f32_4x4x4_16b_bf16 v[232:235], v[218:219], v[108:109], 0
	v_cvt_scalef32_pk_bf16_fp8 v222, v166, 1.0
	v_cvt_scalef32_pk_bf16_fp8 v223, v166, 1.0 op_sel:[1,0,0]
	v_mfma_f32_4x4x4_16b_bf16 v[232:235], v[220:221], v[110:111], v[232:235]
	v_cvt_scalef32_pk_bf16_fp8 v224, v167, 1.0
	v_cvt_scalef32_pk_bf16_fp8 v225, v167, 1.0 op_sel:[1,0,0]
	v_lshl_or_b32 v65, v65, 7, v209
	global_load_dwordx4 v[164:167], v65, s[6:7]
	v_mfma_f32_4x4x4_16b_bf16 v[232:235], v[222:223], v[100:101], v[232:235]
	v_cvt_scalef32_pk_bf16_fp8 v210, v168, 1.0
	v_cvt_scalef32_pk_bf16_fp8 v211, v168, 1.0 op_sel:[1,0,0]
	v_mfma_f32_4x4x4_16b_bf16 v[232:235], v[224:225], v[102:103], v[232:235]
	v_cvt_scalef32_pk_bf16_fp8 v212, v169, 1.0
	v_cvt_scalef32_pk_bf16_fp8 v213, v169, 1.0 op_sel:[1,0,0]
	v_cndmask_b32_e64 v196, v228, v229, s[22:23]
	v_cndmask_b32_e64 v196, v196, v230, s[24:25]
	v_cndmask_b32_e64 v196, v196, v231, s[26:27]
	v_mfma_f32_4x4x4_16b_bf16 v[228:231], v[210:211], v[108:109], 0
	v_cvt_scalef32_pk_bf16_fp8 v214, v170, 1.0
	v_cvt_scalef32_pk_bf16_fp8 v215, v170, 1.0 op_sel:[1,0,0]
	v_mfma_f32_4x4x4_16b_bf16 v[228:231], v[212:213], v[110:111], v[228:231]
	v_cvt_scalef32_pk_bf16_fp8 v216, v171, 1.0
	v_cvt_scalef32_pk_bf16_fp8 v217, v171, 1.0 op_sel:[1,0,0]
	v_lshl_or_b32 v66, v66, 7, v209
	global_load_dwordx4 v[168:171], v66, s[6:7]
	v_mfma_f32_4x4x4_16b_bf16 v[228:231], v[214:215], v[100:101], v[228:231]
	v_cvt_scalef32_pk_bf16_fp8 v218, v172, 1.0
	v_cvt_scalef32_pk_bf16_fp8 v219, v172, 1.0 op_sel:[1,0,0]
	v_mfma_f32_4x4x4_16b_bf16 v[228:231], v[216:217], v[102:103], v[228:231]
	v_cvt_scalef32_pk_bf16_fp8 v220, v173, 1.0
	v_cvt_scalef32_pk_bf16_fp8 v221, v173, 1.0 op_sel:[1,0,0]
	v_cndmask_b32_e64 v197, v232, v233, s[22:23]
	v_cndmask_b32_e64 v197, v197, v234, s[24:25]
	v_cndmask_b32_e64 v197, v197, v235, s[26:27]
	v_mfma_f32_4x4x4_16b_bf16 v[232:235], v[218:219], v[108:109], 0
	v_cvt_scalef32_pk_bf16_fp8 v222, v174, 1.0
	v_cvt_scalef32_pk_bf16_fp8 v223, v174, 1.0 op_sel:[1,0,0]
	v_mfma_f32_4x4x4_16b_bf16 v[232:235], v[220:221], v[110:111], v[232:235]
	v_cvt_scalef32_pk_bf16_fp8 v224, v175, 1.0
	v_cvt_scalef32_pk_bf16_fp8 v225, v175, 1.0 op_sel:[1,0,0]
	v_lshl_or_b32 v67, v67, 7, v209
	global_load_dwordx4 v[172:175], v67, s[6:7]
	v_mfma_f32_4x4x4_16b_bf16 v[232:235], v[222:223], v[100:101], v[232:235]
	s_nop 1
	v_mfma_f32_4x4x4_16b_bf16 v[232:235], v[224:225], v[102:103], v[232:235]
	v_cndmask_b32_e64 v198, v228, v229, s[22:23]
	v_cndmask_b32_e64 v198, v198, v230, s[24:25]
	v_cndmask_b32_e64 v198, v198, v231, s[26:27]
	s_nop 4
	v_cndmask_b32_e64 v199, v232, v233, s[22:23]
	v_cndmask_b32_e64 v199, v199, v234, s[24:25]
	v_cndmask_b32_e64 v199, v199, v235, s[26:27]
	v_cndmask_b32_e64 v200, v184, v192, s[4:5]
	v_cndmask_b32_e64 v201, v192, v184, s[4:5]
	v_cndmask_b32_e64 v202, v185, v193, s[4:5]
	v_cndmask_b32_e64 v203, v193, v185, s[4:5]
	v_cndmask_b32_e64 v204, v186, v194, s[4:5]
	v_cndmask_b32_e64 v205, v194, v186, s[4:5]
	v_cndmask_b32_e64 v236, v187, v195, s[4:5]
	v_cndmask_b32_e64 v237, v195, v187, s[4:5]
	v_cndmask_b32_e64 v238, v188, v196, s[4:5]
	v_cndmask_b32_e64 v239, v196, v188, s[4:5]
	v_cndmask_b32_e64 v240, v189, v197, s[4:5]
	v_cndmask_b32_e64 v241, v197, v189, s[4:5]
	v_cndmask_b32_e64 v242, v190, v198, s[4:5]
	v_cndmask_b32_e64 v243, v198, v190, s[4:5]
	v_cndmask_b32_e64 v244, v191, v199, s[4:5]
	v_cndmask_b32_e64 v245, v199, v191, s[4:5]
	v_add_f32_dpp v246, v200, v201 row_half_mirror row_mask:0xf bank_mask:0xf
	v_add_f32_dpp v247, v202, v203 row_half_mirror row_mask:0xf bank_mask:0xf
	v_add_f32_dpp v248, v204, v205 row_half_mirror row_mask:0xf bank_mask:0xf
	v_add_f32_dpp v249, v236, v237 row_half_mirror row_mask:0xf bank_mask:0xf
	v_add_f32_dpp v226, v238, v239 row_half_mirror row_mask:0xf bank_mask:0xf
	v_add_f32_dpp v227, v240, v241 row_half_mirror row_mask:0xf bank_mask:0xf
	v_add_f32_dpp v210, v242, v243 row_half_mirror row_mask:0xf bank_mask:0xf
	v_add_f32_dpp v211, v244, v245 row_half_mirror row_mask:0xf bank_mask:0xf
	v_cndmask_b32_e64 v200, v246, v226, s[2:3]
	v_cndmask_b32_e64 v201, v226, v246, s[2:3]
	v_cndmask_b32_e64 v202, v247, v227, s[2:3]
	v_cndmask_b32_e64 v203, v227, v247, s[2:3]
	v_cndmask_b32_e64 v204, v248, v210, s[2:3]
	v_cndmask_b32_e64 v205, v210, v248, s[2:3]
	v_cndmask_b32_e64 v236, v249, v211, s[2:3]
	v_cndmask_b32_e64 v237, v211, v249, s[2:3]
	v_add_f32_dpp v212, v200, v201 quad_perm:[2,3,0,1] row_mask:0xf bank_mask:0xf
	v_add_f32_dpp v213, v202, v203 quad_perm:[2,3,0,1] row_mask:0xf bank_mask:0xf
	v_add_f32_dpp v214, v204, v205 quad_perm:[2,3,0,1] row_mask:0xf bank_mask:0xf
	v_add_f32_dpp v215, v236, v237 quad_perm:[2,3,0,1] row_mask:0xf bank_mask:0xf
	v_cndmask_b32_e64 v200, v212, v214, s[0:1]
	v_cndmask_b32_e64 v201, v214, v212, s[0:1]
	v_cndmask_b32_e64 v202, v213, v215, s[0:1]
	v_cndmask_b32_e64 v203, v215, v213, s[0:1]
	s_nop 1
	v_add_f32_dpp v216, v200, v201 quad_perm:[1,0,3,2] row_mask:0xf bank_mask:0xf
	v_add_f32_dpp v217, v202, v203 quad_perm:[1,0,3,2] row_mask:0xf bank_mask:0xf
	s_ashr_i32 s11, s10, 31
	s_lshl_b64 s[10:11], s[10:11], 8
	v_cvt_pk_bf16_f32 v186, v216, v217
	v_lshl_add_u64 v[184:185], v[178:179], 0, s[10:11]
	global_store_dword v[184:185], v186, off
	s_add_u32 s20, s12, 0x300
	s_lshl_b32 s20, s20, 11
	v_lshl_add_u64 v[108:109], v[182:183], 0, s[20:21]
	global_load_dwordx4 v[100:103], v[108:109], off offset:16
	s_nop 0
	global_load_dwordx4 v[108:111], v[108:109], off
	s_add_u32 s12, s12, 0x200
	s_mov_b32 s14, s12
	s_waitcnt vmcnt(19)
	v_cvt_scalef32_pk_bf16_fp8 v210, v24, 1.0
	v_cvt_scalef32_pk_bf16_fp8 v211, v24, 1.0 op_sel:[1,0,0]
	v_cvt_scalef32_pk_bf16_fp8 v212, v25, 1.0
	v_cvt_scalef32_pk_bf16_fp8 v213, v25, 1.0 op_sel:[1,0,0]
	v_mfma_f32_4x4x4_16b_bf16 v[228:231], v[210:211], v[20:21], 0
	v_cvt_scalef32_pk_bf16_fp8 v214, v26, 1.0
	v_cvt_scalef32_pk_bf16_fp8 v215, v26, 1.0 op_sel:[1,0,0]
	v_mfma_f32_4x4x4_16b_bf16 v[228:231], v[212:213], v[22:23], v[228:231]
	v_cvt_scalef32_pk_bf16_fp8 v216, v27, 1.0
	v_cvt_scalef32_pk_bf16_fp8 v217, v27, 1.0 op_sel:[1,0,0]
	v_mfma_f32_4x4x4_16b_bf16 v[228:231], v[214:215], v[16:17], v[228:231]
	v_cvt_scalef32_pk_bf16_fp8 v218, v28, 1.0
	v_cvt_scalef32_pk_bf16_fp8 v219, v28, 1.0 op_sel:[1,0,0]
	v_mfma_f32_4x4x4_16b_bf16 v[228:231], v[216:217], v[18:19], v[228:231]
	v_cvt_scalef32_pk_bf16_fp8 v220, v29, 1.0
	v_cvt_scalef32_pk_bf16_fp8 v221, v29, 1.0 op_sel:[1,0,0]
	v_mfma_f32_4x4x4_16b_bf16 v[232:235], v[218:219], v[20:21], 0
	v_cvt_scalef32_pk_bf16_fp8 v222, v30, 1.0
	v_cvt_scalef32_pk_bf16_fp8 v223, v30, 1.0 op_sel:[1,0,0]
	v_mfma_f32_4x4x4_16b_bf16 v[232:235], v[220:221], v[22:23], v[232:235]
	v_cvt_scalef32_pk_bf16_fp8 v224, v31, 1.0
	v_cvt_scalef32_pk_bf16_fp8 v225, v31, 1.0 op_sel:[1,0,0]
	v_mfma_f32_4x4x4_16b_bf16 v[232:235], v[222:223], v[16:17], v[232:235]
	v_cvt_scalef32_pk_bf16_fp8 v210, v32, 1.0
	v_cvt_scalef32_pk_bf16_fp8 v211, v32, 1.0 op_sel:[1,0,0]
	v_mfma_f32_4x4x4_16b_bf16 v[232:235], v[224:225], v[18:19], v[232:235]
	v_cvt_scalef32_pk_bf16_fp8 v212, v33, 1.0
	v_cvt_scalef32_pk_bf16_fp8 v213, v33, 1.0 op_sel:[1,0,0]
	v_cndmask_b32_e64 v184, v228, v229, s[22:23]
	v_cndmask_b32_e64 v184, v184, v230, s[24:25]
	v_cndmask_b32_e64 v184, v184, v231, s[26:27]
	v_mfma_f32_4x4x4_16b_bf16 v[228:231], v[210:211], v[20:21], 0
	v_cvt_scalef32_pk_bf16_fp8 v214, v34, 1.0
	v_cvt_scalef32_pk_bf16_fp8 v215, v34, 1.0 op_sel:[1,0,0]
	v_mfma_f32_4x4x4_16b_bf16 v[228:231], v[212:213], v[22:23], v[228:231]
	v_cvt_scalef32_pk_bf16_fp8 v216, v35, 1.0
	v_cvt_scalef32_pk_bf16_fp8 v217, v35, 1.0 op_sel:[1,0,0]
	v_mfma_f32_4x4x4_16b_bf16 v[228:231], v[214:215], v[16:17], v[228:231]
	v_cvt_scalef32_pk_bf16_fp8 v218, v36, 1.0
	v_cvt_scalef32_pk_bf16_fp8 v219, v36, 1.0 op_sel:[1,0,0]
	v_mfma_f32_4x4x4_16b_bf16 v[228:231], v[216:217], v[18:19], v[228:231]
	v_cvt_scalef32_pk_bf16_fp8 v220, v37, 1.0
	v_cvt_scalef32_pk_bf16_fp8 v221, v37, 1.0 op_sel:[1,0,0]
	v_cndmask_b32_e64 v185, v232, v233, s[22:23]
	v_cndmask_b32_e64 v185, v185, v234, s[24:25]
	v_cndmask_b32_e64 v185, v185, v235, s[26:27]
	v_mfma_f32_4x4x4_16b_bf16 v[232:235], v[218:219], v[20:21], 0
	v_cvt_scalef32_pk_bf16_fp8 v222, v38, 1.0
	v_cvt_scalef32_pk_bf16_fp8 v223, v38, 1.0 op_sel:[1,0,0]
	v_mfma_f32_4x4x4_16b_bf16 v[232:235], v[220:221], v[22:23], v[232:235]
	v_cvt_scalef32_pk_bf16_fp8 v224, v39, 1.0
	v_cvt_scalef32_pk_bf16_fp8 v225, v39, 1.0 op_sel:[1,0,0]
	v_mfma_f32_4x4x4_16b_bf16 v[232:235], v[222:223], v[16:17], v[232:235]
	v_cvt_scalef32_pk_bf16_fp8 v210, v40, 1.0
	v_cvt_scalef32_pk_bf16_fp8 v211, v40, 1.0 op_sel:[1,0,0]
	v_mfma_f32_4x4x4_16b_bf16 v[232:235], v[224:225], v[18:19], v[232:235]
	v_cvt_scalef32_pk_bf16_fp8 v212, v41, 1.0
	v_cvt_scalef32_pk_bf16_fp8 v213, v41, 1.0 op_sel:[1,0,0]
	v_cndmask_b32_e64 v186, v228, v229, s[22:23]
	v_cndmask_b32_e64 v186, v186, v230, s[24:25]
	v_cndmask_b32_e64 v186, v186, v231, s[26:27]
	v_mfma_f32_4x4x4_16b_bf16 v[228:231], v[210:211], v[20:21], 0
	v_cvt_scalef32_pk_bf16_fp8 v214, v42, 1.0
	v_cvt_scalef32_pk_bf16_fp8 v215, v42, 1.0 op_sel:[1,0,0]
	v_mfma_f32_4x4x4_16b_bf16 v[228:231], v[212:213], v[22:23], v[228:231]
	v_cvt_scalef32_pk_bf16_fp8 v216, v43, 1.0
	v_cvt_scalef32_pk_bf16_fp8 v217, v43, 1.0 op_sel:[1,0,0]
	v_mfma_f32_4x4x4_16b_bf16 v[228:231], v[214:215], v[16:17], v[228:231]
	v_cvt_scalef32_pk_bf16_fp8 v218, v44, 1.0
	v_cvt_scalef32_pk_bf16_fp8 v219, v44, 1.0 op_sel:[1,0,0]
	v_mfma_f32_4x4x4_16b_bf16 v[228:231], v[216:217], v[18:19], v[228:231]
	v_cvt_scalef32_pk_bf16_fp8 v220, v45, 1.0
	v_cvt_scalef32_pk_bf16_fp8 v221, v45, 1.0 op_sel:[1,0,0]
	v_cndmask_b32_e64 v187, v232, v233, s[22:23]
	v_cndmask_b32_e64 v187, v187, v234, s[24:25]
	v_cndmask_b32_e64 v187, v187, v235, s[26:27]
	v_mfma_f32_4x4x4_16b_bf16 v[232:235], v[218:219], v[20:21], 0
	v_cvt_scalef32_pk_bf16_fp8 v222, v46, 1.0
	v_cvt_scalef32_pk_bf16_fp8 v223, v46, 1.0 op_sel:[1,0,0]
	v_mfma_f32_4x4x4_16b_bf16 v[232:235], v[220:221], v[22:23], v[232:235]
	v_cvt_scalef32_pk_bf16_fp8 v224, v47, 1.0
	v_cvt_scalef32_pk_bf16_fp8 v225, v47, 1.0 op_sel:[1,0,0]
	v_mfma_f32_4x4x4_16b_bf16 v[232:235], v[222:223], v[16:17], v[232:235]
	v_cvt_scalef32_pk_bf16_fp8 v210, v48, 1.0
	v_cvt_scalef32_pk_bf16_fp8 v211, v48, 1.0 op_sel:[1,0,0]
	v_mfma_f32_4x4x4_16b_bf16 v[232:235], v[224:225], v[18:19], v[232:235]
	v_cvt_scalef32_pk_bf16_fp8 v212, v49, 1.0
	v_cvt_scalef32_pk_bf16_fp8 v213, v49, 1.0 op_sel:[1,0,0]
	v_cndmask_b32_e64 v188, v228, v229, s[22:23]
	v_cndmask_b32_e64 v188, v188, v230, s[24:25]
	v_cndmask_b32_e64 v188, v188, v231, s[26:27]
	v_mfma_f32_4x4x4_16b_bf16 v[228:231], v[210:211], v[20:21], 0
	v_cvt_scalef32_pk_bf16_fp8 v214, v50, 1.0
	v_cvt_scalef32_pk_bf16_fp8 v215, v50, 1.0 op_sel:[1,0,0]
	v_mfma_f32_4x4x4_16b_bf16 v[228:231], v[212:213], v[22:23], v[228:231]
	v_cvt_scalef32_pk_bf16_fp8 v216, v51, 1.0
	v_cvt_scalef32_pk_bf16_fp8 v217, v51, 1.0 op_sel:[1,0,0]
	v_mfma_f32_4x4x4_16b_bf16 v[228:231], v[214:215], v[16:17], v[228:231]
	v_cvt_scalef32_pk_bf16_fp8 v218, v52, 1.0
	v_cvt_scalef32_pk_bf16_fp8 v219, v52, 1.0 op_sel:[1,0,0]
	v_mfma_f32_4x4x4_16b_bf16 v[228:231], v[216:217], v[18:19], v[228:231]
	v_cvt_scalef32_pk_bf16_fp8 v220, v53, 1.0
	v_cvt_scalef32_pk_bf16_fp8 v221, v53, 1.0 op_sel:[1,0,0]
	v_cndmask_b32_e64 v189, v232, v233, s[22:23]
	v_cndmask_b32_e64 v189, v189, v234, s[24:25]
	v_cndmask_b32_e64 v189, v189, v235, s[26:27]
	v_mfma_f32_4x4x4_16b_bf16 v[232:235], v[218:219], v[20:21], 0
	v_cvt_scalef32_pk_bf16_fp8 v222, v54, 1.0
	v_cvt_scalef32_pk_bf16_fp8 v223, v54, 1.0 op_sel:[1,0,0]
	v_mfma_f32_4x4x4_16b_bf16 v[232:235], v[220:221], v[22:23], v[232:235]
	v_cvt_scalef32_pk_bf16_fp8 v224, v55, 1.0
	v_cvt_scalef32_pk_bf16_fp8 v225, v55, 1.0 op_sel:[1,0,0]
	v_mfma_f32_4x4x4_16b_bf16 v[232:235], v[222:223], v[16:17], v[232:235]
	v_cvt_scalef32_pk_bf16_fp8 v210, v56, 1.0
	v_cvt_scalef32_pk_bf16_fp8 v211, v56, 1.0 op_sel:[1,0,0]
	v_mfma_f32_4x4x4_16b_bf16 v[232:235], v[224:225], v[18:19], v[232:235]
	v_cvt_scalef32_pk_bf16_fp8 v212, v57, 1.0
	v_cvt_scalef32_pk_bf16_fp8 v213, v57, 1.0 op_sel:[1,0,0]
	v_cndmask_b32_e64 v190, v228, v229, s[22:23]
	v_cndmask_b32_e64 v190, v190, v230, s[24:25]
	v_cndmask_b32_e64 v190, v190, v231, s[26:27]
	v_mfma_f32_4x4x4_16b_bf16 v[228:231], v[210:211], v[20:21], 0
	v_cvt_scalef32_pk_bf16_fp8 v214, v58, 1.0
	v_cvt_scalef32_pk_bf16_fp8 v215, v58, 1.0 op_sel:[1,0,0]
	v_mfma_f32_4x4x4_16b_bf16 v[228:231], v[212:213], v[22:23], v[228:231]
	v_cvt_scalef32_pk_bf16_fp8 v216, v59, 1.0
	v_cvt_scalef32_pk_bf16_fp8 v217, v59, 1.0 op_sel:[1,0,0]
	v_mfma_f32_4x4x4_16b_bf16 v[228:231], v[214:215], v[16:17], v[228:231]
	v_cvt_scalef32_pk_bf16_fp8 v218, v60, 1.0
	v_cvt_scalef32_pk_bf16_fp8 v219, v60, 1.0 op_sel:[1,0,0]
	v_mfma_f32_4x4x4_16b_bf16 v[228:231], v[216:217], v[18:19], v[228:231]
	v_cvt_scalef32_pk_bf16_fp8 v220, v61, 1.0
	v_cvt_scalef32_pk_bf16_fp8 v221, v61, 1.0 op_sel:[1,0,0]
	v_cndmask_b32_e64 v191, v232, v233, s[22:23]
	v_cndmask_b32_e64 v191, v191, v234, s[24:25]
	v_cndmask_b32_e64 v191, v191, v235, s[26:27]
	v_mfma_f32_4x4x4_16b_bf16 v[232:235], v[218:219], v[20:21], 0
	v_cvt_scalef32_pk_bf16_fp8 v222, v62, 1.0
	v_cvt_scalef32_pk_bf16_fp8 v223, v62, 1.0 op_sel:[1,0,0]
	v_mfma_f32_4x4x4_16b_bf16 v[232:235], v[220:221], v[22:23], v[232:235]
	v_cvt_scalef32_pk_bf16_fp8 v224, v63, 1.0
	v_cvt_scalef32_pk_bf16_fp8 v225, v63, 1.0 op_sel:[1,0,0]
	v_mfma_f32_4x4x4_16b_bf16 v[232:235], v[222:223], v[16:17], v[232:235]
	v_cvt_scalef32_pk_bf16_fp8 v210, v76, 1.0
	v_cvt_scalef32_pk_bf16_fp8 v211, v76, 1.0 op_sel:[1,0,0]
	v_mfma_f32_4x4x4_16b_bf16 v[232:235], v[224:225], v[18:19], v[232:235]
	v_cvt_scalef32_pk_bf16_fp8 v212, v77, 1.0
	v_cvt_scalef32_pk_bf16_fp8 v213, v77, 1.0 op_sel:[1,0,0]
	v_cndmask_b32_e64 v192, v228, v229, s[22:23]
	v_cndmask_b32_e64 v192, v192, v230, s[24:25]
	v_cndmask_b32_e64 v192, v192, v231, s[26:27]
	v_mfma_f32_4x4x4_16b_bf16 v[228:231], v[210:211], v[20:21], 0
	v_cvt_scalef32_pk_bf16_fp8 v214, v78, 1.0
	v_cvt_scalef32_pk_bf16_fp8 v215, v78, 1.0 op_sel:[1,0,0]
	v_mfma_f32_4x4x4_16b_bf16 v[228:231], v[212:213], v[22:23], v[228:231]
	v_cvt_scalef32_pk_bf16_fp8 v216, v79, 1.0
	v_cvt_scalef32_pk_bf16_fp8 v217, v79, 1.0 op_sel:[1,0,0]
	v_mfma_f32_4x4x4_16b_bf16 v[228:231], v[214:215], v[16:17], v[228:231]
	v_cvt_scalef32_pk_bf16_fp8 v218, v84, 1.0
	v_cvt_scalef32_pk_bf16_fp8 v219, v84, 1.0 op_sel:[1,0,0]
	v_mfma_f32_4x4x4_16b_bf16 v[228:231], v[216:217], v[18:19], v[228:231]
	v_cvt_scalef32_pk_bf16_fp8 v220, v85, 1.0
	v_cvt_scalef32_pk_bf16_fp8 v221, v85, 1.0 op_sel:[1,0,0]
	v_cndmask_b32_e64 v193, v232, v233, s[22:23]
	v_cndmask_b32_e64 v193, v193, v234, s[24:25]
	v_cndmask_b32_e64 v193, v193, v235, s[26:27]
	v_mfma_f32_4x4x4_16b_bf16 v[232:235], v[218:219], v[20:21], 0
	v_cvt_scalef32_pk_bf16_fp8 v222, v86, 1.0
	v_cvt_scalef32_pk_bf16_fp8 v223, v86, 1.0 op_sel:[1,0,0]
	v_mfma_f32_4x4x4_16b_bf16 v[232:235], v[220:221], v[22:23], v[232:235]
	v_cvt_scalef32_pk_bf16_fp8 v224, v87, 1.0
	v_cvt_scalef32_pk_bf16_fp8 v225, v87, 1.0 op_sel:[1,0,0]
	v_mfma_f32_4x4x4_16b_bf16 v[232:235], v[222:223], v[16:17], v[232:235]
	v_cvt_scalef32_pk_bf16_fp8 v210, v88, 1.0
	v_cvt_scalef32_pk_bf16_fp8 v211, v88, 1.0 op_sel:[1,0,0]
	v_mfma_f32_4x4x4_16b_bf16 v[232:235], v[224:225], v[18:19], v[232:235]
	v_cvt_scalef32_pk_bf16_fp8 v212, v89, 1.0
	v_cvt_scalef32_pk_bf16_fp8 v213, v89, 1.0 op_sel:[1,0,0]
	v_cndmask_b32_e64 v194, v228, v229, s[22:23]
	v_cndmask_b32_e64 v194, v194, v230, s[24:25]
	v_cndmask_b32_e64 v194, v194, v231, s[26:27]
	v_mfma_f32_4x4x4_16b_bf16 v[228:231], v[210:211], v[20:21], 0
	v_cvt_scalef32_pk_bf16_fp8 v214, v90, 1.0
	v_cvt_scalef32_pk_bf16_fp8 v215, v90, 1.0 op_sel:[1,0,0]
	v_mfma_f32_4x4x4_16b_bf16 v[228:231], v[212:213], v[22:23], v[228:231]
	v_cvt_scalef32_pk_bf16_fp8 v216, v91, 1.0
	v_cvt_scalef32_pk_bf16_fp8 v217, v91, 1.0 op_sel:[1,0,0]
	v_mfma_f32_4x4x4_16b_bf16 v[228:231], v[214:215], v[16:17], v[228:231]
	v_cvt_scalef32_pk_bf16_fp8 v218, v92, 1.0
	v_cvt_scalef32_pk_bf16_fp8 v219, v92, 1.0 op_sel:[1,0,0]
	v_mfma_f32_4x4x4_16b_bf16 v[228:231], v[216:217], v[18:19], v[228:231]
	v_cvt_scalef32_pk_bf16_fp8 v220, v93, 1.0
	v_cvt_scalef32_pk_bf16_fp8 v221, v93, 1.0 op_sel:[1,0,0]
	v_cndmask_b32_e64 v195, v232, v233, s[22:23]
	v_cndmask_b32_e64 v195, v195, v234, s[24:25]
	v_cndmask_b32_e64 v195, v195, v235, s[26:27]
	v_mfma_f32_4x4x4_16b_bf16 v[232:235], v[218:219], v[20:21], 0
	v_cvt_scalef32_pk_bf16_fp8 v222, v94, 1.0
	v_cvt_scalef32_pk_bf16_fp8 v223, v94, 1.0 op_sel:[1,0,0]
	v_mfma_f32_4x4x4_16b_bf16 v[232:235], v[220:221], v[22:23], v[232:235]
	v_cvt_scalef32_pk_bf16_fp8 v224, v95, 1.0
	v_cvt_scalef32_pk_bf16_fp8 v225, v95, 1.0 op_sel:[1,0,0]
	v_mfma_f32_4x4x4_16b_bf16 v[232:235], v[222:223], v[16:17], v[232:235]
	v_cvt_scalef32_pk_bf16_fp8 v210, v96, 1.0
	v_cvt_scalef32_pk_bf16_fp8 v211, v96, 1.0 op_sel:[1,0,0]
	v_mfma_f32_4x4x4_16b_bf16 v[232:235], v[224:225], v[18:19], v[232:235]
	v_cvt_scalef32_pk_bf16_fp8 v212, v97, 1.0
	v_cvt_scalef32_pk_bf16_fp8 v213, v97, 1.0 op_sel:[1,0,0]
	v_cndmask_b32_e64 v196, v228, v229, s[22:23]
	v_cndmask_b32_e64 v196, v196, v230, s[24:25]
	v_cndmask_b32_e64 v196, v196, v231, s[26:27]
	v_mfma_f32_4x4x4_16b_bf16 v[228:231], v[210:211], v[20:21], 0
	v_cvt_scalef32_pk_bf16_fp8 v214, v98, 1.0
	v_cvt_scalef32_pk_bf16_fp8 v215, v98, 1.0 op_sel:[1,0,0]
	v_mfma_f32_4x4x4_16b_bf16 v[228:231], v[212:213], v[22:23], v[228:231]
	v_cvt_scalef32_pk_bf16_fp8 v216, v99, 1.0
	v_cvt_scalef32_pk_bf16_fp8 v217, v99, 1.0 op_sel:[1,0,0]
	v_mfma_f32_4x4x4_16b_bf16 v[228:231], v[214:215], v[16:17], v[228:231]
	v_cvt_scalef32_pk_bf16_fp8 v218, v104, 1.0
	v_cvt_scalef32_pk_bf16_fp8 v219, v104, 1.0 op_sel:[1,0,0]
	v_mfma_f32_4x4x4_16b_bf16 v[228:231], v[216:217], v[18:19], v[228:231]
	v_cvt_scalef32_pk_bf16_fp8 v220, v105, 1.0
	v_cvt_scalef32_pk_bf16_fp8 v221, v105, 1.0 op_sel:[1,0,0]
	v_cndmask_b32_e64 v197, v232, v233, s[22:23]
	v_cndmask_b32_e64 v197, v197, v234, s[24:25]
	v_cndmask_b32_e64 v197, v197, v235, s[26:27]
	v_mfma_f32_4x4x4_16b_bf16 v[232:235], v[218:219], v[20:21], 0
	v_cvt_scalef32_pk_bf16_fp8 v222, v106, 1.0
	v_cvt_scalef32_pk_bf16_fp8 v223, v106, 1.0 op_sel:[1,0,0]
	v_mfma_f32_4x4x4_16b_bf16 v[232:235], v[220:221], v[22:23], v[232:235]
	v_cvt_scalef32_pk_bf16_fp8 v224, v107, 1.0
	v_cvt_scalef32_pk_bf16_fp8 v225, v107, 1.0 op_sel:[1,0,0]
	v_mfma_f32_4x4x4_16b_bf16 v[232:235], v[222:223], v[16:17], v[232:235]
	s_nop 1
	v_mfma_f32_4x4x4_16b_bf16 v[232:235], v[224:225], v[18:19], v[232:235]
	v_cndmask_b32_e64 v198, v228, v229, s[22:23]
	v_cndmask_b32_e64 v198, v198, v230, s[24:25]
	v_cndmask_b32_e64 v198, v198, v231, s[26:27]
	s_nop 4
	v_cndmask_b32_e64 v199, v232, v233, s[22:23]
	v_cndmask_b32_e64 v199, v199, v234, s[24:25]
	v_cndmask_b32_e64 v199, v199, v235, s[26:27]
	v_cndmask_b32_e64 v200, v184, v192, s[4:5]
	v_cndmask_b32_e64 v201, v192, v184, s[4:5]
	v_cndmask_b32_e64 v202, v185, v193, s[4:5]
	v_cndmask_b32_e64 v203, v193, v185, s[4:5]
	v_cndmask_b32_e64 v204, v186, v194, s[4:5]
	v_cndmask_b32_e64 v205, v194, v186, s[4:5]
	v_cndmask_b32_e64 v236, v187, v195, s[4:5]
	v_cndmask_b32_e64 v237, v195, v187, s[4:5]
	v_cndmask_b32_e64 v238, v188, v196, s[4:5]
	v_cndmask_b32_e64 v239, v196, v188, s[4:5]
	v_cndmask_b32_e64 v240, v189, v197, s[4:5]
	v_cndmask_b32_e64 v241, v197, v189, s[4:5]
	v_cndmask_b32_e64 v242, v190, v198, s[4:5]
	v_cndmask_b32_e64 v243, v198, v190, s[4:5]
	v_cndmask_b32_e64 v244, v191, v199, s[4:5]
	v_cndmask_b32_e64 v245, v199, v191, s[4:5]
	v_add_f32_dpp v246, v200, v201 row_half_mirror row_mask:0xf bank_mask:0xf
	v_add_f32_dpp v247, v202, v203 row_half_mirror row_mask:0xf bank_mask:0xf
	v_add_f32_dpp v248, v204, v205 row_half_mirror row_mask:0xf bank_mask:0xf
	v_add_f32_dpp v249, v236, v237 row_half_mirror row_mask:0xf bank_mask:0xf
	v_add_f32_dpp v226, v238, v239 row_half_mirror row_mask:0xf bank_mask:0xf
	v_add_f32_dpp v227, v240, v241 row_half_mirror row_mask:0xf bank_mask:0xf
	v_add_f32_dpp v210, v242, v243 row_half_mirror row_mask:0xf bank_mask:0xf
	v_add_f32_dpp v211, v244, v245 row_half_mirror row_mask:0xf bank_mask:0xf
	v_cndmask_b32_e64 v200, v246, v226, s[2:3]
	v_cndmask_b32_e64 v201, v226, v246, s[2:3]
	v_cndmask_b32_e64 v202, v247, v227, s[2:3]
	v_cndmask_b32_e64 v203, v227, v247, s[2:3]
	v_cndmask_b32_e64 v204, v248, v210, s[2:3]
	v_cndmask_b32_e64 v205, v210, v248, s[2:3]
	v_cndmask_b32_e64 v236, v249, v211, s[2:3]
	v_cndmask_b32_e64 v237, v211, v249, s[2:3]
	v_add_f32_dpp v212, v200, v201 quad_perm:[2,3,0,1] row_mask:0xf bank_mask:0xf
	v_add_f32_dpp v213, v202, v203 quad_perm:[2,3,0,1] row_mask:0xf bank_mask:0xf
	v_add_f32_dpp v214, v204, v205 quad_perm:[2,3,0,1] row_mask:0xf bank_mask:0xf
	v_add_f32_dpp v215, v236, v237 quad_perm:[2,3,0,1] row_mask:0xf bank_mask:0xf
	v_cndmask_b32_e64 v200, v212, v214, s[0:1]
	v_cndmask_b32_e64 v201, v214, v212, s[0:1]
	v_cndmask_b32_e64 v202, v213, v215, s[0:1]
	v_cndmask_b32_e64 v203, v215, v213, s[0:1]
	s_nop 1
	v_add_f32_dpp v216, v200, v201 quad_perm:[1,0,3,2] row_mask:0xf bank_mask:0xf
	v_add_f32_dpp v217, v202, v203 quad_perm:[1,0,3,2] row_mask:0xf bank_mask:0xf
	s_ashr_i32 s15, s14, 31
	s_lshl_b64 s[14:15], s[14:15], 8
	v_cvt_pk_bf16_f32 v186, v216, v217
	v_lshl_add_u64 v[184:185], v[178:179], 0, s[14:15]
	global_store_dword v[184:185], v186, off
	s_add_u32 s10, s12, 0x100
	s_waitcnt vmcnt(1)
	v_cvt_scalef32_pk_bf16_fp8 v210, v112, 1.0
	v_cvt_scalef32_pk_bf16_fp8 v211, v112, 1.0 op_sel:[1,0,0]
	v_cvt_scalef32_pk_bf16_fp8 v212, v113, 1.0
	v_cvt_scalef32_pk_bf16_fp8 v213, v113, 1.0 op_sel:[1,0,0]
	v_mfma_f32_4x4x4_16b_bf16 v[228:231], v[210:211], v[108:109], 0
	v_cvt_scalef32_pk_bf16_fp8 v214, v114, 1.0
	v_cvt_scalef32_pk_bf16_fp8 v215, v114, 1.0 op_sel:[1,0,0]
	v_mfma_f32_4x4x4_16b_bf16 v[228:231], v[212:213], v[110:111], v[228:231]
	v_cvt_scalef32_pk_bf16_fp8 v216, v115, 1.0
	v_cvt_scalef32_pk_bf16_fp8 v217, v115, 1.0 op_sel:[1,0,0]
	v_mfma_f32_4x4x4_16b_bf16 v[228:231], v[214:215], v[100:101], v[228:231]
	v_cvt_scalef32_pk_bf16_fp8 v218, v116, 1.0
	v_cvt_scalef32_pk_bf16_fp8 v219, v116, 1.0 op_sel:[1,0,0]
	v_mfma_f32_4x4x4_16b_bf16 v[228:231], v[216:217], v[102:103], v[228:231]
	v_cvt_scalef32_pk_bf16_fp8 v220, v117, 1.0
	v_cvt_scalef32_pk_bf16_fp8 v221, v117, 1.0 op_sel:[1,0,0]
	v_mfma_f32_4x4x4_16b_bf16 v[232:235], v[218:219], v[108:109], 0
	v_cvt_scalef32_pk_bf16_fp8 v222, v118, 1.0
	v_cvt_scalef32_pk_bf16_fp8 v223, v118, 1.0 op_sel:[1,0,0]
	v_mfma_f32_4x4x4_16b_bf16 v[232:235], v[220:221], v[110:111], v[232:235]
	v_cvt_scalef32_pk_bf16_fp8 v224, v119, 1.0
	v_cvt_scalef32_pk_bf16_fp8 v225, v119, 1.0 op_sel:[1,0,0]
	v_mfma_f32_4x4x4_16b_bf16 v[232:235], v[222:223], v[100:101], v[232:235]
	v_cvt_scalef32_pk_bf16_fp8 v210, v120, 1.0
	v_cvt_scalef32_pk_bf16_fp8 v211, v120, 1.0 op_sel:[1,0,0]
	v_mfma_f32_4x4x4_16b_bf16 v[232:235], v[224:225], v[102:103], v[232:235]
	v_cvt_scalef32_pk_bf16_fp8 v212, v121, 1.0
	v_cvt_scalef32_pk_bf16_fp8 v213, v121, 1.0 op_sel:[1,0,0]
	v_cndmask_b32_e64 v184, v228, v229, s[22:23]
	v_cndmask_b32_e64 v184, v184, v230, s[24:25]
	v_cndmask_b32_e64 v184, v184, v231, s[26:27]
	v_mfma_f32_4x4x4_16b_bf16 v[228:231], v[210:211], v[108:109], 0
	v_cvt_scalef32_pk_bf16_fp8 v214, v122, 1.0
	v_cvt_scalef32_pk_bf16_fp8 v215, v122, 1.0 op_sel:[1,0,0]
	v_mfma_f32_4x4x4_16b_bf16 v[228:231], v[212:213], v[110:111], v[228:231]
	v_cvt_scalef32_pk_bf16_fp8 v216, v123, 1.0
	v_cvt_scalef32_pk_bf16_fp8 v217, v123, 1.0 op_sel:[1,0,0]
	v_mfma_f32_4x4x4_16b_bf16 v[228:231], v[214:215], v[100:101], v[228:231]
	v_cvt_scalef32_pk_bf16_fp8 v218, v124, 1.0
	v_cvt_scalef32_pk_bf16_fp8 v219, v124, 1.0 op_sel:[1,0,0]
	v_mfma_f32_4x4x4_16b_bf16 v[228:231], v[216:217], v[102:103], v[228:231]
	v_cvt_scalef32_pk_bf16_fp8 v220, v125, 1.0
	v_cvt_scalef32_pk_bf16_fp8 v221, v125, 1.0 op_sel:[1,0,0]
	v_cndmask_b32_e64 v185, v232, v233, s[22:23]
	v_cndmask_b32_e64 v185, v185, v234, s[24:25]
	v_cndmask_b32_e64 v185, v185, v235, s[26:27]
	v_mfma_f32_4x4x4_16b_bf16 v[232:235], v[218:219], v[108:109], 0
	v_cvt_scalef32_pk_bf16_fp8 v222, v126, 1.0
	v_cvt_scalef32_pk_bf16_fp8 v223, v126, 1.0 op_sel:[1,0,0]
	v_mfma_f32_4x4x4_16b_bf16 v[232:235], v[220:221], v[110:111], v[232:235]
	v_cvt_scalef32_pk_bf16_fp8 v224, v127, 1.0
	v_cvt_scalef32_pk_bf16_fp8 v225, v127, 1.0 op_sel:[1,0,0]
	v_mfma_f32_4x4x4_16b_bf16 v[232:235], v[222:223], v[100:101], v[232:235]
	v_cvt_scalef32_pk_bf16_fp8 v210, v128, 1.0
	v_cvt_scalef32_pk_bf16_fp8 v211, v128, 1.0 op_sel:[1,0,0]
	v_mfma_f32_4x4x4_16b_bf16 v[232:235], v[224:225], v[102:103], v[232:235]
	v_cvt_scalef32_pk_bf16_fp8 v212, v129, 1.0
	v_cvt_scalef32_pk_bf16_fp8 v213, v129, 1.0 op_sel:[1,0,0]
	v_cndmask_b32_e64 v186, v228, v229, s[22:23]
	v_cndmask_b32_e64 v186, v186, v230, s[24:25]
	v_cndmask_b32_e64 v186, v186, v231, s[26:27]
	v_mfma_f32_4x4x4_16b_bf16 v[228:231], v[210:211], v[108:109], 0
	v_cvt_scalef32_pk_bf16_fp8 v214, v130, 1.0
	v_cvt_scalef32_pk_bf16_fp8 v215, v130, 1.0 op_sel:[1,0,0]
	v_mfma_f32_4x4x4_16b_bf16 v[228:231], v[212:213], v[110:111], v[228:231]
	v_cvt_scalef32_pk_bf16_fp8 v216, v131, 1.0
	v_cvt_scalef32_pk_bf16_fp8 v217, v131, 1.0 op_sel:[1,0,0]
	v_mfma_f32_4x4x4_16b_bf16 v[228:231], v[214:215], v[100:101], v[228:231]
	v_cvt_scalef32_pk_bf16_fp8 v218, v132, 1.0
	v_cvt_scalef32_pk_bf16_fp8 v219, v132, 1.0 op_sel:[1,0,0]
	v_mfma_f32_4x4x4_16b_bf16 v[228:231], v[216:217], v[102:103], v[228:231]
	v_cvt_scalef32_pk_bf16_fp8 v220, v133, 1.0
	v_cvt_scalef32_pk_bf16_fp8 v221, v133, 1.0 op_sel:[1,0,0]
	v_cndmask_b32_e64 v187, v232, v233, s[22:23]
	v_cndmask_b32_e64 v187, v187, v234, s[24:25]
	v_cndmask_b32_e64 v187, v187, v235, s[26:27]
	v_mfma_f32_4x4x4_16b_bf16 v[232:235], v[218:219], v[108:109], 0
	v_cvt_scalef32_pk_bf16_fp8 v222, v134, 1.0
	v_cvt_scalef32_pk_bf16_fp8 v223, v134, 1.0 op_sel:[1,0,0]
	v_mfma_f32_4x4x4_16b_bf16 v[232:235], v[220:221], v[110:111], v[232:235]
	v_cvt_scalef32_pk_bf16_fp8 v224, v135, 1.0
	v_cvt_scalef32_pk_bf16_fp8 v225, v135, 1.0 op_sel:[1,0,0]
	v_mfma_f32_4x4x4_16b_bf16 v[232:235], v[222:223], v[100:101], v[232:235]
	v_cvt_scalef32_pk_bf16_fp8 v210, v136, 1.0
	v_cvt_scalef32_pk_bf16_fp8 v211, v136, 1.0 op_sel:[1,0,0]
	v_mfma_f32_4x4x4_16b_bf16 v[232:235], v[224:225], v[102:103], v[232:235]
	v_cvt_scalef32_pk_bf16_fp8 v212, v137, 1.0
	v_cvt_scalef32_pk_bf16_fp8 v213, v137, 1.0 op_sel:[1,0,0]
	v_cndmask_b32_e64 v188, v228, v229, s[22:23]
	v_cndmask_b32_e64 v188, v188, v230, s[24:25]
	v_cndmask_b32_e64 v188, v188, v231, s[26:27]
	v_mfma_f32_4x4x4_16b_bf16 v[228:231], v[210:211], v[108:109], 0
	v_cvt_scalef32_pk_bf16_fp8 v214, v138, 1.0
	v_cvt_scalef32_pk_bf16_fp8 v215, v138, 1.0 op_sel:[1,0,0]
	v_mfma_f32_4x4x4_16b_bf16 v[228:231], v[212:213], v[110:111], v[228:231]
	v_cvt_scalef32_pk_bf16_fp8 v216, v139, 1.0
	v_cvt_scalef32_pk_bf16_fp8 v217, v139, 1.0 op_sel:[1,0,0]
	v_mfma_f32_4x4x4_16b_bf16 v[228:231], v[214:215], v[100:101], v[228:231]
	v_cvt_scalef32_pk_bf16_fp8 v218, v140, 1.0
	v_cvt_scalef32_pk_bf16_fp8 v219, v140, 1.0 op_sel:[1,0,0]
	v_mfma_f32_4x4x4_16b_bf16 v[228:231], v[216:217], v[102:103], v[228:231]
	v_cvt_scalef32_pk_bf16_fp8 v220, v141, 1.0
	v_cvt_scalef32_pk_bf16_fp8 v221, v141, 1.0 op_sel:[1,0,0]
	v_cndmask_b32_e64 v189, v232, v233, s[22:23]
	v_cndmask_b32_e64 v189, v189, v234, s[24:25]
	v_cndmask_b32_e64 v189, v189, v235, s[26:27]
	v_mfma_f32_4x4x4_16b_bf16 v[232:235], v[218:219], v[108:109], 0
	v_cvt_scalef32_pk_bf16_fp8 v222, v142, 1.0
	v_cvt_scalef32_pk_bf16_fp8 v223, v142, 1.0 op_sel:[1,0,0]
	v_mfma_f32_4x4x4_16b_bf16 v[232:235], v[220:221], v[110:111], v[232:235]
	v_cvt_scalef32_pk_bf16_fp8 v224, v143, 1.0
	v_cvt_scalef32_pk_bf16_fp8 v225, v143, 1.0 op_sel:[1,0,0]
	v_mfma_f32_4x4x4_16b_bf16 v[232:235], v[222:223], v[100:101], v[232:235]
	v_cvt_scalef32_pk_bf16_fp8 v210, v144, 1.0
	v_cvt_scalef32_pk_bf16_fp8 v211, v144, 1.0 op_sel:[1,0,0]
	v_mfma_f32_4x4x4_16b_bf16 v[232:235], v[224:225], v[102:103], v[232:235]
	v_cvt_scalef32_pk_bf16_fp8 v212, v145, 1.0
	v_cvt_scalef32_pk_bf16_fp8 v213, v145, 1.0 op_sel:[1,0,0]
	v_cndmask_b32_e64 v190, v228, v229, s[22:23]
	v_cndmask_b32_e64 v190, v190, v230, s[24:25]
	v_cndmask_b32_e64 v190, v190, v231, s[26:27]
	v_mfma_f32_4x4x4_16b_bf16 v[228:231], v[210:211], v[108:109], 0
	v_cvt_scalef32_pk_bf16_fp8 v214, v146, 1.0
	v_cvt_scalef32_pk_bf16_fp8 v215, v146, 1.0 op_sel:[1,0,0]
	v_mfma_f32_4x4x4_16b_bf16 v[228:231], v[212:213], v[110:111], v[228:231]
	v_cvt_scalef32_pk_bf16_fp8 v216, v147, 1.0
	v_cvt_scalef32_pk_bf16_fp8 v217, v147, 1.0 op_sel:[1,0,0]
	v_mfma_f32_4x4x4_16b_bf16 v[228:231], v[214:215], v[100:101], v[228:231]
	v_cvt_scalef32_pk_bf16_fp8 v218, v148, 1.0
	v_cvt_scalef32_pk_bf16_fp8 v219, v148, 1.0 op_sel:[1,0,0]
	v_mfma_f32_4x4x4_16b_bf16 v[228:231], v[216:217], v[102:103], v[228:231]
	v_cvt_scalef32_pk_bf16_fp8 v220, v149, 1.0
	v_cvt_scalef32_pk_bf16_fp8 v221, v149, 1.0 op_sel:[1,0,0]
	v_cndmask_b32_e64 v191, v232, v233, s[22:23]
	v_cndmask_b32_e64 v191, v191, v234, s[24:25]
	v_cndmask_b32_e64 v191, v191, v235, s[26:27]
	v_mfma_f32_4x4x4_16b_bf16 v[232:235], v[218:219], v[108:109], 0
	v_cvt_scalef32_pk_bf16_fp8 v222, v150, 1.0
	v_cvt_scalef32_pk_bf16_fp8 v223, v150, 1.0 op_sel:[1,0,0]
	v_mfma_f32_4x4x4_16b_bf16 v[232:235], v[220:221], v[110:111], v[232:235]
	v_cvt_scalef32_pk_bf16_fp8 v224, v151, 1.0
	v_cvt_scalef32_pk_bf16_fp8 v225, v151, 1.0 op_sel:[1,0,0]
	v_mfma_f32_4x4x4_16b_bf16 v[232:235], v[222:223], v[100:101], v[232:235]
	v_cvt_scalef32_pk_bf16_fp8 v210, v152, 1.0
	v_cvt_scalef32_pk_bf16_fp8 v211, v152, 1.0 op_sel:[1,0,0]
	v_mfma_f32_4x4x4_16b_bf16 v[232:235], v[224:225], v[102:103], v[232:235]
	v_cvt_scalef32_pk_bf16_fp8 v212, v153, 1.0
	v_cvt_scalef32_pk_bf16_fp8 v213, v153, 1.0 op_sel:[1,0,0]
	v_cndmask_b32_e64 v192, v228, v229, s[22:23]
	v_cndmask_b32_e64 v192, v192, v230, s[24:25]
	v_cndmask_b32_e64 v192, v192, v231, s[26:27]
	v_mfma_f32_4x4x4_16b_bf16 v[228:231], v[210:211], v[108:109], 0
	v_cvt_scalef32_pk_bf16_fp8 v214, v154, 1.0
	v_cvt_scalef32_pk_bf16_fp8 v215, v154, 1.0 op_sel:[1,0,0]
	v_mfma_f32_4x4x4_16b_bf16 v[228:231], v[212:213], v[110:111], v[228:231]
	v_cvt_scalef32_pk_bf16_fp8 v216, v155, 1.0
	v_cvt_scalef32_pk_bf16_fp8 v217, v155, 1.0 op_sel:[1,0,0]
	v_mfma_f32_4x4x4_16b_bf16 v[228:231], v[214:215], v[100:101], v[228:231]
	v_cvt_scalef32_pk_bf16_fp8 v218, v156, 1.0
	v_cvt_scalef32_pk_bf16_fp8 v219, v156, 1.0 op_sel:[1,0,0]
	v_mfma_f32_4x4x4_16b_bf16 v[228:231], v[216:217], v[102:103], v[228:231]
	v_cvt_scalef32_pk_bf16_fp8 v220, v157, 1.0
	v_cvt_scalef32_pk_bf16_fp8 v221, v157, 1.0 op_sel:[1,0,0]
	v_cndmask_b32_e64 v193, v232, v233, s[22:23]
	v_cndmask_b32_e64 v193, v193, v234, s[24:25]
	v_cndmask_b32_e64 v193, v193, v235, s[26:27]
	v_mfma_f32_4x4x4_16b_bf16 v[232:235], v[218:219], v[108:109], 0
	v_cvt_scalef32_pk_bf16_fp8 v222, v158, 1.0
	v_cvt_scalef32_pk_bf16_fp8 v223, v158, 1.0 op_sel:[1,0,0]
	v_mfma_f32_4x4x4_16b_bf16 v[232:235], v[220:221], v[110:111], v[232:235]
	v_cvt_scalef32_pk_bf16_fp8 v224, v159, 1.0
	v_cvt_scalef32_pk_bf16_fp8 v225, v159, 1.0 op_sel:[1,0,0]
	v_mfma_f32_4x4x4_16b_bf16 v[232:235], v[222:223], v[100:101], v[232:235]
	v_cvt_scalef32_pk_bf16_fp8 v210, v160, 1.0
	v_cvt_scalef32_pk_bf16_fp8 v211, v160, 1.0 op_sel:[1,0,0]
	v_mfma_f32_4x4x4_16b_bf16 v[232:235], v[224:225], v[102:103], v[232:235]
	v_cvt_scalef32_pk_bf16_fp8 v212, v161, 1.0
	v_cvt_scalef32_pk_bf16_fp8 v213, v161, 1.0 op_sel:[1,0,0]
	v_cndmask_b32_e64 v194, v228, v229, s[22:23]
	v_cndmask_b32_e64 v194, v194, v230, s[24:25]
	v_cndmask_b32_e64 v194, v194, v231, s[26:27]
	v_mfma_f32_4x4x4_16b_bf16 v[228:231], v[210:211], v[108:109], 0
	v_cvt_scalef32_pk_bf16_fp8 v214, v162, 1.0
	v_cvt_scalef32_pk_bf16_fp8 v215, v162, 1.0 op_sel:[1,0,0]
	v_mfma_f32_4x4x4_16b_bf16 v[228:231], v[212:213], v[110:111], v[228:231]
	v_cvt_scalef32_pk_bf16_fp8 v216, v163, 1.0
	v_cvt_scalef32_pk_bf16_fp8 v217, v163, 1.0 op_sel:[1,0,0]
	v_mfma_f32_4x4x4_16b_bf16 v[228:231], v[214:215], v[100:101], v[228:231]
	v_cvt_scalef32_pk_bf16_fp8 v218, v164, 1.0
	v_cvt_scalef32_pk_bf16_fp8 v219, v164, 1.0 op_sel:[1,0,0]
	v_mfma_f32_4x4x4_16b_bf16 v[228:231], v[216:217], v[102:103], v[228:231]
	v_cvt_scalef32_pk_bf16_fp8 v220, v165, 1.0
	v_cvt_scalef32_pk_bf16_fp8 v221, v165, 1.0 op_sel:[1,0,0]
	v_cndmask_b32_e64 v195, v232, v233, s[22:23]
	v_cndmask_b32_e64 v195, v195, v234, s[24:25]
	v_cndmask_b32_e64 v195, v195, v235, s[26:27]
	v_mfma_f32_4x4x4_16b_bf16 v[232:235], v[218:219], v[108:109], 0
	v_cvt_scalef32_pk_bf16_fp8 v222, v166, 1.0
	v_cvt_scalef32_pk_bf16_fp8 v223, v166, 1.0 op_sel:[1,0,0]
	v_mfma_f32_4x4x4_16b_bf16 v[232:235], v[220:221], v[110:111], v[232:235]
	v_cvt_scalef32_pk_bf16_fp8 v224, v167, 1.0
	v_cvt_scalef32_pk_bf16_fp8 v225, v167, 1.0 op_sel:[1,0,0]
	v_mfma_f32_4x4x4_16b_bf16 v[232:235], v[222:223], v[100:101], v[232:235]
	v_cvt_scalef32_pk_bf16_fp8 v210, v168, 1.0
	v_cvt_scalef32_pk_bf16_fp8 v211, v168, 1.0 op_sel:[1,0,0]
	v_mfma_f32_4x4x4_16b_bf16 v[232:235], v[224:225], v[102:103], v[232:235]
	v_cvt_scalef32_pk_bf16_fp8 v212, v169, 1.0
	v_cvt_scalef32_pk_bf16_fp8 v213, v169, 1.0 op_sel:[1,0,0]
	v_cndmask_b32_e64 v196, v228, v229, s[22:23]
	v_cndmask_b32_e64 v196, v196, v230, s[24:25]
	v_cndmask_b32_e64 v196, v196, v231, s[26:27]
	v_mfma_f32_4x4x4_16b_bf16 v[228:231], v[210:211], v[108:109], 0
	v_cvt_scalef32_pk_bf16_fp8 v214, v170, 1.0
	v_cvt_scalef32_pk_bf16_fp8 v215, v170, 1.0 op_sel:[1,0,0]
	v_mfma_f32_4x4x4_16b_bf16 v[228:231], v[212:213], v[110:111], v[228:231]
	v_cvt_scalef32_pk_bf16_fp8 v216, v171, 1.0
	v_cvt_scalef32_pk_bf16_fp8 v217, v171, 1.0 op_sel:[1,0,0]
	v_mfma_f32_4x4x4_16b_bf16 v[228:231], v[214:215], v[100:101], v[228:231]
	v_cvt_scalef32_pk_bf16_fp8 v218, v172, 1.0
	v_cvt_scalef32_pk_bf16_fp8 v219, v172, 1.0 op_sel:[1,0,0]
	v_mfma_f32_4x4x4_16b_bf16 v[228:231], v[216:217], v[102:103], v[228:231]
	v_cvt_scalef32_pk_bf16_fp8 v220, v173, 1.0
	v_cvt_scalef32_pk_bf16_fp8 v221, v173, 1.0 op_sel:[1,0,0]
	v_cndmask_b32_e64 v197, v232, v233, s[22:23]
	v_cndmask_b32_e64 v197, v197, v234, s[24:25]
	v_cndmask_b32_e64 v197, v197, v235, s[26:27]
	v_mfma_f32_4x4x4_16b_bf16 v[232:235], v[218:219], v[108:109], 0
	v_cvt_scalef32_pk_bf16_fp8 v222, v174, 1.0
	v_cvt_scalef32_pk_bf16_fp8 v223, v174, 1.0 op_sel:[1,0,0]
	v_mfma_f32_4x4x4_16b_bf16 v[232:235], v[220:221], v[110:111], v[232:235]
	v_cvt_scalef32_pk_bf16_fp8 v224, v175, 1.0
	v_cvt_scalef32_pk_bf16_fp8 v225, v175, 1.0 op_sel:[1,0,0]
	v_mfma_f32_4x4x4_16b_bf16 v[232:235], v[222:223], v[100:101], v[232:235]
	s_nop 1
	v_mfma_f32_4x4x4_16b_bf16 v[232:235], v[224:225], v[102:103], v[232:235]
	v_cndmask_b32_e64 v198, v228, v229, s[22:23]
	v_cndmask_b32_e64 v198, v198, v230, s[24:25]
	v_cndmask_b32_e64 v198, v198, v231, s[26:27]
	s_nop 4
	v_cndmask_b32_e64 v199, v232, v233, s[22:23]
	v_cndmask_b32_e64 v199, v199, v234, s[24:25]
	v_cndmask_b32_e64 v199, v199, v235, s[26:27]
	v_cndmask_b32_e64 v200, v184, v192, s[4:5]
	v_cndmask_b32_e64 v201, v192, v184, s[4:5]
	v_cndmask_b32_e64 v202, v185, v193, s[4:5]
	v_cndmask_b32_e64 v203, v193, v185, s[4:5]
	v_cndmask_b32_e64 v204, v186, v194, s[4:5]
	v_cndmask_b32_e64 v205, v194, v186, s[4:5]
	v_cndmask_b32_e64 v236, v187, v195, s[4:5]
	v_cndmask_b32_e64 v237, v195, v187, s[4:5]
	v_cndmask_b32_e64 v238, v188, v196, s[4:5]
	v_cndmask_b32_e64 v239, v196, v188, s[4:5]
	v_cndmask_b32_e64 v240, v189, v197, s[4:5]
	v_cndmask_b32_e64 v241, v197, v189, s[4:5]
	v_cndmask_b32_e64 v242, v190, v198, s[4:5]
	v_cndmask_b32_e64 v243, v198, v190, s[4:5]
	v_cndmask_b32_e64 v244, v191, v199, s[4:5]
	v_cndmask_b32_e64 v245, v199, v191, s[4:5]
	v_add_f32_dpp v246, v200, v201 row_half_mirror row_mask:0xf bank_mask:0xf
	v_add_f32_dpp v247, v202, v203 row_half_mirror row_mask:0xf bank_mask:0xf
	v_add_f32_dpp v248, v204, v205 row_half_mirror row_mask:0xf bank_mask:0xf
	v_add_f32_dpp v249, v236, v237 row_half_mirror row_mask:0xf bank_mask:0xf
	v_add_f32_dpp v226, v238, v239 row_half_mirror row_mask:0xf bank_mask:0xf
	v_add_f32_dpp v227, v240, v241 row_half_mirror row_mask:0xf bank_mask:0xf
	v_add_f32_dpp v210, v242, v243 row_half_mirror row_mask:0xf bank_mask:0xf
	v_add_f32_dpp v211, v244, v245 row_half_mirror row_mask:0xf bank_mask:0xf
	v_cndmask_b32_e64 v200, v246, v226, s[2:3]
	v_cndmask_b32_e64 v201, v226, v246, s[2:3]
	v_cndmask_b32_e64 v202, v247, v227, s[2:3]
	v_cndmask_b32_e64 v203, v227, v247, s[2:3]
	v_cndmask_b32_e64 v204, v248, v210, s[2:3]
	v_cndmask_b32_e64 v205, v210, v248, s[2:3]
	v_cndmask_b32_e64 v236, v249, v211, s[2:3]
	v_cndmask_b32_e64 v237, v211, v249, s[2:3]
	v_add_f32_dpp v212, v200, v201 quad_perm:[2,3,0,1] row_mask:0xf bank_mask:0xf
	v_add_f32_dpp v213, v202, v203 quad_perm:[2,3,0,1] row_mask:0xf bank_mask:0xf
	v_add_f32_dpp v214, v204, v205 quad_perm:[2,3,0,1] row_mask:0xf bank_mask:0xf
	v_add_f32_dpp v215, v236, v237 quad_perm:[2,3,0,1] row_mask:0xf bank_mask:0xf
	v_cndmask_b32_e64 v200, v212, v214, s[0:1]
	v_cndmask_b32_e64 v201, v214, v212, s[0:1]
	v_cndmask_b32_e64 v202, v213, v215, s[0:1]
	v_cndmask_b32_e64 v203, v215, v213, s[0:1]
	s_nop 1
	v_add_f32_dpp v216, v200, v201 quad_perm:[1,0,3,2] row_mask:0xf bank_mask:0xf
	v_add_f32_dpp v217, v202, v203 quad_perm:[1,0,3,2] row_mask:0xf bank_mask:0xf
	s_ashr_i32 s11, s10, 31
	s_lshl_b64 s[10:11], s[10:11], 8
	v_cvt_pk_bf16_f32 v186, v216, v217
	v_lshl_add_u64 v[184:185], v[178:179], 0, s[10:11]
	global_store_dword v[184:185], v186, off
